# P0: silu-table build requests its 18 inputs at once (one round trip instead of 18)
# speedup vs baseline: 1.0037x; 1.0037x over previous
; __device__ __forceinline__ float sigmoidf_(float x) { return frcp_(1.0f + fexp_(-x)); }
; __device__ __forceinline__ void p0_prologue(const Args& a, const Frame& F) {
;     ...
;         __syncthreads();
;         for (int i = F.tid; i < 9 * 1024; i += 512) { const int r = i >> 10, k = i & 1023; const float v = (r < 8) ? a.in[IN_C][r * 1024 + k] : a.in[IN_CCTX][k]; sc[i] = v * sigmoidf_(v); }
;         __syncthreads();
;         const int col = 64 * item + F.lane, k0 = F.wave * 128; const float* W = a.in[IN_WADA] + col;
;         float acc[9];
; #pragma unroll
;         for (int q = 0; q < 9; ++q) acc[q] = 0.f;
;         for (int kk = 0; kk < 128; kk += 8) {
;             float wv[8];
; #pragma unroll
;             for (int u = 0; u < 8; ++u) wv[u] = W[(size_t)(k0 + kk + u) * 6144];
.LBB0_11:
	s_mov_b64 s[14:15], 0
	v_mov_b32_e32 v7, v1
	v_mov_b64_e32 v[8:9], v[4:5]
	v_mov_b32_e32 v10, v0
	s_barrier
	global_load_dword v100, v[8:9], off
	v_lshl_add_u64 v[8:9], v[8:9], 0, s[10:11]
	global_load_dword v101, v[8:9], off
	v_lshl_add_u64 v[8:9], v[8:9], 0, s[10:11]
	global_load_dword v102, v[8:9], off
	v_lshl_add_u64 v[8:9], v[8:9], 0, s[10:11]
	global_load_dword v103, v[8:9], off
	v_lshl_add_u64 v[8:9], v[8:9], 0, s[10:11]
	global_load_dword v104, v[8:9], off
	v_lshl_add_u64 v[8:9], v[8:9], 0, s[10:11]
	global_load_dword v105, v[8:9], off
	v_lshl_add_u64 v[8:9], v[8:9], 0, s[10:11]
	global_load_dword v106, v[8:9], off
	v_lshl_add_u64 v[8:9], v[8:9], 0, s[10:11]
	global_load_dword v107, v[8:9], off
	v_lshl_add_u64 v[8:9], v[8:9], 0, s[10:11]
	global_load_dword v108, v[8:9], off
	v_lshl_add_u64 v[8:9], v[8:9], 0, s[10:11]
	global_load_dword v109, v[8:9], off
	v_lshl_add_u64 v[8:9], v[8:9], 0, s[10:11]
	global_load_dword v110, v[8:9], off
	v_lshl_add_u64 v[8:9], v[8:9], 0, s[10:11]
	global_load_dword v111, v[8:9], off
	v_lshl_add_u64 v[8:9], v[8:9], 0, s[10:11]
	global_load_dword v112, v[8:9], off
	v_lshl_add_u64 v[8:9], v[8:9], 0, s[10:11]
	global_load_dword v113, v[8:9], off
	v_lshl_add_u64 v[8:9], v[8:9], 0, s[10:11]
	global_load_dword v114, v[8:9], off
	v_lshl_add_u64 v[8:9], v[8:9], 0, s[10:11]
	global_load_dword v115, v[8:9], off
	v_lshlrev_b32_e32 v2, 2, v0
	v_lshl_add_u64 v[12:13], s[42:43], 0, v[2:3]
	global_load_dword v116, v[12:13], off
	global_load_dword v117, v[12:13], off offset:2048
	s_waitcnt vmcnt(0)
	v_mul_f32_e32 v12, 0xbfb8aa3b, v100
	v_exp_f32_e32 v12, v12
	s_nop 0
	v_add_f32_e32 v10, 1.0, v12
	v_rcp_f32_e32 v12, v10
	s_nop 0
	v_mul_f32_e32 v2, v100, v12
	ds_write_b32 v7, v2
	v_mul_f32_e32 v12, 0xbfb8aa3b, v101
	v_exp_f32_e32 v12, v12
	s_nop 0
	v_add_f32_e32 v10, 1.0, v12
	v_rcp_f32_e32 v12, v10
	s_nop 0
	v_mul_f32_e32 v2, v101, v12
	ds_write_b32 v7, v2 offset:2048
	v_mul_f32_e32 v12, 0xbfb8aa3b, v102
	v_exp_f32_e32 v12, v12
	s_nop 0
	v_add_f32_e32 v10, 1.0, v12
	v_rcp_f32_e32 v12, v10
	s_nop 0
	v_mul_f32_e32 v2, v102, v12
	ds_write_b32 v7, v2 offset:4096
	v_mul_f32_e32 v12, 0xbfb8aa3b, v103
	v_exp_f32_e32 v12, v12
	s_nop 0
	v_add_f32_e32 v10, 1.0, v12
	v_rcp_f32_e32 v12, v10
	s_nop 0
	v_mul_f32_e32 v2, v103, v12
	ds_write_b32 v7, v2 offset:6144
	v_mul_f32_e32 v12, 0xbfb8aa3b, v104
	v_exp_f32_e32 v12, v12
	s_nop 0
	v_add_f32_e32 v10, 1.0, v12
	v_rcp_f32_e32 v12, v10
	s_nop 0
	v_mul_f32_e32 v2, v104, v12
	ds_write_b32 v7, v2 offset:8192
	v_mul_f32_e32 v12, 0xbfb8aa3b, v105
	v_exp_f32_e32 v12, v12
	s_nop 0
	v_add_f32_e32 v10, 1.0, v12
	v_rcp_f32_e32 v12, v10
	s_nop 0
	v_mul_f32_e32 v2, v105, v12
	ds_write_b32 v7, v2 offset:10240
	v_mul_f32_e32 v12, 0xbfb8aa3b, v106
	v_exp_f32_e32 v12, v12
	s_nop 0
	v_add_f32_e32 v10, 1.0, v12
	v_rcp_f32_e32 v12, v10
	s_nop 0
	v_mul_f32_e32 v2, v106, v12
	ds_write_b32 v7, v2 offset:12288
	v_mul_f32_e32 v12, 0xbfb8aa3b, v107
	v_exp_f32_e32 v12, v12
	s_nop 0
	v_add_f32_e32 v10, 1.0, v12
	v_rcp_f32_e32 v12, v10
	s_nop 0
	v_mul_f32_e32 v2, v107, v12
	ds_write_b32 v7, v2 offset:14336
	v_mul_f32_e32 v12, 0xbfb8aa3b, v108
	v_exp_f32_e32 v12, v12
	s_nop 0
	v_add_f32_e32 v10, 1.0, v12
	v_rcp_f32_e32 v12, v10
	s_nop 0
	v_mul_f32_e32 v2, v108, v12
	ds_write_b32 v7, v2 offset:16384
	v_mul_f32_e32 v12, 0xbfb8aa3b, v109
	v_exp_f32_e32 v12, v12
	s_nop 0
	v_add_f32_e32 v10, 1.0, v12
	v_rcp_f32_e32 v12, v10
	s_nop 0
	v_mul_f32_e32 v2, v109, v12
	ds_write_b32 v7, v2 offset:18432
	v_mul_f32_e32 v12, 0xbfb8aa3b, v110
	v_exp_f32_e32 v12, v12
	s_nop 0
	v_add_f32_e32 v10, 1.0, v12
	v_rcp_f32_e32 v12, v10
	s_nop 0
	v_mul_f32_e32 v2, v110, v12
	ds_write_b32 v7, v2 offset:20480
	v_mul_f32_e32 v12, 0xbfb8aa3b, v111
	v_exp_f32_e32 v12, v12
	s_nop 0
	v_add_f32_e32 v10, 1.0, v12
	v_rcp_f32_e32 v12, v10
	s_nop 0
	v_mul_f32_e32 v2, v111, v12
	ds_write_b32 v7, v2 offset:22528
	v_mul_f32_e32 v12, 0xbfb8aa3b, v112
	v_exp_f32_e32 v12, v12
	s_nop 0
	v_add_f32_e32 v10, 1.0, v12
	v_rcp_f32_e32 v12, v10
	s_nop 0
	v_mul_f32_e32 v2, v112, v12
	ds_write_b32 v7, v2 offset:24576
	v_mul_f32_e32 v12, 0xbfb8aa3b, v113
	v_exp_f32_e32 v12, v12
	s_nop 0
	v_add_f32_e32 v10, 1.0, v12
	v_rcp_f32_e32 v12, v10
	s_nop 0
	v_mul_f32_e32 v2, v113, v12
	ds_write_b32 v7, v2 offset:26624
	v_mul_f32_e32 v12, 0xbfb8aa3b, v114
	v_exp_f32_e32 v12, v12
	s_nop 0
	v_add_f32_e32 v10, 1.0, v12
	v_rcp_f32_e32 v12, v10
	s_nop 0
	v_mul_f32_e32 v2, v114, v12
	ds_write_b32 v7, v2 offset:28672
	v_mul_f32_e32 v12, 0xbfb8aa3b, v115
	v_exp_f32_e32 v12, v12
	s_nop 0
	v_add_f32_e32 v10, 1.0, v12
	v_rcp_f32_e32 v12, v10
	s_nop 0
	v_mul_f32_e32 v2, v115, v12
	ds_write_b32 v7, v2 offset:30720
	v_mul_f32_e32 v12, 0xbfb8aa3b, v116
	v_exp_f32_e32 v12, v12
	s_nop 0
	v_add_f32_e32 v10, 1.0, v12
	v_rcp_f32_e32 v12, v10
	s_nop 0
	v_mul_f32_e32 v2, v116, v12
	ds_write_b32 v7, v2 offset:32768
	v_mul_f32_e32 v12, 0xbfb8aa3b, v117
	v_exp_f32_e32 v12, v12
	s_nop 0
	v_add_f32_e32 v10, 1.0, v12
	v_rcp_f32_e32 v12, v10
	s_nop 0
	v_mul_f32_e32 v2, v117, v12
	ds_write_b32 v7, v2 offset:34816
	s_or_b64 exec, exec, s[14:15]
	v_ashrrev_i32_e32 v7, 31, v6
	v_mov_b32_e32 v10, 0
	v_lshl_add_u64 v[8:9], v[6:7], 2, s[8:9]
	v_mov_b64_e32 v[248:249], v[8:9]
	s_mov_b64 s[98:99], 0x6000
	global_load_dword v120, v[248:249], off
	v_lshl_add_u64 v[248:249], v[248:249], 0, s[98:99]
	global_load_dword v121, v[248:249], off
	v_lshl_add_u64 v[248:249], v[248:249], 0, s[98:99]
	global_load_dword v122, v[248:249], off
	v_lshl_add_u64 v[248:249], v[248:249], 0, s[98:99]
	global_load_dword v123, v[248:249], off
	v_lshl_add_u64 v[248:249], v[248:249], 0, s[98:99]
	global_load_dword v124, v[248:249], off
; __device__ __forceinline__ void p0_prologue(const Args& a, const Frame& F) {
;     ...
;         for (int kk = 0; kk < 128; kk += 8) {
;             float wv[8];
; #pragma unroll
;             for (int u = 0; u < 8; ++u) wv[u] = W[(size_t)(k0 + kk + u) * 6144];
	v_lshl_add_u64 v[248:249], v[248:249], 0, s[98:99]
	global_load_dword v125, v[248:249], off
	v_lshl_add_u64 v[248:249], v[248:249], 0, s[98:99]
	global_load_dword v126, v[248:249], off
	v_lshl_add_u64 v[248:249], v[248:249], 0, s[98:99]
	global_load_dword v127, v[248:249], off
	v_lshl_add_u64 v[248:249], v[248:249], 0, s[98:99]
	global_load_dword v128, v[248:249], off
	v_lshl_add_u64 v[248:249], v[248:249], 0, s[98:99]
	global_load_dword v129, v[248:249], off
	v_lshl_add_u64 v[248:249], v[248:249], 0, s[98:99]
	global_load_dword v130, v[248:249], off
	v_lshl_add_u64 v[248:249], v[248:249], 0, s[98:99]
	global_load_dword v131, v[248:249], off
	v_lshl_add_u64 v[248:249], v[248:249], 0, s[98:99]
	global_load_dword v132, v[248:249], off
	v_lshl_add_u64 v[248:249], v[248:249], 0, s[98:99]
	global_load_dword v133, v[248:249], off
	v_lshl_add_u64 v[248:249], v[248:249], 0, s[98:99]
	global_load_dword v134, v[248:249], off
	v_lshl_add_u64 v[248:249], v[248:249], 0, s[98:99]
	global_load_dword v135, v[248:249], off
	v_lshl_add_u64 v[248:249], v[248:249], 0, s[98:99]
	global_load_dword v136, v[248:249], off
	v_lshl_add_u64 v[248:249], v[248:249], 0, s[98:99]
	global_load_dword v137, v[248:249], off
	v_lshl_add_u64 v[248:249], v[248:249], 0, s[98:99]
	global_load_dword v138, v[248:249], off
	v_lshl_add_u64 v[248:249], v[248:249], 0, s[98:99]
	global_load_dword v139, v[248:249], off
	v_lshl_add_u64 v[248:249], v[248:249], 0, s[98:99]
	global_load_dword v140, v[248:249], off
	v_lshl_add_u64 v[248:249], v[248:249], 0, s[98:99]
	global_load_dword v141, v[248:249], off
	v_lshl_add_u64 v[248:249], v[248:249], 0, s[98:99]
	global_load_dword v142, v[248:249], off
	v_lshl_add_u64 v[248:249], v[248:249], 0, s[98:99]
	global_load_dword v143, v[248:249], off
	v_lshl_add_u64 v[248:249], v[248:249], 0, s[98:99]
	global_load_dword v144, v[248:249], off
	v_lshl_add_u64 v[248:249], v[248:249], 0, s[98:99]
	global_load_dword v145, v[248:249], off
	v_lshl_add_u64 v[248:249], v[248:249], 0, s[98:99]
	global_load_dword v146, v[248:249], off
	v_lshl_add_u64 v[248:249], v[248:249], 0, s[98:99]
	global_load_dword v147, v[248:249], off
	v_lshl_add_u64 v[248:249], v[248:249], 0, s[98:99]
	global_load_dword v148, v[248:249], off
	v_lshl_add_u64 v[248:249], v[248:249], 0, s[98:99]
	global_load_dword v149, v[248:249], off
	v_lshl_add_u64 v[248:249], v[248:249], 0, s[98:99]
	global_load_dword v150, v[248:249], off
	v_lshl_add_u64 v[248:249], v[248:249], 0, s[98:99]
	global_load_dword v151, v[248:249], off
	v_lshl_add_u64 v[248:249], v[248:249], 0, s[98:99]
	global_load_dword v152, v[248:249], off
	v_lshl_add_u64 v[248:249], v[248:249], 0, s[98:99]
	global_load_dword v153, v[248:249], off
	v_lshl_add_u64 v[248:249], v[248:249], 0, s[98:99]
	global_load_dword v154, v[248:249], off
	v_lshl_add_u64 v[248:249], v[248:249], 0, s[98:99]
	global_load_dword v155, v[248:249], off
	v_lshl_add_u64 v[248:249], v[248:249], 0, s[98:99]
	global_load_dword v156, v[248:249], off
	v_lshl_add_u64 v[248:249], v[248:249], 0, s[98:99]
	global_load_dword v157, v[248:249], off
	v_lshl_add_u64 v[248:249], v[248:249], 0, s[98:99]
	global_load_dword v158, v[248:249], off
	v_lshl_add_u64 v[248:249], v[248:249], 0, s[98:99]
	global_load_dword v159, v[248:249], off
	v_lshl_add_u64 v[248:249], v[248:249], 0, s[98:99]
	global_load_dword v160, v[248:249], off
	v_lshl_add_u64 v[248:249], v[248:249], 0, s[98:99]
	global_load_dword v161, v[248:249], off
	v_lshl_add_u64 v[248:249], v[248:249], 0, s[98:99]
	global_load_dword v162, v[248:249], off
	v_lshl_add_u64 v[248:249], v[248:249], 0, s[98:99]
	global_load_dword v163, v[248:249], off
	v_lshl_add_u64 v[248:249], v[248:249], 0, s[98:99]
	global_load_dword v164, v[248:249], off
	v_lshl_add_u64 v[248:249], v[248:249], 0, s[98:99]
	global_load_dword v165, v[248:249], off
	v_lshl_add_u64 v[248:249], v[248:249], 0, s[98:99]
	global_load_dword v166, v[248:249], off
	v_lshl_add_u64 v[248:249], v[248:249], 0, s[98:99]
	global_load_dword v167, v[248:249], off
	v_lshl_add_u64 v[248:249], v[248:249], 0, s[98:99]
	global_load_dword v168, v[248:249], off
	v_lshl_add_u64 v[248:249], v[248:249], 0, s[98:99]
	global_load_dword v169, v[248:249], off
	v_lshl_add_u64 v[248:249], v[248:249], 0, s[98:99]
	global_load_dword v170, v[248:249], off
	v_lshl_add_u64 v[248:249], v[248:249], 0, s[98:99]
	global_load_dword v171, v[248:249], off
	v_lshl_add_u64 v[248:249], v[248:249], 0, s[98:99]
	global_load_dword v172, v[248:249], off
	v_lshl_add_u64 v[248:249], v[248:249], 0, s[98:99]
	global_load_dword v173, v[248:249], off
	v_lshl_add_u64 v[248:249], v[248:249], 0, s[98:99]
	global_load_dword v174, v[248:249], off
	v_lshl_add_u64 v[248:249], v[248:249], 0, s[98:99]
	global_load_dword v175, v[248:249], off
	v_lshl_add_u64 v[248:249], v[248:249], 0, s[98:99]
	global_load_dword v176, v[248:249], off
	v_lshl_add_u64 v[248:249], v[248:249], 0, s[98:99]
	global_load_dword v177, v[248:249], off
	v_lshl_add_u64 v[248:249], v[248:249], 0, s[98:99]
	global_load_dword v178, v[248:249], off
	v_lshl_add_u64 v[248:249], v[248:249], 0, s[98:99]
	global_load_dword v179, v[248:249], off
	v_lshl_add_u64 v[248:249], v[248:249], 0, s[98:99]
	global_load_dword v180, v[248:249], off
	v_lshl_add_u64 v[248:249], v[248:249], 0, s[98:99]
	global_load_dword v181, v[248:249], off
	v_lshl_add_u64 v[248:249], v[248:249], 0, s[98:99]
	global_load_dword v182, v[248:249], off
	v_lshl_add_u64 v[248:249], v[248:249], 0, s[98:99]
	global_load_dword v183, v[248:249], off
	v_lshl_add_u64 v[248:249], v[248:249], 0, s[98:99]
	global_load_dword v184, v[248:249], off
	v_lshl_add_u64 v[248:249], v[248:249], 0, s[98:99]
; __device__ __forceinline__ void p0_prologue(const Args& a, const Frame& F) {
;     ...
;         float acc[9];
; #pragma unroll
;         for (int q = 0; q < 9; ++q) acc[q] = 0.f;
;         for (int kk = 0; kk < 128; kk += 8) {
;             float wv[8];
; #pragma unroll
;             for (int u = 0; u < 8; ++u) wv[u] = W[(size_t)(k0 + kk + u) * 6144];
	global_load_dword v185, v[248:249], off
	v_lshl_add_u64 v[248:249], v[248:249], 0, s[98:99]
	global_load_dword v186, v[248:249], off
	v_lshl_add_u64 v[248:249], v[248:249], 0, s[98:99]
	global_load_dword v187, v[248:249], off
	v_lshl_add_u64 v[248:249], v[248:249], 0, s[98:99]
	global_load_dword v188, v[248:249], off
	v_lshl_add_u64 v[248:249], v[248:249], 0, s[98:99]
	global_load_dword v189, v[248:249], off
	v_lshl_add_u64 v[248:249], v[248:249], 0, s[98:99]
	global_load_dword v190, v[248:249], off
	v_lshl_add_u64 v[248:249], v[248:249], 0, s[98:99]
	global_load_dword v191, v[248:249], off
	v_lshl_add_u64 v[248:249], v[248:249], 0, s[98:99]
	global_load_dword v192, v[248:249], off
	v_lshl_add_u64 v[248:249], v[248:249], 0, s[98:99]
	global_load_dword v193, v[248:249], off
	v_lshl_add_u64 v[248:249], v[248:249], 0, s[98:99]
	global_load_dword v194, v[248:249], off
	v_lshl_add_u64 v[248:249], v[248:249], 0, s[98:99]
	global_load_dword v195, v[248:249], off
	v_lshl_add_u64 v[248:249], v[248:249], 0, s[98:99]
	global_load_dword v196, v[248:249], off
	v_lshl_add_u64 v[248:249], v[248:249], 0, s[98:99]
	global_load_dword v197, v[248:249], off
	v_lshl_add_u64 v[248:249], v[248:249], 0, s[98:99]
	global_load_dword v198, v[248:249], off
	v_lshl_add_u64 v[248:249], v[248:249], 0, s[98:99]
	global_load_dword v199, v[248:249], off
	v_lshl_add_u64 v[248:249], v[248:249], 0, s[98:99]
	global_load_dword v200, v[248:249], off
	v_lshl_add_u64 v[248:249], v[248:249], 0, s[98:99]
	global_load_dword v201, v[248:249], off
	v_lshl_add_u64 v[248:249], v[248:249], 0, s[98:99]
	global_load_dword v202, v[248:249], off
	v_lshl_add_u64 v[248:249], v[248:249], 0, s[98:99]
	global_load_dword v203, v[248:249], off
	v_lshl_add_u64 v[248:249], v[248:249], 0, s[98:99]
	global_load_dword v204, v[248:249], off
	v_lshl_add_u64 v[248:249], v[248:249], 0, s[98:99]
	global_load_dword v205, v[248:249], off
	v_lshl_add_u64 v[248:249], v[248:249], 0, s[98:99]
	global_load_dword v206, v[248:249], off
	v_lshl_add_u64 v[248:249], v[248:249], 0, s[98:99]
	global_load_dword v207, v[248:249], off
	v_lshl_add_u64 v[248:249], v[248:249], 0, s[98:99]
	global_load_dword v208, v[248:249], off
	v_lshl_add_u64 v[248:249], v[248:249], 0, s[98:99]
	global_load_dword v209, v[248:249], off
	v_lshl_add_u64 v[248:249], v[248:249], 0, s[98:99]
	global_load_dword v210, v[248:249], off
	v_lshl_add_u64 v[248:249], v[248:249], 0, s[98:99]
	global_load_dword v211, v[248:249], off
	v_lshl_add_u64 v[248:249], v[248:249], 0, s[98:99]
	global_load_dword v212, v[248:249], off
	v_lshl_add_u64 v[248:249], v[248:249], 0, s[98:99]
	global_load_dword v213, v[248:249], off
	v_lshl_add_u64 v[248:249], v[248:249], 0, s[98:99]
	global_load_dword v214, v[248:249], off
	v_lshl_add_u64 v[248:249], v[248:249], 0, s[98:99]
	global_load_dword v215, v[248:249], off
	v_lshl_add_u64 v[248:249], v[248:249], 0, s[98:99]
	global_load_dword v216, v[248:249], off
	v_lshl_add_u64 v[248:249], v[248:249], 0, s[98:99]
	global_load_dword v217, v[248:249], off
	v_lshl_add_u64 v[248:249], v[248:249], 0, s[98:99]
	global_load_dword v218, v[248:249], off
	v_lshl_add_u64 v[248:249], v[248:249], 0, s[98:99]
	global_load_dword v219, v[248:249], off
	v_lshl_add_u64 v[248:249], v[248:249], 0, s[98:99]
	global_load_dword v220, v[248:249], off
	v_lshl_add_u64 v[248:249], v[248:249], 0, s[98:99]
	global_load_dword v221, v[248:249], off
	v_lshl_add_u64 v[248:249], v[248:249], 0, s[98:99]
	global_load_dword v222, v[248:249], off
	v_lshl_add_u64 v[248:249], v[248:249], 0, s[98:99]
	global_load_dword v223, v[248:249], off
	v_lshl_add_u64 v[248:249], v[248:249], 0, s[98:99]
	global_load_dword v224, v[248:249], off
	v_lshl_add_u64 v[248:249], v[248:249], 0, s[98:99]
	global_load_dword v225, v[248:249], off
	v_lshl_add_u64 v[248:249], v[248:249], 0, s[98:99]
	global_load_dword v226, v[248:249], off
	v_lshl_add_u64 v[248:249], v[248:249], 0, s[98:99]
	global_load_dword v227, v[248:249], off
	v_lshl_add_u64 v[248:249], v[248:249], 0, s[98:99]
	global_load_dword v228, v[248:249], off
	v_lshl_add_u64 v[248:249], v[248:249], 0, s[98:99]
	global_load_dword v229, v[248:249], off
	v_lshl_add_u64 v[248:249], v[248:249], 0, s[98:99]
	global_load_dword v230, v[248:249], off
	v_lshl_add_u64 v[248:249], v[248:249], 0, s[98:99]
	global_load_dword v231, v[248:249], off
	v_lshl_add_u64 v[248:249], v[248:249], 0, s[98:99]
	global_load_dword v232, v[248:249], off
	v_lshl_add_u64 v[248:249], v[248:249], 0, s[98:99]
	global_load_dword v233, v[248:249], off
	v_lshl_add_u64 v[248:249], v[248:249], 0, s[98:99]
	global_load_dword v234, v[248:249], off
	v_lshl_add_u64 v[248:249], v[248:249], 0, s[98:99]
	global_load_dword v235, v[248:249], off
	v_lshl_add_u64 v[248:249], v[248:249], 0, s[98:99]
	global_load_dword v236, v[248:249], off
	v_lshl_add_u64 v[248:249], v[248:249], 0, s[98:99]
	global_load_dword v237, v[248:249], off
	v_lshl_add_u64 v[248:249], v[248:249], 0, s[98:99]
	global_load_dword v238, v[248:249], off
	v_lshl_add_u64 v[248:249], v[248:249], 0, s[98:99]
	global_load_dword v239, v[248:249], off
	v_lshl_add_u64 v[248:249], v[248:249], 0, s[98:99]
	global_load_dword v240, v[248:249], off
	v_lshl_add_u64 v[248:249], v[248:249], 0, s[98:99]
	global_load_dword v241, v[248:249], off
	v_lshl_add_u64 v[248:249], v[248:249], 0, s[98:99]
	global_load_dword v242, v[248:249], off
	v_lshl_add_u64 v[248:249], v[248:249], 0, s[98:99]
	global_load_dword v243, v[248:249], off
	v_lshl_add_u64 v[248:249], v[248:249], 0, s[98:99]
	global_load_dword v244, v[248:249], off
	v_lshl_add_u64 v[248:249], v[248:249], 0, s[98:99]
	global_load_dword v245, v[248:249], off
	v_lshl_add_u64 v[248:249], v[248:249], 0, s[98:99]
	global_load_dword v246, v[248:249], off
	v_lshl_add_u64 v[248:249], v[248:249], 0, s[98:99]
	global_load_dword v247, v[248:249], off
	s_mov_b32 s14, -8
	s_mov_b32 s15, s33
	v_mov_b32_e32 v11, v10
	v_mov_b32_e32 v12, v10
	v_mov_b32_e32 v13, v10
	v_mov_b32_e32 v14, v10
	v_mov_b32_e32 v15, v10
	v_mov_b32_e32 v16, v10
	v_mov_b32_e32 v17, v10
	v_mov_b32_e32 v2, v10
	s_waitcnt lgkmcnt(0)
	s_barrier
; #define LAS __attribute__((address_space(3)))
; __device__ __forceinline__ void p0_prologue(const Args& a, const Frame& F) {
;     ...
;         for (int kk = 0; kk < 128; kk += 8) {
;             float wv[8];
; #pragma unroll
;             for (int u = 0; u < 8; ++u) wv[u] = W[(size_t)(k0 + kk + u) * 6144];
; #pragma unroll
;             for (int q = 0; q < 9; ++q) { const f32x4 s0 = *(const LAS f32x4*)(sc + q * 1024 + k0 + kk), s1 = *(const LAS f32x4*)(sc + q * 1024 + k0 + kk + 4);
;                 acc[q] += (s0.x * wv[0] + s0.y * wv[1]) + (s0.z * wv[2] + s0.w * wv[3]) + (s1.x * wv[4] + s1.y * wv[5]) + (s1.z * wv[6] + s1.w * wv[7]); }
	s_waitcnt vmcnt(63)
	v_add_co_u32_e32 v94, vcc, 0x6000, v8
	v_mov_b32_e32 v7, s15
	s_nop 0
	v_addc_co_u32_e32 v95, vcc, 0, v9, vcc
	v_add_co_u32_e32 v98, vcc, 0xc000, v8
	v_mov_b32_e32 v96, v120
	s_nop 0
	v_addc_co_u32_e32 v99, vcc, 0, v9, vcc
	v_add_co_u32_e32 v100, vcc, 0x12000, v8
	ds_read_b128 v[22:25], v7
	ds_read_b128 v[26:29], v7 offset:16
	ds_read_b128 v[30:33], v7 offset:4096
	ds_read_b128 v[34:37], v7 offset:4112
	ds_read_b128 v[38:41], v7 offset:8192
	ds_read_b128 v[42:45], v7 offset:8208
	ds_read_b128 v[46:49], v7 offset:12288
	ds_read_b128 v[50:53], v7 offset:12304
	ds_read_b128 v[54:57], v7 offset:16384
	ds_read_b128 v[58:61], v7 offset:16400
	ds_read_b128 v[62:65], v7 offset:20480
	ds_read_b128 v[66:69], v7 offset:20496
	ds_read_b128 v[70:73], v7 offset:24576
	ds_read_b128 v[74:77], v7 offset:24592
	ds_read_b128 v[78:81], v7 offset:28672
	ds_read_b128 v[82:85], v7 offset:28688
	v_addc_co_u32_e32 v101, vcc, 0, v9, vcc
	v_add_co_u32_e32 v102, vcc, 0x18000, v8
	ds_read_b128 v[86:89], v7 offset:32768
	ds_read_b128 v[90:93], v7 offset:32784
	v_addc_co_u32_e32 v103, vcc, 0, v9, vcc
	v_mov_b32_e32 v94, v121
	v_add_co_u32_e32 v104, vcc, 0x1e000, v8
	v_mov_b32_e32 v98, v122
	s_nop 0
	v_mov_b32_e32 v100, v123
	v_addc_co_u32_e32 v105, vcc, 0, v9, vcc
	v_add_co_u32_e32 v106, vcc, 0x24000, v8
	v_mov_b32_e32 v102, v124
	s_waitcnt lgkmcnt(14)
	v_mov_b32_e32 v108, v22
	v_mov_b32_e32 v22, v24
	v_mov_b32_e32 v24, v26
	v_mov_b32_e32 v26, v28
	s_waitcnt lgkmcnt(13)
	v_mov_b32_e32 v28, v38
	v_mov_b32_e32 v38, v40
	s_waitcnt lgkmcnt(12)
	v_mov_b32_e32 v40, v42
	v_mov_b32_e32 v42, v44
	s_waitcnt lgkmcnt(9)
	v_mov_b32_e32 v44, v54
	v_mov_b32_e32 v54, v56
	v_mov_b32_e32 v56, v125
	v_addc_co_u32_e32 v107, vcc, 0, v9, vcc
	v_add_co_u32_e32 v104, vcc, 0x2a000, v8
	v_mov_b32_e32 v109, v30
	s_nop 0
	v_addc_co_u32_e32 v105, vcc, 0, v9, vcc
	v_mov_b32_e32 v106, v126
	s_nop 0
	v_mov_b32_e32 v104, v127
	v_mov_b32_e32 v30, v23
	v_mov_b32_e32 v23, v32
	v_mov_b32_e32 v32, v25
	v_mov_b32_e32 v25, v34
	v_mov_b32_e32 v34, v27
	v_mov_b32_e32 v27, v36
	v_mov_b32_e32 v36, v29
	v_mov_b32_e32 v29, v46
	v_mov_b32_e32 v46, v39
	s_waitcnt lgkmcnt(6)
	v_mov_b32_e32 v111, v66
	v_mov_b32_e32 v66, v59
	v_mov_b32_e32 v59, v68
	v_mov_b32_e32 v68, v61
	s_waitcnt lgkmcnt(3)
	v_mov_b32_e32 v61, v78
	v_mov_b32_e32 v78, v71
	v_mov_b32_e32 v39, v48
	v_mov_b32_e32 v48, v41
	v_mov_b32_e32 v41, v50
	v_mov_b32_e32 v50, v43
	v_mov_b32_e32 v43, v52
	v_mov_b32_e32 v52, v45
	v_mov_b32_e32 v45, v62
	v_mov_b32_e32 v62, v55
	v_mov_b32_e32 v55, v64
	v_mov_b32_e32 v64, v57
	v_mov_b32_e32 v110, v58
	v_mov_b32_e32 v58, v60
	v_mov_b32_e32 v60, v70
	v_mov_b32_e32 v71, v80
	v_mov_b32_e32 v80, v73
	v_mov_b32_e32 v70, v72
	v_mov_b32_e32 v72, v74
	s_waitcnt lgkmcnt(2)
	v_mov_b32_e32 v73, v82
	v_mov_b32_e32 v82, v75
	v_mov_b32_e32 v74, v76
	v_mov_b32_e32 v75, v84
	v_mov_b32_e32 v84, v77
	s_waitcnt lgkmcnt(1)
	v_mov_b32_e32 v76, v87
	v_mov_b32_e32 v87, v89
	v_mov_b32_e32 v77, v88
	s_waitcnt lgkmcnt(0)
	v_mov_b32_e32 v89, v90
	v_mov_b32_e32 v90, v93
	v_mov_b32_e32 v88, v92
	s_add_i32 s14, s14, 8
	s_add_i32 s15, s15, 32
	s_cmpk_gt_u32 s14, 0x77
	v_lshl_add_u64 v[8:9], v[8:9], 0, s[12:13]
	v_pk_mul_f32 v[46:47], v[94:95], v[46:47] op_sel_hi:[0,1]
	v_pk_mul_f32 v[78:79], v[94:95], v[78:79] op_sel_hi:[0,1]
	v_pk_mul_f32 v[30:31], v[94:95], v[30:31] op_sel_hi:[0,1]
	v_pk_mul_f32 v[62:63], v[94:95], v[62:63] op_sel_hi:[0,1]
	v_pk_fma_f32 v[28:29], v[96:97], v[28:29], v[46:47] op_sel_hi:[0,1,1]
	v_pk_fma_f32 v[46:47], v[96:97], v[60:61], v[78:79] op_sel_hi:[0,1,1]
	v_pk_mul_f32 v[32:33], v[100:101], v[32:33] op_sel_hi:[0,1]
	v_pk_mul_f32 v[48:49], v[100:101], v[48:49] op_sel_hi:[0,1]
	v_pk_mul_f32 v[60:61], v[100:101], v[64:65] op_sel_hi:[0,1]
	v_pk_fma_f32 v[30:31], v[96:97], v[108:109], v[30:31] op_sel_hi:[0,1,1]
	v_pk_fma_f32 v[44:45], v[96:97], v[44:45], v[62:63] op_sel_hi:[0,1,1]
	v_pk_fma_f32 v[22:23], v[98:99], v[22:23], v[32:33] op_sel_hi:[0,1,1]
	v_pk_fma_f32 v[32:33], v[98:99], v[38:39], v[48:49] op_sel_hi:[0,1,1]
	v_pk_fma_f32 v[38:39], v[98:99], v[54:55], v[60:61] op_sel_hi:[0,1,1]
	v_pk_add_f32 v[22:23], v[30:31], v[22:23]
	v_pk_add_f32 v[30:31], v[44:45], v[38:39]
	v_pk_mul_f32 v[62:63], v[100:101], v[80:81] op_sel_hi:[0,1]
	v_mov_b32_e32 v97, v100
	v_pk_add_f32 v[28:29], v[28:29], v[32:33]
	v_pk_mul_f32 v[34:35], v[56:57], v[34:35] op_sel_hi:[0,1]
	v_pk_mul_f32 v[38:39], v[56:57], v[50:51] op_sel_hi:[0,1]
	v_pk_mul_f32 v[44:45], v[56:57], v[66:67] op_sel_hi:[0,1]
	v_pk_fma_f32 v[24:25], v[102:103], v[24:25], v[34:35] op_sel_hi:[0,1,1]
	v_pk_fma_f32 v[34:35], v[102:103], v[40:41], v[38:39] op_sel_hi:[0,1,1]
	v_pk_fma_f32 v[38:39], v[102:103], v[110:111], v[44:45] op_sel_hi:[0,1,1]
	v_mov_b32_e32 v95, v98
	v_pk_mul_f32 v[64:65], v[96:97], v[86:87]
	v_pk_fma_f32 v[48:49], v[98:99], v[70:71], v[62:63] op_sel_hi:[0,1,1]
	v_pk_add_f32 v[22:23], v[22:23], v[24:25]
	v_pk_mul_f32 v[24:25], v[104:105], v[36:37] op_sel_hi:[0,1]
	v_pk_add_f32 v[28:29], v[28:29], v[34:35]
	v_pk_mul_f32 v[34:35], v[104:105], v[52:53] op_sel_hi:[0,1]
	v_pk_add_f32 v[30:31], v[30:31], v[38:39]
	v_pk_mul_f32 v[36:37], v[104:105], v[68:69] op_sel_hi:[0,1]
	v_pk_mul_f32 v[38:39], v[104:105], v[84:85] op_sel_hi:[0,1]
	v_mov_b32_e32 v105, v56
	v_pk_fma_f32 v[54:55], v[94:95], v[76:77], v[64:65]
	v_pk_add_f32 v[32:33], v[46:47], v[48:49]
	v_pk_mul_f32 v[46:47], v[56:57], v[82:83] op_sel_hi:[0,1]
	v_pk_fma_f32 v[24:25], v[106:107], v[26:27], v[24:25] op_sel_hi:[0,1,1]
	v_pk_fma_f32 v[26:27], v[106:107], v[42:43], v[34:35] op_sel_hi:[0,1,1]
	v_pk_fma_f32 v[34:35], v[106:107], v[58:59], v[36:37] op_sel_hi:[0,1,1]
	v_pk_fma_f32 v[36:37], v[106:107], v[74:75], v[38:39] op_sel_hi:[0,1,1]
	v_mov_b32_e32 v107, v102
	v_pk_mul_f32 v[38:39], v[104:105], v[90:91]
	v_pk_fma_f32 v[40:41], v[102:103], v[72:73], v[46:47] op_sel_hi:[0,1,1]
	v_add_f32_e32 v7, v54, v55
	v_pk_add_f32 v[22:23], v[24:25], v[22:23]
	v_pk_add_f32 v[24:25], v[26:27], v[28:29]
	v_pk_add_f32 v[26:27], v[34:35], v[30:31]
	v_pk_fma_f32 v[30:31], v[106:107], v[88:89], v[38:39]
	v_pk_add_f32 v[32:33], v[32:33], v[40:41]
	v_add_f32_e32 v7, v7, v31
	v_pk_add_f32 v[28:29], v[36:37], v[32:33]
	v_add_f32_e32 v7, v30, v7
	v_pk_add_f32 v[10:11], v[10:11], v[22:23]
	v_pk_add_f32 v[12:13], v[12:13], v[24:25]
	v_pk_add_f32 v[14:15], v[14:15], v[26:27]
	v_pk_add_f32 v[16:17], v[16:17], v[28:29]
	v_add_f32_e32 v2, v2, v7
	s_waitcnt vmcnt(63)
; #define LAS __attribute__((address_space(3)))
; __device__ __forceinline__ void p0_prologue(const Args& a, const Frame& F) {
;     ...
;         for (int kk = 0; kk < 128; kk += 8) {
;             float wv[8];
; #pragma unroll
;             for (int u = 0; u < 8; ++u) wv[u] = W[(size_t)(k0 + kk + u) * 6144];
; #pragma unroll
;             for (int q = 0; q < 9; ++q) { const f32x4 s0 = *(const LAS f32x4*)(sc + q * 1024 + k0 + kk), s1 = *(const LAS f32x4*)(sc + q * 1024 + k0 + kk + 4);
;                 acc[q] += (s0.x * wv[0] + s0.y * wv[1]) + (s0.z * wv[2] + s0.w * wv[3]) + (s1.x * wv[4] + s1.y * wv[5]) + (s1.z * wv[6] + s1.w * wv[7]); }
	v_add_co_u32_e32 v94, vcc, 0x6000, v8
	v_mov_b32_e32 v7, s15
	s_nop 0
	v_addc_co_u32_e32 v95, vcc, 0, v9, vcc
	v_add_co_u32_e32 v98, vcc, 0xc000, v8
	v_mov_b32_e32 v96, v128
	s_nop 0
	v_addc_co_u32_e32 v99, vcc, 0, v9, vcc
	v_add_co_u32_e32 v100, vcc, 0x12000, v8
	ds_read_b128 v[22:25], v7
	ds_read_b128 v[26:29], v7 offset:16
	ds_read_b128 v[30:33], v7 offset:4096
	ds_read_b128 v[34:37], v7 offset:4112
	ds_read_b128 v[38:41], v7 offset:8192
	ds_read_b128 v[42:45], v7 offset:8208
	ds_read_b128 v[46:49], v7 offset:12288
	ds_read_b128 v[50:53], v7 offset:12304
	ds_read_b128 v[54:57], v7 offset:16384
	ds_read_b128 v[58:61], v7 offset:16400
	ds_read_b128 v[62:65], v7 offset:20480
	ds_read_b128 v[66:69], v7 offset:20496
	ds_read_b128 v[70:73], v7 offset:24576
	ds_read_b128 v[74:77], v7 offset:24592
	ds_read_b128 v[78:81], v7 offset:28672
	ds_read_b128 v[82:85], v7 offset:28688
	v_addc_co_u32_e32 v101, vcc, 0, v9, vcc
	v_add_co_u32_e32 v102, vcc, 0x18000, v8
	ds_read_b128 v[86:89], v7 offset:32768
	ds_read_b128 v[90:93], v7 offset:32784
	v_addc_co_u32_e32 v103, vcc, 0, v9, vcc
	v_mov_b32_e32 v94, v129
	v_add_co_u32_e32 v104, vcc, 0x1e000, v8
	v_mov_b32_e32 v98, v130
	s_nop 0
	v_mov_b32_e32 v100, v131
	v_addc_co_u32_e32 v105, vcc, 0, v9, vcc
	v_add_co_u32_e32 v106, vcc, 0x24000, v8
	v_mov_b32_e32 v102, v132
	s_waitcnt lgkmcnt(14)
	v_mov_b32_e32 v108, v22
	v_mov_b32_e32 v22, v24
	v_mov_b32_e32 v24, v26
	v_mov_b32_e32 v26, v28
	s_waitcnt lgkmcnt(13)
	v_mov_b32_e32 v28, v38
	v_mov_b32_e32 v38, v40
	s_waitcnt lgkmcnt(12)
	v_mov_b32_e32 v40, v42
	v_mov_b32_e32 v42, v44
	s_waitcnt lgkmcnt(9)
	v_mov_b32_e32 v44, v54
	v_mov_b32_e32 v54, v56
	v_mov_b32_e32 v56, v133
	v_addc_co_u32_e32 v107, vcc, 0, v9, vcc
	v_add_co_u32_e32 v104, vcc, 0x2a000, v8
	v_mov_b32_e32 v109, v30
	s_nop 0
	v_addc_co_u32_e32 v105, vcc, 0, v9, vcc
	v_mov_b32_e32 v106, v134
	s_nop 0
	v_mov_b32_e32 v104, v135
	v_mov_b32_e32 v30, v23
	v_mov_b32_e32 v23, v32
	v_mov_b32_e32 v32, v25
	v_mov_b32_e32 v25, v34
	v_mov_b32_e32 v34, v27
	v_mov_b32_e32 v27, v36
	v_mov_b32_e32 v36, v29
	v_mov_b32_e32 v29, v46
	v_mov_b32_e32 v46, v39
	s_waitcnt lgkmcnt(6)
	v_mov_b32_e32 v111, v66
	v_mov_b32_e32 v66, v59
	v_mov_b32_e32 v59, v68
	v_mov_b32_e32 v68, v61
	s_waitcnt lgkmcnt(3)
	v_mov_b32_e32 v61, v78
	v_mov_b32_e32 v78, v71
	v_mov_b32_e32 v39, v48
	v_mov_b32_e32 v48, v41
	v_mov_b32_e32 v41, v50
	v_mov_b32_e32 v50, v43
	v_mov_b32_e32 v43, v52
	v_mov_b32_e32 v52, v45
	v_mov_b32_e32 v45, v62
	v_mov_b32_e32 v62, v55
	v_mov_b32_e32 v55, v64
	v_mov_b32_e32 v64, v57
	v_mov_b32_e32 v110, v58
	v_mov_b32_e32 v58, v60
	v_mov_b32_e32 v60, v70
	v_mov_b32_e32 v71, v80
	v_mov_b32_e32 v80, v73
	v_mov_b32_e32 v70, v72
	v_mov_b32_e32 v72, v74
	s_waitcnt lgkmcnt(2)
	v_mov_b32_e32 v73, v82
	v_mov_b32_e32 v82, v75
	v_mov_b32_e32 v74, v76
	v_mov_b32_e32 v75, v84
	v_mov_b32_e32 v84, v77
	s_waitcnt lgkmcnt(1)
	v_mov_b32_e32 v76, v87
	v_mov_b32_e32 v87, v89
	v_mov_b32_e32 v77, v88
	s_waitcnt lgkmcnt(0)
	v_mov_b32_e32 v89, v90
	v_mov_b32_e32 v90, v93
	v_mov_b32_e32 v88, v92
	s_add_i32 s14, s14, 8
	s_add_i32 s15, s15, 32
	s_cmpk_gt_u32 s14, 0x77
	v_lshl_add_u64 v[8:9], v[8:9], 0, s[12:13]
	v_pk_mul_f32 v[46:47], v[94:95], v[46:47] op_sel_hi:[0,1]
	v_pk_mul_f32 v[78:79], v[94:95], v[78:79] op_sel_hi:[0,1]
	v_pk_mul_f32 v[30:31], v[94:95], v[30:31] op_sel_hi:[0,1]
	v_pk_mul_f32 v[62:63], v[94:95], v[62:63] op_sel_hi:[0,1]
	v_pk_fma_f32 v[28:29], v[96:97], v[28:29], v[46:47] op_sel_hi:[0,1,1]
	v_pk_fma_f32 v[46:47], v[96:97], v[60:61], v[78:79] op_sel_hi:[0,1,1]
	v_pk_mul_f32 v[32:33], v[100:101], v[32:33] op_sel_hi:[0,1]
	v_pk_mul_f32 v[48:49], v[100:101], v[48:49] op_sel_hi:[0,1]
	v_pk_mul_f32 v[60:61], v[100:101], v[64:65] op_sel_hi:[0,1]
	v_pk_fma_f32 v[30:31], v[96:97], v[108:109], v[30:31] op_sel_hi:[0,1,1]
	v_pk_fma_f32 v[44:45], v[96:97], v[44:45], v[62:63] op_sel_hi:[0,1,1]
	v_pk_fma_f32 v[22:23], v[98:99], v[22:23], v[32:33] op_sel_hi:[0,1,1]
	v_pk_fma_f32 v[32:33], v[98:99], v[38:39], v[48:49] op_sel_hi:[0,1,1]
	v_pk_fma_f32 v[38:39], v[98:99], v[54:55], v[60:61] op_sel_hi:[0,1,1]
	v_pk_add_f32 v[22:23], v[30:31], v[22:23]
	v_pk_add_f32 v[30:31], v[44:45], v[38:39]
	v_pk_mul_f32 v[62:63], v[100:101], v[80:81] op_sel_hi:[0,1]
	v_mov_b32_e32 v97, v100
	v_pk_add_f32 v[28:29], v[28:29], v[32:33]
	v_pk_mul_f32 v[34:35], v[56:57], v[34:35] op_sel_hi:[0,1]
	v_pk_mul_f32 v[38:39], v[56:57], v[50:51] op_sel_hi:[0,1]
	v_pk_mul_f32 v[44:45], v[56:57], v[66:67] op_sel_hi:[0,1]
	v_pk_fma_f32 v[24:25], v[102:103], v[24:25], v[34:35] op_sel_hi:[0,1,1]
	v_pk_fma_f32 v[34:35], v[102:103], v[40:41], v[38:39] op_sel_hi:[0,1,1]
	v_pk_fma_f32 v[38:39], v[102:103], v[110:111], v[44:45] op_sel_hi:[0,1,1]
	v_mov_b32_e32 v95, v98
	v_pk_mul_f32 v[64:65], v[96:97], v[86:87]
	v_pk_fma_f32 v[48:49], v[98:99], v[70:71], v[62:63] op_sel_hi:[0,1,1]
	v_pk_add_f32 v[22:23], v[22:23], v[24:25]
	v_pk_mul_f32 v[24:25], v[104:105], v[36:37] op_sel_hi:[0,1]
	v_pk_add_f32 v[28:29], v[28:29], v[34:35]
	v_pk_mul_f32 v[34:35], v[104:105], v[52:53] op_sel_hi:[0,1]
	v_pk_add_f32 v[30:31], v[30:31], v[38:39]
	v_pk_mul_f32 v[36:37], v[104:105], v[68:69] op_sel_hi:[0,1]
	v_pk_mul_f32 v[38:39], v[104:105], v[84:85] op_sel_hi:[0,1]
	v_mov_b32_e32 v105, v56
	v_pk_fma_f32 v[54:55], v[94:95], v[76:77], v[64:65]
	v_pk_add_f32 v[32:33], v[46:47], v[48:49]
	v_pk_mul_f32 v[46:47], v[56:57], v[82:83] op_sel_hi:[0,1]
	v_pk_fma_f32 v[24:25], v[106:107], v[26:27], v[24:25] op_sel_hi:[0,1,1]
	v_pk_fma_f32 v[26:27], v[106:107], v[42:43], v[34:35] op_sel_hi:[0,1,1]
	v_pk_fma_f32 v[34:35], v[106:107], v[58:59], v[36:37] op_sel_hi:[0,1,1]
	v_pk_fma_f32 v[36:37], v[106:107], v[74:75], v[38:39] op_sel_hi:[0,1,1]
	v_mov_b32_e32 v107, v102
	v_pk_mul_f32 v[38:39], v[104:105], v[90:91]
	v_pk_fma_f32 v[40:41], v[102:103], v[72:73], v[46:47] op_sel_hi:[0,1,1]
	v_add_f32_e32 v7, v54, v55
	v_pk_add_f32 v[22:23], v[24:25], v[22:23]
	v_pk_add_f32 v[24:25], v[26:27], v[28:29]
	v_pk_add_f32 v[26:27], v[34:35], v[30:31]
	v_pk_fma_f32 v[30:31], v[106:107], v[88:89], v[38:39]
	v_pk_add_f32 v[32:33], v[32:33], v[40:41]
	v_add_f32_e32 v7, v7, v31
	v_pk_add_f32 v[28:29], v[36:37], v[32:33]
	v_add_f32_e32 v7, v30, v7
	v_pk_add_f32 v[10:11], v[10:11], v[22:23]
	v_pk_add_f32 v[12:13], v[12:13], v[24:25]
	v_pk_add_f32 v[14:15], v[14:15], v[26:27]
	v_pk_add_f32 v[16:17], v[16:17], v[28:29]
	v_add_f32_e32 v2, v2, v7
	s_waitcnt vmcnt(63)
; #define LAS __attribute__((address_space(3)))
; __device__ __forceinline__ void p0_prologue(const Args& a, const Frame& F) {
;     ...
;         for (int kk = 0; kk < 128; kk += 8) {
;             float wv[8];
; #pragma unroll
;             for (int u = 0; u < 8; ++u) wv[u] = W[(size_t)(k0 + kk + u) * 6144];
; #pragma unroll
;             for (int q = 0; q < 9; ++q) { const f32x4 s0 = *(const LAS f32x4*)(sc + q * 1024 + k0 + kk), s1 = *(const LAS f32x4*)(sc + q * 1024 + k0 + kk + 4);
;                 acc[q] += (s0.x * wv[0] + s0.y * wv[1]) + (s0.z * wv[2] + s0.w * wv[3]) + (s1.x * wv[4] + s1.y * wv[5]) + (s1.z * wv[6] + s1.w * wv[7]); }
	v_add_co_u32_e32 v94, vcc, 0x6000, v8
	v_mov_b32_e32 v7, s15
	s_nop 0
	v_addc_co_u32_e32 v95, vcc, 0, v9, vcc
	v_add_co_u32_e32 v98, vcc, 0xc000, v8
	v_mov_b32_e32 v96, v136
	s_nop 0
	v_addc_co_u32_e32 v99, vcc, 0, v9, vcc
	v_add_co_u32_e32 v100, vcc, 0x12000, v8
	ds_read_b128 v[22:25], v7
	ds_read_b128 v[26:29], v7 offset:16
	ds_read_b128 v[30:33], v7 offset:4096
	ds_read_b128 v[34:37], v7 offset:4112
	ds_read_b128 v[38:41], v7 offset:8192
	ds_read_b128 v[42:45], v7 offset:8208
	ds_read_b128 v[46:49], v7 offset:12288
	ds_read_b128 v[50:53], v7 offset:12304
	ds_read_b128 v[54:57], v7 offset:16384
	ds_read_b128 v[58:61], v7 offset:16400
	ds_read_b128 v[62:65], v7 offset:20480
	ds_read_b128 v[66:69], v7 offset:20496
	ds_read_b128 v[70:73], v7 offset:24576
	ds_read_b128 v[74:77], v7 offset:24592
	ds_read_b128 v[78:81], v7 offset:28672
	ds_read_b128 v[82:85], v7 offset:28688
	v_addc_co_u32_e32 v101, vcc, 0, v9, vcc
	v_add_co_u32_e32 v102, vcc, 0x18000, v8
	ds_read_b128 v[86:89], v7 offset:32768
	ds_read_b128 v[90:93], v7 offset:32784
	v_addc_co_u32_e32 v103, vcc, 0, v9, vcc
	v_mov_b32_e32 v94, v137
	v_add_co_u32_e32 v104, vcc, 0x1e000, v8
	v_mov_b32_e32 v98, v138
	s_nop 0
	v_mov_b32_e32 v100, v139
	v_addc_co_u32_e32 v105, vcc, 0, v9, vcc
	v_add_co_u32_e32 v106, vcc, 0x24000, v8
	v_mov_b32_e32 v102, v140
	s_waitcnt lgkmcnt(14)
	v_mov_b32_e32 v108, v22
	v_mov_b32_e32 v22, v24
	v_mov_b32_e32 v24, v26
	v_mov_b32_e32 v26, v28
	s_waitcnt lgkmcnt(13)
	v_mov_b32_e32 v28, v38
	v_mov_b32_e32 v38, v40
	s_waitcnt lgkmcnt(12)
	v_mov_b32_e32 v40, v42
	v_mov_b32_e32 v42, v44
	s_waitcnt lgkmcnt(9)
	v_mov_b32_e32 v44, v54
	v_mov_b32_e32 v54, v56
	v_mov_b32_e32 v56, v141
	v_addc_co_u32_e32 v107, vcc, 0, v9, vcc
	v_add_co_u32_e32 v104, vcc, 0x2a000, v8
	v_mov_b32_e32 v109, v30
	s_nop 0
	v_addc_co_u32_e32 v105, vcc, 0, v9, vcc
	v_mov_b32_e32 v106, v142
	s_nop 0
	v_mov_b32_e32 v104, v143
	v_mov_b32_e32 v30, v23
	v_mov_b32_e32 v23, v32
	v_mov_b32_e32 v32, v25
	v_mov_b32_e32 v25, v34
	v_mov_b32_e32 v34, v27
	v_mov_b32_e32 v27, v36
	v_mov_b32_e32 v36, v29
	v_mov_b32_e32 v29, v46
	v_mov_b32_e32 v46, v39
	s_waitcnt lgkmcnt(6)
	v_mov_b32_e32 v111, v66
	v_mov_b32_e32 v66, v59
	v_mov_b32_e32 v59, v68
	v_mov_b32_e32 v68, v61
	s_waitcnt lgkmcnt(3)
	v_mov_b32_e32 v61, v78
	v_mov_b32_e32 v78, v71
	v_mov_b32_e32 v39, v48
	v_mov_b32_e32 v48, v41
	v_mov_b32_e32 v41, v50
	v_mov_b32_e32 v50, v43
	v_mov_b32_e32 v43, v52
	v_mov_b32_e32 v52, v45
	v_mov_b32_e32 v45, v62
	v_mov_b32_e32 v62, v55
	v_mov_b32_e32 v55, v64
	v_mov_b32_e32 v64, v57
	v_mov_b32_e32 v110, v58
	v_mov_b32_e32 v58, v60
	v_mov_b32_e32 v60, v70
	v_mov_b32_e32 v71, v80
	v_mov_b32_e32 v80, v73
	v_mov_b32_e32 v70, v72
	v_mov_b32_e32 v72, v74
	s_waitcnt lgkmcnt(2)
	v_mov_b32_e32 v73, v82
	v_mov_b32_e32 v82, v75
	v_mov_b32_e32 v74, v76
	v_mov_b32_e32 v75, v84
	v_mov_b32_e32 v84, v77
	s_waitcnt lgkmcnt(1)
	v_mov_b32_e32 v76, v87
	v_mov_b32_e32 v87, v89
	v_mov_b32_e32 v77, v88
	s_waitcnt lgkmcnt(0)
	v_mov_b32_e32 v89, v90
	v_mov_b32_e32 v90, v93
	v_mov_b32_e32 v88, v92
	s_add_i32 s14, s14, 8
	s_add_i32 s15, s15, 32
	s_cmpk_gt_u32 s14, 0x77
	v_lshl_add_u64 v[8:9], v[8:9], 0, s[12:13]
	v_pk_mul_f32 v[46:47], v[94:95], v[46:47] op_sel_hi:[0,1]
	v_pk_mul_f32 v[78:79], v[94:95], v[78:79] op_sel_hi:[0,1]
	v_pk_mul_f32 v[30:31], v[94:95], v[30:31] op_sel_hi:[0,1]
	v_pk_mul_f32 v[62:63], v[94:95], v[62:63] op_sel_hi:[0,1]
	v_pk_fma_f32 v[28:29], v[96:97], v[28:29], v[46:47] op_sel_hi:[0,1,1]
	v_pk_fma_f32 v[46:47], v[96:97], v[60:61], v[78:79] op_sel_hi:[0,1,1]
	v_pk_mul_f32 v[32:33], v[100:101], v[32:33] op_sel_hi:[0,1]
	v_pk_mul_f32 v[48:49], v[100:101], v[48:49] op_sel_hi:[0,1]
	v_pk_mul_f32 v[60:61], v[100:101], v[64:65] op_sel_hi:[0,1]
	v_pk_fma_f32 v[30:31], v[96:97], v[108:109], v[30:31] op_sel_hi:[0,1,1]
	v_pk_fma_f32 v[44:45], v[96:97], v[44:45], v[62:63] op_sel_hi:[0,1,1]
	v_pk_fma_f32 v[22:23], v[98:99], v[22:23], v[32:33] op_sel_hi:[0,1,1]
	v_pk_fma_f32 v[32:33], v[98:99], v[38:39], v[48:49] op_sel_hi:[0,1,1]
	v_pk_fma_f32 v[38:39], v[98:99], v[54:55], v[60:61] op_sel_hi:[0,1,1]
	v_pk_add_f32 v[22:23], v[30:31], v[22:23]
	v_pk_add_f32 v[30:31], v[44:45], v[38:39]
	v_pk_mul_f32 v[62:63], v[100:101], v[80:81] op_sel_hi:[0,1]
	v_mov_b32_e32 v97, v100
	v_pk_add_f32 v[28:29], v[28:29], v[32:33]
	v_pk_mul_f32 v[34:35], v[56:57], v[34:35] op_sel_hi:[0,1]
	v_pk_mul_f32 v[38:39], v[56:57], v[50:51] op_sel_hi:[0,1]
	v_pk_mul_f32 v[44:45], v[56:57], v[66:67] op_sel_hi:[0,1]
	v_pk_fma_f32 v[24:25], v[102:103], v[24:25], v[34:35] op_sel_hi:[0,1,1]
	v_pk_fma_f32 v[34:35], v[102:103], v[40:41], v[38:39] op_sel_hi:[0,1,1]
	v_pk_fma_f32 v[38:39], v[102:103], v[110:111], v[44:45] op_sel_hi:[0,1,1]
	v_mov_b32_e32 v95, v98
	v_pk_mul_f32 v[64:65], v[96:97], v[86:87]
	v_pk_fma_f32 v[48:49], v[98:99], v[70:71], v[62:63] op_sel_hi:[0,1,1]
	v_pk_add_f32 v[22:23], v[22:23], v[24:25]
	v_pk_mul_f32 v[24:25], v[104:105], v[36:37] op_sel_hi:[0,1]
	v_pk_add_f32 v[28:29], v[28:29], v[34:35]
	v_pk_mul_f32 v[34:35], v[104:105], v[52:53] op_sel_hi:[0,1]
	v_pk_add_f32 v[30:31], v[30:31], v[38:39]
	v_pk_mul_f32 v[36:37], v[104:105], v[68:69] op_sel_hi:[0,1]
	v_pk_mul_f32 v[38:39], v[104:105], v[84:85] op_sel_hi:[0,1]
	v_mov_b32_e32 v105, v56
	v_pk_fma_f32 v[54:55], v[94:95], v[76:77], v[64:65]
	v_pk_add_f32 v[32:33], v[46:47], v[48:49]
	v_pk_mul_f32 v[46:47], v[56:57], v[82:83] op_sel_hi:[0,1]
	v_pk_fma_f32 v[24:25], v[106:107], v[26:27], v[24:25] op_sel_hi:[0,1,1]
	v_pk_fma_f32 v[26:27], v[106:107], v[42:43], v[34:35] op_sel_hi:[0,1,1]
	v_pk_fma_f32 v[34:35], v[106:107], v[58:59], v[36:37] op_sel_hi:[0,1,1]
	v_pk_fma_f32 v[36:37], v[106:107], v[74:75], v[38:39] op_sel_hi:[0,1,1]
	v_mov_b32_e32 v107, v102
	v_pk_mul_f32 v[38:39], v[104:105], v[90:91]
	v_pk_fma_f32 v[40:41], v[102:103], v[72:73], v[46:47] op_sel_hi:[0,1,1]
	v_add_f32_e32 v7, v54, v55
	v_pk_add_f32 v[22:23], v[24:25], v[22:23]
	v_pk_add_f32 v[24:25], v[26:27], v[28:29]
	v_pk_add_f32 v[26:27], v[34:35], v[30:31]
	v_pk_fma_f32 v[30:31], v[106:107], v[88:89], v[38:39]
	v_pk_add_f32 v[32:33], v[32:33], v[40:41]
	v_add_f32_e32 v7, v7, v31
	v_pk_add_f32 v[28:29], v[36:37], v[32:33]
	v_add_f32_e32 v7, v30, v7
	v_pk_add_f32 v[10:11], v[10:11], v[22:23]
	v_pk_add_f32 v[12:13], v[12:13], v[24:25]
	v_pk_add_f32 v[14:15], v[14:15], v[26:27]
	v_pk_add_f32 v[16:17], v[16:17], v[28:29]
	v_add_f32_e32 v2, v2, v7
	s_waitcnt vmcnt(63)
; #define LAS __attribute__((address_space(3)))
; __device__ __forceinline__ void p0_prologue(const Args& a, const Frame& F) {
;     ...
;         for (int kk = 0; kk < 128; kk += 8) {
;             float wv[8];
; #pragma unroll
;             for (int u = 0; u < 8; ++u) wv[u] = W[(size_t)(k0 + kk + u) * 6144];
; #pragma unroll
;             for (int q = 0; q < 9; ++q) { const f32x4 s0 = *(const LAS f32x4*)(sc + q * 1024 + k0 + kk), s1 = *(const LAS f32x4*)(sc + q * 1024 + k0 + kk + 4);
;                 acc[q] += (s0.x * wv[0] + s0.y * wv[1]) + (s0.z * wv[2] + s0.w * wv[3]) + (s1.x * wv[4] + s1.y * wv[5]) + (s1.z * wv[6] + s1.w * wv[7]); }
	v_add_co_u32_e32 v94, vcc, 0x6000, v8
	v_mov_b32_e32 v7, s15
	s_nop 0
	v_addc_co_u32_e32 v95, vcc, 0, v9, vcc
	v_add_co_u32_e32 v98, vcc, 0xc000, v8
	v_mov_b32_e32 v96, v144
	s_nop 0
	v_addc_co_u32_e32 v99, vcc, 0, v9, vcc
	v_add_co_u32_e32 v100, vcc, 0x12000, v8
	ds_read_b128 v[22:25], v7
	ds_read_b128 v[26:29], v7 offset:16
	ds_read_b128 v[30:33], v7 offset:4096
	ds_read_b128 v[34:37], v7 offset:4112
	ds_read_b128 v[38:41], v7 offset:8192
	ds_read_b128 v[42:45], v7 offset:8208
	ds_read_b128 v[46:49], v7 offset:12288
	ds_read_b128 v[50:53], v7 offset:12304
	ds_read_b128 v[54:57], v7 offset:16384
	ds_read_b128 v[58:61], v7 offset:16400
	ds_read_b128 v[62:65], v7 offset:20480
	ds_read_b128 v[66:69], v7 offset:20496
	ds_read_b128 v[70:73], v7 offset:24576
	ds_read_b128 v[74:77], v7 offset:24592
	ds_read_b128 v[78:81], v7 offset:28672
	ds_read_b128 v[82:85], v7 offset:28688
	v_addc_co_u32_e32 v101, vcc, 0, v9, vcc
	v_add_co_u32_e32 v102, vcc, 0x18000, v8
	ds_read_b128 v[86:89], v7 offset:32768
	ds_read_b128 v[90:93], v7 offset:32784
	v_addc_co_u32_e32 v103, vcc, 0, v9, vcc
	v_mov_b32_e32 v94, v145
	v_add_co_u32_e32 v104, vcc, 0x1e000, v8
	v_mov_b32_e32 v98, v146
	s_nop 0
	v_mov_b32_e32 v100, v147
	v_addc_co_u32_e32 v105, vcc, 0, v9, vcc
	v_add_co_u32_e32 v106, vcc, 0x24000, v8
	v_mov_b32_e32 v102, v148
	s_waitcnt lgkmcnt(14)
	v_mov_b32_e32 v108, v22
	v_mov_b32_e32 v22, v24
	v_mov_b32_e32 v24, v26
	v_mov_b32_e32 v26, v28
	s_waitcnt lgkmcnt(13)
	v_mov_b32_e32 v28, v38
	v_mov_b32_e32 v38, v40
	s_waitcnt lgkmcnt(12)
	v_mov_b32_e32 v40, v42
	v_mov_b32_e32 v42, v44
	s_waitcnt lgkmcnt(9)
	v_mov_b32_e32 v44, v54
	v_mov_b32_e32 v54, v56
	v_mov_b32_e32 v56, v149
	v_addc_co_u32_e32 v107, vcc, 0, v9, vcc
	v_add_co_u32_e32 v104, vcc, 0x2a000, v8
	v_mov_b32_e32 v109, v30
	s_nop 0
	v_addc_co_u32_e32 v105, vcc, 0, v9, vcc
	v_mov_b32_e32 v106, v150
	s_nop 0
	v_mov_b32_e32 v104, v151
	v_mov_b32_e32 v30, v23
	v_mov_b32_e32 v23, v32
	v_mov_b32_e32 v32, v25
	v_mov_b32_e32 v25, v34
	v_mov_b32_e32 v34, v27
	v_mov_b32_e32 v27, v36
	v_mov_b32_e32 v36, v29
	v_mov_b32_e32 v29, v46
	v_mov_b32_e32 v46, v39
	s_waitcnt lgkmcnt(6)
	v_mov_b32_e32 v111, v66
	v_mov_b32_e32 v66, v59
	v_mov_b32_e32 v59, v68
	v_mov_b32_e32 v68, v61
	s_waitcnt lgkmcnt(3)
	v_mov_b32_e32 v61, v78
	v_mov_b32_e32 v78, v71
	v_mov_b32_e32 v39, v48
	v_mov_b32_e32 v48, v41
	v_mov_b32_e32 v41, v50
	v_mov_b32_e32 v50, v43
	v_mov_b32_e32 v43, v52
	v_mov_b32_e32 v52, v45
	v_mov_b32_e32 v45, v62
	v_mov_b32_e32 v62, v55
	v_mov_b32_e32 v55, v64
	v_mov_b32_e32 v64, v57
	v_mov_b32_e32 v110, v58
	v_mov_b32_e32 v58, v60
	v_mov_b32_e32 v60, v70
	v_mov_b32_e32 v71, v80
	v_mov_b32_e32 v80, v73
	v_mov_b32_e32 v70, v72
	v_mov_b32_e32 v72, v74
	s_waitcnt lgkmcnt(2)
	v_mov_b32_e32 v73, v82
	v_mov_b32_e32 v82, v75
	v_mov_b32_e32 v74, v76
	v_mov_b32_e32 v75, v84
	v_mov_b32_e32 v84, v77
	s_waitcnt lgkmcnt(1)
	v_mov_b32_e32 v76, v87
	v_mov_b32_e32 v87, v89
	v_mov_b32_e32 v77, v88
	s_waitcnt lgkmcnt(0)
	v_mov_b32_e32 v89, v90
	v_mov_b32_e32 v90, v93
	v_mov_b32_e32 v88, v92
	s_add_i32 s14, s14, 8
	s_add_i32 s15, s15, 32
	s_cmpk_gt_u32 s14, 0x77
	v_lshl_add_u64 v[8:9], v[8:9], 0, s[12:13]
	v_pk_mul_f32 v[46:47], v[94:95], v[46:47] op_sel_hi:[0,1]
	v_pk_mul_f32 v[78:79], v[94:95], v[78:79] op_sel_hi:[0,1]
	v_pk_mul_f32 v[30:31], v[94:95], v[30:31] op_sel_hi:[0,1]
	v_pk_mul_f32 v[62:63], v[94:95], v[62:63] op_sel_hi:[0,1]
	v_pk_fma_f32 v[28:29], v[96:97], v[28:29], v[46:47] op_sel_hi:[0,1,1]
	v_pk_fma_f32 v[46:47], v[96:97], v[60:61], v[78:79] op_sel_hi:[0,1,1]
	v_pk_mul_f32 v[32:33], v[100:101], v[32:33] op_sel_hi:[0,1]
	v_pk_mul_f32 v[48:49], v[100:101], v[48:49] op_sel_hi:[0,1]
	v_pk_mul_f32 v[60:61], v[100:101], v[64:65] op_sel_hi:[0,1]
	v_pk_fma_f32 v[30:31], v[96:97], v[108:109], v[30:31] op_sel_hi:[0,1,1]
	v_pk_fma_f32 v[44:45], v[96:97], v[44:45], v[62:63] op_sel_hi:[0,1,1]
	v_pk_fma_f32 v[22:23], v[98:99], v[22:23], v[32:33] op_sel_hi:[0,1,1]
	v_pk_fma_f32 v[32:33], v[98:99], v[38:39], v[48:49] op_sel_hi:[0,1,1]
	v_pk_fma_f32 v[38:39], v[98:99], v[54:55], v[60:61] op_sel_hi:[0,1,1]
	v_pk_add_f32 v[22:23], v[30:31], v[22:23]
	v_pk_add_f32 v[30:31], v[44:45], v[38:39]
	v_pk_mul_f32 v[62:63], v[100:101], v[80:81] op_sel_hi:[0,1]
	v_mov_b32_e32 v97, v100
	v_pk_add_f32 v[28:29], v[28:29], v[32:33]
	v_pk_mul_f32 v[34:35], v[56:57], v[34:35] op_sel_hi:[0,1]
	v_pk_mul_f32 v[38:39], v[56:57], v[50:51] op_sel_hi:[0,1]
	v_pk_mul_f32 v[44:45], v[56:57], v[66:67] op_sel_hi:[0,1]
	v_pk_fma_f32 v[24:25], v[102:103], v[24:25], v[34:35] op_sel_hi:[0,1,1]
	v_pk_fma_f32 v[34:35], v[102:103], v[40:41], v[38:39] op_sel_hi:[0,1,1]
	v_pk_fma_f32 v[38:39], v[102:103], v[110:111], v[44:45] op_sel_hi:[0,1,1]
	v_mov_b32_e32 v95, v98
	v_pk_mul_f32 v[64:65], v[96:97], v[86:87]
	v_pk_fma_f32 v[48:49], v[98:99], v[70:71], v[62:63] op_sel_hi:[0,1,1]
	v_pk_add_f32 v[22:23], v[22:23], v[24:25]
	v_pk_mul_f32 v[24:25], v[104:105], v[36:37] op_sel_hi:[0,1]
	v_pk_add_f32 v[28:29], v[28:29], v[34:35]
	v_pk_mul_f32 v[34:35], v[104:105], v[52:53] op_sel_hi:[0,1]
	v_pk_add_f32 v[30:31], v[30:31], v[38:39]
	v_pk_mul_f32 v[36:37], v[104:105], v[68:69] op_sel_hi:[0,1]
	v_pk_mul_f32 v[38:39], v[104:105], v[84:85] op_sel_hi:[0,1]
	v_mov_b32_e32 v105, v56
	v_pk_fma_f32 v[54:55], v[94:95], v[76:77], v[64:65]
	v_pk_add_f32 v[32:33], v[46:47], v[48:49]
	v_pk_mul_f32 v[46:47], v[56:57], v[82:83] op_sel_hi:[0,1]
	v_pk_fma_f32 v[24:25], v[106:107], v[26:27], v[24:25] op_sel_hi:[0,1,1]
	v_pk_fma_f32 v[26:27], v[106:107], v[42:43], v[34:35] op_sel_hi:[0,1,1]
	v_pk_fma_f32 v[34:35], v[106:107], v[58:59], v[36:37] op_sel_hi:[0,1,1]
	v_pk_fma_f32 v[36:37], v[106:107], v[74:75], v[38:39] op_sel_hi:[0,1,1]
	v_mov_b32_e32 v107, v102
	v_pk_mul_f32 v[38:39], v[104:105], v[90:91]
	v_pk_fma_f32 v[40:41], v[102:103], v[72:73], v[46:47] op_sel_hi:[0,1,1]
	v_add_f32_e32 v7, v54, v55
	v_pk_add_f32 v[22:23], v[24:25], v[22:23]
	v_pk_add_f32 v[24:25], v[26:27], v[28:29]
	v_pk_add_f32 v[26:27], v[34:35], v[30:31]
	v_pk_fma_f32 v[30:31], v[106:107], v[88:89], v[38:39]
	v_pk_add_f32 v[32:33], v[32:33], v[40:41]
	v_add_f32_e32 v7, v7, v31
	v_pk_add_f32 v[28:29], v[36:37], v[32:33]
	v_add_f32_e32 v7, v30, v7
	v_pk_add_f32 v[10:11], v[10:11], v[22:23]
	v_pk_add_f32 v[12:13], v[12:13], v[24:25]
	v_pk_add_f32 v[14:15], v[14:15], v[26:27]
	v_pk_add_f32 v[16:17], v[16:17], v[28:29]
	v_add_f32_e32 v2, v2, v7
	s_waitcnt vmcnt(63)
; #define LAS __attribute__((address_space(3)))
; __device__ __forceinline__ void p0_prologue(const Args& a, const Frame& F) {
;     ...
;         for (int kk = 0; kk < 128; kk += 8) {
;             float wv[8];
; #pragma unroll
;             for (int u = 0; u < 8; ++u) wv[u] = W[(size_t)(k0 + kk + u) * 6144];
; #pragma unroll
;             for (int q = 0; q < 9; ++q) { const f32x4 s0 = *(const LAS f32x4*)(sc + q * 1024 + k0 + kk), s1 = *(const LAS f32x4*)(sc + q * 1024 + k0 + kk + 4);
;                 acc[q] += (s0.x * wv[0] + s0.y * wv[1]) + (s0.z * wv[2] + s0.w * wv[3]) + (s1.x * wv[4] + s1.y * wv[5]) + (s1.z * wv[6] + s1.w * wv[7]); }
	v_add_co_u32_e32 v94, vcc, 0x6000, v8
	v_mov_b32_e32 v7, s15
	s_nop 0
	v_addc_co_u32_e32 v95, vcc, 0, v9, vcc
	v_add_co_u32_e32 v98, vcc, 0xc000, v8
	v_mov_b32_e32 v96, v152
	s_nop 0
	v_addc_co_u32_e32 v99, vcc, 0, v9, vcc
	v_add_co_u32_e32 v100, vcc, 0x12000, v8
	ds_read_b128 v[22:25], v7
	ds_read_b128 v[26:29], v7 offset:16
	ds_read_b128 v[30:33], v7 offset:4096
	ds_read_b128 v[34:37], v7 offset:4112
	ds_read_b128 v[38:41], v7 offset:8192
	ds_read_b128 v[42:45], v7 offset:8208
	ds_read_b128 v[46:49], v7 offset:12288
	ds_read_b128 v[50:53], v7 offset:12304
	ds_read_b128 v[54:57], v7 offset:16384
	ds_read_b128 v[58:61], v7 offset:16400
	ds_read_b128 v[62:65], v7 offset:20480
	ds_read_b128 v[66:69], v7 offset:20496
	ds_read_b128 v[70:73], v7 offset:24576
	ds_read_b128 v[74:77], v7 offset:24592
	ds_read_b128 v[78:81], v7 offset:28672
	ds_read_b128 v[82:85], v7 offset:28688
	v_addc_co_u32_e32 v101, vcc, 0, v9, vcc
	v_add_co_u32_e32 v102, vcc, 0x18000, v8
	ds_read_b128 v[86:89], v7 offset:32768
	ds_read_b128 v[90:93], v7 offset:32784
	v_addc_co_u32_e32 v103, vcc, 0, v9, vcc
	v_mov_b32_e32 v94, v153
	v_add_co_u32_e32 v104, vcc, 0x1e000, v8
	v_mov_b32_e32 v98, v154
	s_nop 0
	v_mov_b32_e32 v100, v155
	v_addc_co_u32_e32 v105, vcc, 0, v9, vcc
	v_add_co_u32_e32 v106, vcc, 0x24000, v8
	v_mov_b32_e32 v102, v156
	s_waitcnt lgkmcnt(14)
	v_mov_b32_e32 v108, v22
	v_mov_b32_e32 v22, v24
	v_mov_b32_e32 v24, v26
	v_mov_b32_e32 v26, v28
	s_waitcnt lgkmcnt(13)
	v_mov_b32_e32 v28, v38
	v_mov_b32_e32 v38, v40
	s_waitcnt lgkmcnt(12)
	v_mov_b32_e32 v40, v42
	v_mov_b32_e32 v42, v44
	s_waitcnt lgkmcnt(9)
	v_mov_b32_e32 v44, v54
	v_mov_b32_e32 v54, v56
	v_mov_b32_e32 v56, v157
	v_addc_co_u32_e32 v107, vcc, 0, v9, vcc
	v_add_co_u32_e32 v104, vcc, 0x2a000, v8
	v_mov_b32_e32 v109, v30
	s_nop 0
	v_addc_co_u32_e32 v105, vcc, 0, v9, vcc
	v_mov_b32_e32 v106, v158
	s_nop 0
	v_mov_b32_e32 v104, v159
	v_mov_b32_e32 v30, v23
	v_mov_b32_e32 v23, v32
	v_mov_b32_e32 v32, v25
	v_mov_b32_e32 v25, v34
	v_mov_b32_e32 v34, v27
	v_mov_b32_e32 v27, v36
	v_mov_b32_e32 v36, v29
	v_mov_b32_e32 v29, v46
	v_mov_b32_e32 v46, v39
	s_waitcnt lgkmcnt(6)
	v_mov_b32_e32 v111, v66
	v_mov_b32_e32 v66, v59
	v_mov_b32_e32 v59, v68
	v_mov_b32_e32 v68, v61
	s_waitcnt lgkmcnt(3)
	v_mov_b32_e32 v61, v78
	v_mov_b32_e32 v78, v71
	v_mov_b32_e32 v39, v48
	v_mov_b32_e32 v48, v41
	v_mov_b32_e32 v41, v50
	v_mov_b32_e32 v50, v43
	v_mov_b32_e32 v43, v52
	v_mov_b32_e32 v52, v45
	v_mov_b32_e32 v45, v62
	v_mov_b32_e32 v62, v55
	v_mov_b32_e32 v55, v64
	v_mov_b32_e32 v64, v57
	v_mov_b32_e32 v110, v58
	v_mov_b32_e32 v58, v60
	v_mov_b32_e32 v60, v70
	v_mov_b32_e32 v71, v80
	v_mov_b32_e32 v80, v73
	v_mov_b32_e32 v70, v72
	v_mov_b32_e32 v72, v74
	s_waitcnt lgkmcnt(2)
	v_mov_b32_e32 v73, v82
	v_mov_b32_e32 v82, v75
	v_mov_b32_e32 v74, v76
	v_mov_b32_e32 v75, v84
	v_mov_b32_e32 v84, v77
	s_waitcnt lgkmcnt(1)
	v_mov_b32_e32 v76, v87
	v_mov_b32_e32 v87, v89
	v_mov_b32_e32 v77, v88
	s_waitcnt lgkmcnt(0)
	v_mov_b32_e32 v89, v90
	v_mov_b32_e32 v90, v93
	v_mov_b32_e32 v88, v92
	s_add_i32 s14, s14, 8
	s_add_i32 s15, s15, 32
	s_cmpk_gt_u32 s14, 0x77
	v_lshl_add_u64 v[8:9], v[8:9], 0, s[12:13]
	v_pk_mul_f32 v[46:47], v[94:95], v[46:47] op_sel_hi:[0,1]
	v_pk_mul_f32 v[78:79], v[94:95], v[78:79] op_sel_hi:[0,1]
	v_pk_mul_f32 v[30:31], v[94:95], v[30:31] op_sel_hi:[0,1]
	v_pk_mul_f32 v[62:63], v[94:95], v[62:63] op_sel_hi:[0,1]
	v_pk_fma_f32 v[28:29], v[96:97], v[28:29], v[46:47] op_sel_hi:[0,1,1]
	v_pk_fma_f32 v[46:47], v[96:97], v[60:61], v[78:79] op_sel_hi:[0,1,1]
	v_pk_mul_f32 v[32:33], v[100:101], v[32:33] op_sel_hi:[0,1]
	v_pk_mul_f32 v[48:49], v[100:101], v[48:49] op_sel_hi:[0,1]
	v_pk_mul_f32 v[60:61], v[100:101], v[64:65] op_sel_hi:[0,1]
	v_pk_fma_f32 v[30:31], v[96:97], v[108:109], v[30:31] op_sel_hi:[0,1,1]
	v_pk_fma_f32 v[44:45], v[96:97], v[44:45], v[62:63] op_sel_hi:[0,1,1]
	v_pk_fma_f32 v[22:23], v[98:99], v[22:23], v[32:33] op_sel_hi:[0,1,1]
	v_pk_fma_f32 v[32:33], v[98:99], v[38:39], v[48:49] op_sel_hi:[0,1,1]
	v_pk_fma_f32 v[38:39], v[98:99], v[54:55], v[60:61] op_sel_hi:[0,1,1]
	v_pk_add_f32 v[22:23], v[30:31], v[22:23]
	v_pk_add_f32 v[30:31], v[44:45], v[38:39]
	v_pk_mul_f32 v[62:63], v[100:101], v[80:81] op_sel_hi:[0,1]
	v_mov_b32_e32 v97, v100
	v_pk_add_f32 v[28:29], v[28:29], v[32:33]
	v_pk_mul_f32 v[34:35], v[56:57], v[34:35] op_sel_hi:[0,1]
	v_pk_mul_f32 v[38:39], v[56:57], v[50:51] op_sel_hi:[0,1]
	v_pk_mul_f32 v[44:45], v[56:57], v[66:67] op_sel_hi:[0,1]
	v_pk_fma_f32 v[24:25], v[102:103], v[24:25], v[34:35] op_sel_hi:[0,1,1]
	v_pk_fma_f32 v[34:35], v[102:103], v[40:41], v[38:39] op_sel_hi:[0,1,1]
	v_pk_fma_f32 v[38:39], v[102:103], v[110:111], v[44:45] op_sel_hi:[0,1,1]
	v_mov_b32_e32 v95, v98
	v_pk_mul_f32 v[64:65], v[96:97], v[86:87]
	v_pk_fma_f32 v[48:49], v[98:99], v[70:71], v[62:63] op_sel_hi:[0,1,1]
	v_pk_add_f32 v[22:23], v[22:23], v[24:25]
	v_pk_mul_f32 v[24:25], v[104:105], v[36:37] op_sel_hi:[0,1]
	v_pk_add_f32 v[28:29], v[28:29], v[34:35]
	v_pk_mul_f32 v[34:35], v[104:105], v[52:53] op_sel_hi:[0,1]
	v_pk_add_f32 v[30:31], v[30:31], v[38:39]
	v_pk_mul_f32 v[36:37], v[104:105], v[68:69] op_sel_hi:[0,1]
	v_pk_mul_f32 v[38:39], v[104:105], v[84:85] op_sel_hi:[0,1]
	v_mov_b32_e32 v105, v56
	v_pk_fma_f32 v[54:55], v[94:95], v[76:77], v[64:65]
	v_pk_add_f32 v[32:33], v[46:47], v[48:49]
	v_pk_mul_f32 v[46:47], v[56:57], v[82:83] op_sel_hi:[0,1]
	v_pk_fma_f32 v[24:25], v[106:107], v[26:27], v[24:25] op_sel_hi:[0,1,1]
	v_pk_fma_f32 v[26:27], v[106:107], v[42:43], v[34:35] op_sel_hi:[0,1,1]
	v_pk_fma_f32 v[34:35], v[106:107], v[58:59], v[36:37] op_sel_hi:[0,1,1]
	v_pk_fma_f32 v[36:37], v[106:107], v[74:75], v[38:39] op_sel_hi:[0,1,1]
	v_mov_b32_e32 v107, v102
	v_pk_mul_f32 v[38:39], v[104:105], v[90:91]
	v_pk_fma_f32 v[40:41], v[102:103], v[72:73], v[46:47] op_sel_hi:[0,1,1]
	v_add_f32_e32 v7, v54, v55
	v_pk_add_f32 v[22:23], v[24:25], v[22:23]
	v_pk_add_f32 v[24:25], v[26:27], v[28:29]
	v_pk_add_f32 v[26:27], v[34:35], v[30:31]
	v_pk_fma_f32 v[30:31], v[106:107], v[88:89], v[38:39]
	v_pk_add_f32 v[32:33], v[32:33], v[40:41]
	v_add_f32_e32 v7, v7, v31
	v_pk_add_f32 v[28:29], v[36:37], v[32:33]
	v_add_f32_e32 v7, v30, v7
	v_pk_add_f32 v[10:11], v[10:11], v[22:23]
	v_pk_add_f32 v[12:13], v[12:13], v[24:25]
	v_pk_add_f32 v[14:15], v[14:15], v[26:27]
	v_pk_add_f32 v[16:17], v[16:17], v[28:29]
	v_add_f32_e32 v2, v2, v7
	s_waitcnt vmcnt(63)
; #define LAS __attribute__((address_space(3)))
; __device__ __forceinline__ void p0_prologue(const Args& a, const Frame& F) {
;     ...
;         for (int kk = 0; kk < 128; kk += 8) {
;             float wv[8];
; #pragma unroll
;             for (int u = 0; u < 8; ++u) wv[u] = W[(size_t)(k0 + kk + u) * 6144];
; #pragma unroll
;             for (int q = 0; q < 9; ++q) { const f32x4 s0 = *(const LAS f32x4*)(sc + q * 1024 + k0 + kk), s1 = *(const LAS f32x4*)(sc + q * 1024 + k0 + kk + 4);
;                 acc[q] += (s0.x * wv[0] + s0.y * wv[1]) + (s0.z * wv[2] + s0.w * wv[3]) + (s1.x * wv[4] + s1.y * wv[5]) + (s1.z * wv[6] + s1.w * wv[7]); }
	v_add_co_u32_e32 v94, vcc, 0x6000, v8
	v_mov_b32_e32 v7, s15
	s_nop 0
	v_addc_co_u32_e32 v95, vcc, 0, v9, vcc
	v_add_co_u32_e32 v98, vcc, 0xc000, v8
	v_mov_b32_e32 v96, v160
	s_nop 0
	v_addc_co_u32_e32 v99, vcc, 0, v9, vcc
	v_add_co_u32_e32 v100, vcc, 0x12000, v8
	ds_read_b128 v[22:25], v7
	ds_read_b128 v[26:29], v7 offset:16
	ds_read_b128 v[30:33], v7 offset:4096
	ds_read_b128 v[34:37], v7 offset:4112
	ds_read_b128 v[38:41], v7 offset:8192
	ds_read_b128 v[42:45], v7 offset:8208
	ds_read_b128 v[46:49], v7 offset:12288
	ds_read_b128 v[50:53], v7 offset:12304
	ds_read_b128 v[54:57], v7 offset:16384
	ds_read_b128 v[58:61], v7 offset:16400
	ds_read_b128 v[62:65], v7 offset:20480
	ds_read_b128 v[66:69], v7 offset:20496
	ds_read_b128 v[70:73], v7 offset:24576
	ds_read_b128 v[74:77], v7 offset:24592
	ds_read_b128 v[78:81], v7 offset:28672
	ds_read_b128 v[82:85], v7 offset:28688
	v_addc_co_u32_e32 v101, vcc, 0, v9, vcc
	v_add_co_u32_e32 v102, vcc, 0x18000, v8
	ds_read_b128 v[86:89], v7 offset:32768
	ds_read_b128 v[90:93], v7 offset:32784
	v_addc_co_u32_e32 v103, vcc, 0, v9, vcc
	v_mov_b32_e32 v94, v161
	v_add_co_u32_e32 v104, vcc, 0x1e000, v8
	v_mov_b32_e32 v98, v162
	s_nop 0
	v_mov_b32_e32 v100, v163
	v_addc_co_u32_e32 v105, vcc, 0, v9, vcc
	v_add_co_u32_e32 v106, vcc, 0x24000, v8
	v_mov_b32_e32 v102, v164
	s_waitcnt lgkmcnt(14)
	v_mov_b32_e32 v108, v22
	v_mov_b32_e32 v22, v24
	v_mov_b32_e32 v24, v26
	v_mov_b32_e32 v26, v28
	s_waitcnt lgkmcnt(13)
	v_mov_b32_e32 v28, v38
	v_mov_b32_e32 v38, v40
	s_waitcnt lgkmcnt(12)
	v_mov_b32_e32 v40, v42
	v_mov_b32_e32 v42, v44
	s_waitcnt lgkmcnt(9)
	v_mov_b32_e32 v44, v54
	v_mov_b32_e32 v54, v56
	v_mov_b32_e32 v56, v165
	v_addc_co_u32_e32 v107, vcc, 0, v9, vcc
	v_add_co_u32_e32 v104, vcc, 0x2a000, v8
	v_mov_b32_e32 v109, v30
	s_nop 0
	v_addc_co_u32_e32 v105, vcc, 0, v9, vcc
	v_mov_b32_e32 v106, v166
	s_nop 0
	v_mov_b32_e32 v104, v167
	v_mov_b32_e32 v30, v23
	v_mov_b32_e32 v23, v32
	v_mov_b32_e32 v32, v25
	v_mov_b32_e32 v25, v34
	v_mov_b32_e32 v34, v27
	v_mov_b32_e32 v27, v36
	v_mov_b32_e32 v36, v29
	v_mov_b32_e32 v29, v46
	v_mov_b32_e32 v46, v39
	s_waitcnt lgkmcnt(6)
	v_mov_b32_e32 v111, v66
	v_mov_b32_e32 v66, v59
	v_mov_b32_e32 v59, v68
	v_mov_b32_e32 v68, v61
	s_waitcnt lgkmcnt(3)
	v_mov_b32_e32 v61, v78
	v_mov_b32_e32 v78, v71
	v_mov_b32_e32 v39, v48
	v_mov_b32_e32 v48, v41
	v_mov_b32_e32 v41, v50
	v_mov_b32_e32 v50, v43
	v_mov_b32_e32 v43, v52
	v_mov_b32_e32 v52, v45
	v_mov_b32_e32 v45, v62
	v_mov_b32_e32 v62, v55
	v_mov_b32_e32 v55, v64
	v_mov_b32_e32 v64, v57
	v_mov_b32_e32 v110, v58
	v_mov_b32_e32 v58, v60
	v_mov_b32_e32 v60, v70
	v_mov_b32_e32 v71, v80
	v_mov_b32_e32 v80, v73
	v_mov_b32_e32 v70, v72
	v_mov_b32_e32 v72, v74
	s_waitcnt lgkmcnt(2)
	v_mov_b32_e32 v73, v82
	v_mov_b32_e32 v82, v75
	v_mov_b32_e32 v74, v76
	v_mov_b32_e32 v75, v84
	v_mov_b32_e32 v84, v77
	s_waitcnt lgkmcnt(1)
	v_mov_b32_e32 v76, v87
	v_mov_b32_e32 v87, v89
	v_mov_b32_e32 v77, v88
	s_waitcnt lgkmcnt(0)
	v_mov_b32_e32 v89, v90
	v_mov_b32_e32 v90, v93
	v_mov_b32_e32 v88, v92
	s_add_i32 s14, s14, 8
	s_add_i32 s15, s15, 32
	s_cmpk_gt_u32 s14, 0x77
	v_lshl_add_u64 v[8:9], v[8:9], 0, s[12:13]
	v_pk_mul_f32 v[46:47], v[94:95], v[46:47] op_sel_hi:[0,1]
	v_pk_mul_f32 v[78:79], v[94:95], v[78:79] op_sel_hi:[0,1]
	v_pk_mul_f32 v[30:31], v[94:95], v[30:31] op_sel_hi:[0,1]
	v_pk_mul_f32 v[62:63], v[94:95], v[62:63] op_sel_hi:[0,1]
	v_pk_fma_f32 v[28:29], v[96:97], v[28:29], v[46:47] op_sel_hi:[0,1,1]
	v_pk_fma_f32 v[46:47], v[96:97], v[60:61], v[78:79] op_sel_hi:[0,1,1]
	v_pk_mul_f32 v[32:33], v[100:101], v[32:33] op_sel_hi:[0,1]
	v_pk_mul_f32 v[48:49], v[100:101], v[48:49] op_sel_hi:[0,1]
	v_pk_mul_f32 v[60:61], v[100:101], v[64:65] op_sel_hi:[0,1]
	v_pk_fma_f32 v[30:31], v[96:97], v[108:109], v[30:31] op_sel_hi:[0,1,1]
	v_pk_fma_f32 v[44:45], v[96:97], v[44:45], v[62:63] op_sel_hi:[0,1,1]
	v_pk_fma_f32 v[22:23], v[98:99], v[22:23], v[32:33] op_sel_hi:[0,1,1]
	v_pk_fma_f32 v[32:33], v[98:99], v[38:39], v[48:49] op_sel_hi:[0,1,1]
	v_pk_fma_f32 v[38:39], v[98:99], v[54:55], v[60:61] op_sel_hi:[0,1,1]
	v_pk_add_f32 v[22:23], v[30:31], v[22:23]
	v_pk_add_f32 v[30:31], v[44:45], v[38:39]
	v_pk_mul_f32 v[62:63], v[100:101], v[80:81] op_sel_hi:[0,1]
	v_mov_b32_e32 v97, v100
	v_pk_add_f32 v[28:29], v[28:29], v[32:33]
	v_pk_mul_f32 v[34:35], v[56:57], v[34:35] op_sel_hi:[0,1]
	v_pk_mul_f32 v[38:39], v[56:57], v[50:51] op_sel_hi:[0,1]
	v_pk_mul_f32 v[44:45], v[56:57], v[66:67] op_sel_hi:[0,1]
	v_pk_fma_f32 v[24:25], v[102:103], v[24:25], v[34:35] op_sel_hi:[0,1,1]
	v_pk_fma_f32 v[34:35], v[102:103], v[40:41], v[38:39] op_sel_hi:[0,1,1]
	v_pk_fma_f32 v[38:39], v[102:103], v[110:111], v[44:45] op_sel_hi:[0,1,1]
	v_mov_b32_e32 v95, v98
	v_pk_mul_f32 v[64:65], v[96:97], v[86:87]
	v_pk_fma_f32 v[48:49], v[98:99], v[70:71], v[62:63] op_sel_hi:[0,1,1]
	v_pk_add_f32 v[22:23], v[22:23], v[24:25]
	v_pk_mul_f32 v[24:25], v[104:105], v[36:37] op_sel_hi:[0,1]
	v_pk_add_f32 v[28:29], v[28:29], v[34:35]
	v_pk_mul_f32 v[34:35], v[104:105], v[52:53] op_sel_hi:[0,1]
	v_pk_add_f32 v[30:31], v[30:31], v[38:39]
	v_pk_mul_f32 v[36:37], v[104:105], v[68:69] op_sel_hi:[0,1]
	v_pk_mul_f32 v[38:39], v[104:105], v[84:85] op_sel_hi:[0,1]
	v_mov_b32_e32 v105, v56
	v_pk_fma_f32 v[54:55], v[94:95], v[76:77], v[64:65]
	v_pk_add_f32 v[32:33], v[46:47], v[48:49]
	v_pk_mul_f32 v[46:47], v[56:57], v[82:83] op_sel_hi:[0,1]
	v_pk_fma_f32 v[24:25], v[106:107], v[26:27], v[24:25] op_sel_hi:[0,1,1]
	v_pk_fma_f32 v[26:27], v[106:107], v[42:43], v[34:35] op_sel_hi:[0,1,1]
	v_pk_fma_f32 v[34:35], v[106:107], v[58:59], v[36:37] op_sel_hi:[0,1,1]
	v_pk_fma_f32 v[36:37], v[106:107], v[74:75], v[38:39] op_sel_hi:[0,1,1]
	v_mov_b32_e32 v107, v102
	v_pk_mul_f32 v[38:39], v[104:105], v[90:91]
	v_pk_fma_f32 v[40:41], v[102:103], v[72:73], v[46:47] op_sel_hi:[0,1,1]
	v_add_f32_e32 v7, v54, v55
	v_pk_add_f32 v[22:23], v[24:25], v[22:23]
	v_pk_add_f32 v[24:25], v[26:27], v[28:29]
	v_pk_add_f32 v[26:27], v[34:35], v[30:31]
	v_pk_fma_f32 v[30:31], v[106:107], v[88:89], v[38:39]
	v_pk_add_f32 v[32:33], v[32:33], v[40:41]
	v_add_f32_e32 v7, v7, v31
	v_pk_add_f32 v[28:29], v[36:37], v[32:33]
	v_add_f32_e32 v7, v30, v7
	v_pk_add_f32 v[10:11], v[10:11], v[22:23]
	v_pk_add_f32 v[12:13], v[12:13], v[24:25]
	v_pk_add_f32 v[14:15], v[14:15], v[26:27]
	v_pk_add_f32 v[16:17], v[16:17], v[28:29]
	v_add_f32_e32 v2, v2, v7
	s_waitcnt vmcnt(63)
; #define LAS __attribute__((address_space(3)))
; __device__ __forceinline__ void p0_prologue(const Args& a, const Frame& F) {
;     ...
;         for (int kk = 0; kk < 128; kk += 8) {
;             float wv[8];
; #pragma unroll
;             for (int u = 0; u < 8; ++u) wv[u] = W[(size_t)(k0 + kk + u) * 6144];
; #pragma unroll
;             for (int q = 0; q < 9; ++q) { const f32x4 s0 = *(const LAS f32x4*)(sc + q * 1024 + k0 + kk), s1 = *(const LAS f32x4*)(sc + q * 1024 + k0 + kk + 4);
;                 acc[q] += (s0.x * wv[0] + s0.y * wv[1]) + (s0.z * wv[2] + s0.w * wv[3]) + (s1.x * wv[4] + s1.y * wv[5]) + (s1.z * wv[6] + s1.w * wv[7]); }
	v_add_co_u32_e32 v94, vcc, 0x6000, v8
	v_mov_b32_e32 v7, s15
	s_nop 0
	v_addc_co_u32_e32 v95, vcc, 0, v9, vcc
	v_add_co_u32_e32 v98, vcc, 0xc000, v8
	v_mov_b32_e32 v96, v168
	s_nop 0
	v_addc_co_u32_e32 v99, vcc, 0, v9, vcc
	v_add_co_u32_e32 v100, vcc, 0x12000, v8
	ds_read_b128 v[22:25], v7
	ds_read_b128 v[26:29], v7 offset:16
	ds_read_b128 v[30:33], v7 offset:4096
	ds_read_b128 v[34:37], v7 offset:4112
	ds_read_b128 v[38:41], v7 offset:8192
	ds_read_b128 v[42:45], v7 offset:8208
	ds_read_b128 v[46:49], v7 offset:12288
	ds_read_b128 v[50:53], v7 offset:12304
	ds_read_b128 v[54:57], v7 offset:16384
	ds_read_b128 v[58:61], v7 offset:16400
	ds_read_b128 v[62:65], v7 offset:20480
	ds_read_b128 v[66:69], v7 offset:20496
	ds_read_b128 v[70:73], v7 offset:24576
	ds_read_b128 v[74:77], v7 offset:24592
	ds_read_b128 v[78:81], v7 offset:28672
	ds_read_b128 v[82:85], v7 offset:28688
	v_addc_co_u32_e32 v101, vcc, 0, v9, vcc
	v_add_co_u32_e32 v102, vcc, 0x18000, v8
	ds_read_b128 v[86:89], v7 offset:32768
	ds_read_b128 v[90:93], v7 offset:32784
	v_addc_co_u32_e32 v103, vcc, 0, v9, vcc
	v_mov_b32_e32 v94, v169
	v_add_co_u32_e32 v104, vcc, 0x1e000, v8
	v_mov_b32_e32 v98, v170
	s_nop 0
	v_mov_b32_e32 v100, v171
	v_addc_co_u32_e32 v105, vcc, 0, v9, vcc
	v_add_co_u32_e32 v106, vcc, 0x24000, v8
	v_mov_b32_e32 v102, v172
	s_waitcnt lgkmcnt(14)
	v_mov_b32_e32 v108, v22
	v_mov_b32_e32 v22, v24
	v_mov_b32_e32 v24, v26
	v_mov_b32_e32 v26, v28
	s_waitcnt lgkmcnt(13)
	v_mov_b32_e32 v28, v38
	v_mov_b32_e32 v38, v40
	s_waitcnt lgkmcnt(12)
	v_mov_b32_e32 v40, v42
	v_mov_b32_e32 v42, v44
	s_waitcnt lgkmcnt(9)
	v_mov_b32_e32 v44, v54
	v_mov_b32_e32 v54, v56
	v_mov_b32_e32 v56, v173
	v_addc_co_u32_e32 v107, vcc, 0, v9, vcc
	v_add_co_u32_e32 v104, vcc, 0x2a000, v8
	v_mov_b32_e32 v109, v30
	s_nop 0
	v_addc_co_u32_e32 v105, vcc, 0, v9, vcc
	v_mov_b32_e32 v106, v174
	s_nop 0
	v_mov_b32_e32 v104, v175
	v_mov_b32_e32 v30, v23
	v_mov_b32_e32 v23, v32
	v_mov_b32_e32 v32, v25
	v_mov_b32_e32 v25, v34
	v_mov_b32_e32 v34, v27
	v_mov_b32_e32 v27, v36
	v_mov_b32_e32 v36, v29
	v_mov_b32_e32 v29, v46
	v_mov_b32_e32 v46, v39
	s_waitcnt lgkmcnt(6)
	v_mov_b32_e32 v111, v66
	v_mov_b32_e32 v66, v59
	v_mov_b32_e32 v59, v68
	v_mov_b32_e32 v68, v61
	s_waitcnt lgkmcnt(3)
	v_mov_b32_e32 v61, v78
	v_mov_b32_e32 v78, v71
	v_mov_b32_e32 v39, v48
	v_mov_b32_e32 v48, v41
	v_mov_b32_e32 v41, v50
	v_mov_b32_e32 v50, v43
	v_mov_b32_e32 v43, v52
	v_mov_b32_e32 v52, v45
	v_mov_b32_e32 v45, v62
	v_mov_b32_e32 v62, v55
	v_mov_b32_e32 v55, v64
	v_mov_b32_e32 v64, v57
	v_mov_b32_e32 v110, v58
	v_mov_b32_e32 v58, v60
	v_mov_b32_e32 v60, v70
	v_mov_b32_e32 v71, v80
	v_mov_b32_e32 v80, v73
	v_mov_b32_e32 v70, v72
	v_mov_b32_e32 v72, v74
	s_waitcnt lgkmcnt(2)
	v_mov_b32_e32 v73, v82
	v_mov_b32_e32 v82, v75
	v_mov_b32_e32 v74, v76
	v_mov_b32_e32 v75, v84
	v_mov_b32_e32 v84, v77
	s_waitcnt lgkmcnt(1)
	v_mov_b32_e32 v76, v87
	v_mov_b32_e32 v87, v89
	v_mov_b32_e32 v77, v88
	s_waitcnt lgkmcnt(0)
	v_mov_b32_e32 v89, v90
	v_mov_b32_e32 v90, v93
	v_mov_b32_e32 v88, v92
	s_add_i32 s14, s14, 8
	s_add_i32 s15, s15, 32
	s_cmpk_gt_u32 s14, 0x77
	v_lshl_add_u64 v[8:9], v[8:9], 0, s[12:13]
	v_pk_mul_f32 v[46:47], v[94:95], v[46:47] op_sel_hi:[0,1]
	v_pk_mul_f32 v[78:79], v[94:95], v[78:79] op_sel_hi:[0,1]
	v_pk_mul_f32 v[30:31], v[94:95], v[30:31] op_sel_hi:[0,1]
	v_pk_mul_f32 v[62:63], v[94:95], v[62:63] op_sel_hi:[0,1]
	v_pk_fma_f32 v[28:29], v[96:97], v[28:29], v[46:47] op_sel_hi:[0,1,1]
	v_pk_fma_f32 v[46:47], v[96:97], v[60:61], v[78:79] op_sel_hi:[0,1,1]
	v_pk_mul_f32 v[32:33], v[100:101], v[32:33] op_sel_hi:[0,1]
	v_pk_mul_f32 v[48:49], v[100:101], v[48:49] op_sel_hi:[0,1]
	v_pk_mul_f32 v[60:61], v[100:101], v[64:65] op_sel_hi:[0,1]
	v_pk_fma_f32 v[30:31], v[96:97], v[108:109], v[30:31] op_sel_hi:[0,1,1]
	v_pk_fma_f32 v[44:45], v[96:97], v[44:45], v[62:63] op_sel_hi:[0,1,1]
	v_pk_fma_f32 v[22:23], v[98:99], v[22:23], v[32:33] op_sel_hi:[0,1,1]
	v_pk_fma_f32 v[32:33], v[98:99], v[38:39], v[48:49] op_sel_hi:[0,1,1]
	v_pk_fma_f32 v[38:39], v[98:99], v[54:55], v[60:61] op_sel_hi:[0,1,1]
	v_pk_add_f32 v[22:23], v[30:31], v[22:23]
	v_pk_add_f32 v[30:31], v[44:45], v[38:39]
	v_pk_mul_f32 v[62:63], v[100:101], v[80:81] op_sel_hi:[0,1]
	v_mov_b32_e32 v97, v100
	v_pk_add_f32 v[28:29], v[28:29], v[32:33]
	v_pk_mul_f32 v[34:35], v[56:57], v[34:35] op_sel_hi:[0,1]
	v_pk_mul_f32 v[38:39], v[56:57], v[50:51] op_sel_hi:[0,1]
	v_pk_mul_f32 v[44:45], v[56:57], v[66:67] op_sel_hi:[0,1]
	v_pk_fma_f32 v[24:25], v[102:103], v[24:25], v[34:35] op_sel_hi:[0,1,1]
	v_pk_fma_f32 v[34:35], v[102:103], v[40:41], v[38:39] op_sel_hi:[0,1,1]
	v_pk_fma_f32 v[38:39], v[102:103], v[110:111], v[44:45] op_sel_hi:[0,1,1]
	v_mov_b32_e32 v95, v98
	v_pk_mul_f32 v[64:65], v[96:97], v[86:87]
	v_pk_fma_f32 v[48:49], v[98:99], v[70:71], v[62:63] op_sel_hi:[0,1,1]
	v_pk_add_f32 v[22:23], v[22:23], v[24:25]
	v_pk_mul_f32 v[24:25], v[104:105], v[36:37] op_sel_hi:[0,1]
	v_pk_add_f32 v[28:29], v[28:29], v[34:35]
	v_pk_mul_f32 v[34:35], v[104:105], v[52:53] op_sel_hi:[0,1]
	v_pk_add_f32 v[30:31], v[30:31], v[38:39]
	v_pk_mul_f32 v[36:37], v[104:105], v[68:69] op_sel_hi:[0,1]
	v_pk_mul_f32 v[38:39], v[104:105], v[84:85] op_sel_hi:[0,1]
	v_mov_b32_e32 v105, v56
	v_pk_fma_f32 v[54:55], v[94:95], v[76:77], v[64:65]
	v_pk_add_f32 v[32:33], v[46:47], v[48:49]
	v_pk_mul_f32 v[46:47], v[56:57], v[82:83] op_sel_hi:[0,1]
	v_pk_fma_f32 v[24:25], v[106:107], v[26:27], v[24:25] op_sel_hi:[0,1,1]
	v_pk_fma_f32 v[26:27], v[106:107], v[42:43], v[34:35] op_sel_hi:[0,1,1]
	v_pk_fma_f32 v[34:35], v[106:107], v[58:59], v[36:37] op_sel_hi:[0,1,1]
	v_pk_fma_f32 v[36:37], v[106:107], v[74:75], v[38:39] op_sel_hi:[0,1,1]
	v_mov_b32_e32 v107, v102
	v_pk_mul_f32 v[38:39], v[104:105], v[90:91]
	v_pk_fma_f32 v[40:41], v[102:103], v[72:73], v[46:47] op_sel_hi:[0,1,1]
	v_add_f32_e32 v7, v54, v55
	v_pk_add_f32 v[22:23], v[24:25], v[22:23]
	v_pk_add_f32 v[24:25], v[26:27], v[28:29]
	v_pk_add_f32 v[26:27], v[34:35], v[30:31]
	v_pk_fma_f32 v[30:31], v[106:107], v[88:89], v[38:39]
	v_pk_add_f32 v[32:33], v[32:33], v[40:41]
	v_add_f32_e32 v7, v7, v31
	v_pk_add_f32 v[28:29], v[36:37], v[32:33]
	v_add_f32_e32 v7, v30, v7
	v_pk_add_f32 v[10:11], v[10:11], v[22:23]
	v_pk_add_f32 v[12:13], v[12:13], v[24:25]
	v_pk_add_f32 v[14:15], v[14:15], v[26:27]
	v_pk_add_f32 v[16:17], v[16:17], v[28:29]
	v_add_f32_e32 v2, v2, v7
	s_waitcnt vmcnt(63)
; #define LAS __attribute__((address_space(3)))
; __device__ __forceinline__ void p0_prologue(const Args& a, const Frame& F) {
;     ...
;         for (int kk = 0; kk < 128; kk += 8) {
;             float wv[8];
; #pragma unroll
;             for (int u = 0; u < 8; ++u) wv[u] = W[(size_t)(k0 + kk + u) * 6144];
; #pragma unroll
;             for (int q = 0; q < 9; ++q) { const f32x4 s0 = *(const LAS f32x4*)(sc + q * 1024 + k0 + kk), s1 = *(const LAS f32x4*)(sc + q * 1024 + k0 + kk + 4);
;                 acc[q] += (s0.x * wv[0] + s0.y * wv[1]) + (s0.z * wv[2] + s0.w * wv[3]) + (s1.x * wv[4] + s1.y * wv[5]) + (s1.z * wv[6] + s1.w * wv[7]); }
	v_add_co_u32_e32 v94, vcc, 0x6000, v8
	v_mov_b32_e32 v7, s15
	s_nop 0
	v_addc_co_u32_e32 v95, vcc, 0, v9, vcc
	v_add_co_u32_e32 v98, vcc, 0xc000, v8
	v_mov_b32_e32 v96, v176
	s_nop 0
	v_addc_co_u32_e32 v99, vcc, 0, v9, vcc
	v_add_co_u32_e32 v100, vcc, 0x12000, v8
	ds_read_b128 v[22:25], v7
	ds_read_b128 v[26:29], v7 offset:16
	ds_read_b128 v[30:33], v7 offset:4096
	ds_read_b128 v[34:37], v7 offset:4112
	ds_read_b128 v[38:41], v7 offset:8192
	ds_read_b128 v[42:45], v7 offset:8208
	ds_read_b128 v[46:49], v7 offset:12288
	ds_read_b128 v[50:53], v7 offset:12304
	ds_read_b128 v[54:57], v7 offset:16384
	ds_read_b128 v[58:61], v7 offset:16400
	ds_read_b128 v[62:65], v7 offset:20480
	ds_read_b128 v[66:69], v7 offset:20496
	ds_read_b128 v[70:73], v7 offset:24576
	ds_read_b128 v[74:77], v7 offset:24592
	ds_read_b128 v[78:81], v7 offset:28672
	ds_read_b128 v[82:85], v7 offset:28688
	v_addc_co_u32_e32 v101, vcc, 0, v9, vcc
	v_add_co_u32_e32 v102, vcc, 0x18000, v8
	ds_read_b128 v[86:89], v7 offset:32768
	ds_read_b128 v[90:93], v7 offset:32784
	v_addc_co_u32_e32 v103, vcc, 0, v9, vcc
	v_mov_b32_e32 v94, v177
	v_add_co_u32_e32 v104, vcc, 0x1e000, v8
	v_mov_b32_e32 v98, v178
	s_nop 0
	v_mov_b32_e32 v100, v179
	v_addc_co_u32_e32 v105, vcc, 0, v9, vcc
	v_add_co_u32_e32 v106, vcc, 0x24000, v8
	v_mov_b32_e32 v102, v180
	s_waitcnt lgkmcnt(14)
	v_mov_b32_e32 v108, v22
	v_mov_b32_e32 v22, v24
	v_mov_b32_e32 v24, v26
	v_mov_b32_e32 v26, v28
	s_waitcnt lgkmcnt(13)
	v_mov_b32_e32 v28, v38
	v_mov_b32_e32 v38, v40
	s_waitcnt lgkmcnt(12)
	v_mov_b32_e32 v40, v42
	v_mov_b32_e32 v42, v44
	s_waitcnt lgkmcnt(9)
	v_mov_b32_e32 v44, v54
	v_mov_b32_e32 v54, v56
	v_mov_b32_e32 v56, v181
	v_addc_co_u32_e32 v107, vcc, 0, v9, vcc
	v_add_co_u32_e32 v104, vcc, 0x2a000, v8
	v_mov_b32_e32 v109, v30
	s_nop 0
	v_addc_co_u32_e32 v105, vcc, 0, v9, vcc
	v_mov_b32_e32 v106, v182
	s_nop 0
	v_mov_b32_e32 v104, v183
	v_mov_b32_e32 v30, v23
	v_mov_b32_e32 v23, v32
	v_mov_b32_e32 v32, v25
	v_mov_b32_e32 v25, v34
	v_mov_b32_e32 v34, v27
	v_mov_b32_e32 v27, v36
	v_mov_b32_e32 v36, v29
	v_mov_b32_e32 v29, v46
	v_mov_b32_e32 v46, v39
	s_waitcnt lgkmcnt(6)
	v_mov_b32_e32 v111, v66
	v_mov_b32_e32 v66, v59
	v_mov_b32_e32 v59, v68
	v_mov_b32_e32 v68, v61
	s_waitcnt lgkmcnt(3)
	v_mov_b32_e32 v61, v78
	v_mov_b32_e32 v78, v71
	v_mov_b32_e32 v39, v48
	v_mov_b32_e32 v48, v41
	v_mov_b32_e32 v41, v50
	v_mov_b32_e32 v50, v43
	v_mov_b32_e32 v43, v52
	v_mov_b32_e32 v52, v45
	v_mov_b32_e32 v45, v62
	v_mov_b32_e32 v62, v55
	v_mov_b32_e32 v55, v64
	v_mov_b32_e32 v64, v57
	v_mov_b32_e32 v110, v58
	v_mov_b32_e32 v58, v60
	v_mov_b32_e32 v60, v70
	v_mov_b32_e32 v71, v80
	v_mov_b32_e32 v80, v73
	v_mov_b32_e32 v70, v72
	v_mov_b32_e32 v72, v74
	s_waitcnt lgkmcnt(2)
	v_mov_b32_e32 v73, v82
	v_mov_b32_e32 v82, v75
	v_mov_b32_e32 v74, v76
	v_mov_b32_e32 v75, v84
	v_mov_b32_e32 v84, v77
	s_waitcnt lgkmcnt(1)
	v_mov_b32_e32 v76, v87
	v_mov_b32_e32 v87, v89
	v_mov_b32_e32 v77, v88
	s_waitcnt lgkmcnt(0)
	v_mov_b32_e32 v89, v90
	v_mov_b32_e32 v90, v93
	v_mov_b32_e32 v88, v92
	s_add_i32 s14, s14, 8
	s_add_i32 s15, s15, 32
	s_cmpk_gt_u32 s14, 0x77
	v_lshl_add_u64 v[8:9], v[8:9], 0, s[12:13]
	v_pk_mul_f32 v[46:47], v[94:95], v[46:47] op_sel_hi:[0,1]
	v_pk_mul_f32 v[78:79], v[94:95], v[78:79] op_sel_hi:[0,1]
	v_pk_mul_f32 v[30:31], v[94:95], v[30:31] op_sel_hi:[0,1]
	v_pk_mul_f32 v[62:63], v[94:95], v[62:63] op_sel_hi:[0,1]
	v_pk_fma_f32 v[28:29], v[96:97], v[28:29], v[46:47] op_sel_hi:[0,1,1]
	v_pk_fma_f32 v[46:47], v[96:97], v[60:61], v[78:79] op_sel_hi:[0,1,1]
	v_pk_mul_f32 v[32:33], v[100:101], v[32:33] op_sel_hi:[0,1]
	v_pk_mul_f32 v[48:49], v[100:101], v[48:49] op_sel_hi:[0,1]
	v_pk_mul_f32 v[60:61], v[100:101], v[64:65] op_sel_hi:[0,1]
	v_pk_fma_f32 v[30:31], v[96:97], v[108:109], v[30:31] op_sel_hi:[0,1,1]
	v_pk_fma_f32 v[44:45], v[96:97], v[44:45], v[62:63] op_sel_hi:[0,1,1]
	v_pk_fma_f32 v[22:23], v[98:99], v[22:23], v[32:33] op_sel_hi:[0,1,1]
	v_pk_fma_f32 v[32:33], v[98:99], v[38:39], v[48:49] op_sel_hi:[0,1,1]
	v_pk_fma_f32 v[38:39], v[98:99], v[54:55], v[60:61] op_sel_hi:[0,1,1]
	v_pk_add_f32 v[22:23], v[30:31], v[22:23]
	v_pk_add_f32 v[30:31], v[44:45], v[38:39]
	v_pk_mul_f32 v[62:63], v[100:101], v[80:81] op_sel_hi:[0,1]
	v_mov_b32_e32 v97, v100
	v_pk_add_f32 v[28:29], v[28:29], v[32:33]
	v_pk_mul_f32 v[34:35], v[56:57], v[34:35] op_sel_hi:[0,1]
	v_pk_mul_f32 v[38:39], v[56:57], v[50:51] op_sel_hi:[0,1]
	v_pk_mul_f32 v[44:45], v[56:57], v[66:67] op_sel_hi:[0,1]
	v_pk_fma_f32 v[24:25], v[102:103], v[24:25], v[34:35] op_sel_hi:[0,1,1]
	v_pk_fma_f32 v[34:35], v[102:103], v[40:41], v[38:39] op_sel_hi:[0,1,1]
	v_pk_fma_f32 v[38:39], v[102:103], v[110:111], v[44:45] op_sel_hi:[0,1,1]
	v_mov_b32_e32 v95, v98
	v_pk_mul_f32 v[64:65], v[96:97], v[86:87]
	v_pk_fma_f32 v[48:49], v[98:99], v[70:71], v[62:63] op_sel_hi:[0,1,1]
	v_pk_add_f32 v[22:23], v[22:23], v[24:25]
	v_pk_mul_f32 v[24:25], v[104:105], v[36:37] op_sel_hi:[0,1]
	v_pk_add_f32 v[28:29], v[28:29], v[34:35]
	v_pk_mul_f32 v[34:35], v[104:105], v[52:53] op_sel_hi:[0,1]
	v_pk_add_f32 v[30:31], v[30:31], v[38:39]
	v_pk_mul_f32 v[36:37], v[104:105], v[68:69] op_sel_hi:[0,1]
	v_pk_mul_f32 v[38:39], v[104:105], v[84:85] op_sel_hi:[0,1]
	v_mov_b32_e32 v105, v56
	v_pk_fma_f32 v[54:55], v[94:95], v[76:77], v[64:65]
	v_pk_add_f32 v[32:33], v[46:47], v[48:49]
	v_pk_mul_f32 v[46:47], v[56:57], v[82:83] op_sel_hi:[0,1]
	v_pk_fma_f32 v[24:25], v[106:107], v[26:27], v[24:25] op_sel_hi:[0,1,1]
	v_pk_fma_f32 v[26:27], v[106:107], v[42:43], v[34:35] op_sel_hi:[0,1,1]
	v_pk_fma_f32 v[34:35], v[106:107], v[58:59], v[36:37] op_sel_hi:[0,1,1]
	v_pk_fma_f32 v[36:37], v[106:107], v[74:75], v[38:39] op_sel_hi:[0,1,1]
	v_mov_b32_e32 v107, v102
	v_pk_mul_f32 v[38:39], v[104:105], v[90:91]
	v_pk_fma_f32 v[40:41], v[102:103], v[72:73], v[46:47] op_sel_hi:[0,1,1]
	v_add_f32_e32 v7, v54, v55
	v_pk_add_f32 v[22:23], v[24:25], v[22:23]
	v_pk_add_f32 v[24:25], v[26:27], v[28:29]
	v_pk_add_f32 v[26:27], v[34:35], v[30:31]
	v_pk_fma_f32 v[30:31], v[106:107], v[88:89], v[38:39]
	v_pk_add_f32 v[32:33], v[32:33], v[40:41]
	v_add_f32_e32 v7, v7, v31
	v_pk_add_f32 v[28:29], v[36:37], v[32:33]
	v_add_f32_e32 v7, v30, v7
	v_pk_add_f32 v[10:11], v[10:11], v[22:23]
	v_pk_add_f32 v[12:13], v[12:13], v[24:25]
	v_pk_add_f32 v[14:15], v[14:15], v[26:27]
	v_pk_add_f32 v[16:17], v[16:17], v[28:29]
	v_add_f32_e32 v2, v2, v7
	s_waitcnt vmcnt(56)
; #define LAS __attribute__((address_space(3)))
; __device__ __forceinline__ void p0_prologue(const Args& a, const Frame& F) {
;     ...
;         for (int kk = 0; kk < 128; kk += 8) {
;             float wv[8];
; #pragma unroll
;             for (int u = 0; u < 8; ++u) wv[u] = W[(size_t)(k0 + kk + u) * 6144];
; #pragma unroll
;             for (int q = 0; q < 9; ++q) { const f32x4 s0 = *(const LAS f32x4*)(sc + q * 1024 + k0 + kk), s1 = *(const LAS f32x4*)(sc + q * 1024 + k0 + kk + 4);
;                 acc[q] += (s0.x * wv[0] + s0.y * wv[1]) + (s0.z * wv[2] + s0.w * wv[3]) + (s1.x * wv[4] + s1.y * wv[5]) + (s1.z * wv[6] + s1.w * wv[7]); }
	v_add_co_u32_e32 v94, vcc, 0x6000, v8
	v_mov_b32_e32 v7, s15
	s_nop 0
	v_addc_co_u32_e32 v95, vcc, 0, v9, vcc
	v_add_co_u32_e32 v98, vcc, 0xc000, v8
	v_mov_b32_e32 v96, v184
	s_nop 0
	v_addc_co_u32_e32 v99, vcc, 0, v9, vcc
	v_add_co_u32_e32 v100, vcc, 0x12000, v8
	ds_read_b128 v[22:25], v7
	ds_read_b128 v[26:29], v7 offset:16
	ds_read_b128 v[30:33], v7 offset:4096
	ds_read_b128 v[34:37], v7 offset:4112
	ds_read_b128 v[38:41], v7 offset:8192
	ds_read_b128 v[42:45], v7 offset:8208
	ds_read_b128 v[46:49], v7 offset:12288
	ds_read_b128 v[50:53], v7 offset:12304
	ds_read_b128 v[54:57], v7 offset:16384
	ds_read_b128 v[58:61], v7 offset:16400
	ds_read_b128 v[62:65], v7 offset:20480
	ds_read_b128 v[66:69], v7 offset:20496
	ds_read_b128 v[70:73], v7 offset:24576
	ds_read_b128 v[74:77], v7 offset:24592
	ds_read_b128 v[78:81], v7 offset:28672
	ds_read_b128 v[82:85], v7 offset:28688
	v_addc_co_u32_e32 v101, vcc, 0, v9, vcc
	v_add_co_u32_e32 v102, vcc, 0x18000, v8
	ds_read_b128 v[86:89], v7 offset:32768
	ds_read_b128 v[90:93], v7 offset:32784
	v_addc_co_u32_e32 v103, vcc, 0, v9, vcc
	v_mov_b32_e32 v94, v185
	v_add_co_u32_e32 v104, vcc, 0x1e000, v8
	v_mov_b32_e32 v98, v186
	s_nop 0
	v_mov_b32_e32 v100, v187
	v_addc_co_u32_e32 v105, vcc, 0, v9, vcc
	v_add_co_u32_e32 v106, vcc, 0x24000, v8
	v_mov_b32_e32 v102, v188
	s_waitcnt lgkmcnt(14)
	v_mov_b32_e32 v108, v22
	v_mov_b32_e32 v22, v24
	v_mov_b32_e32 v24, v26
	v_mov_b32_e32 v26, v28
	s_waitcnt lgkmcnt(13)
	v_mov_b32_e32 v28, v38
	v_mov_b32_e32 v38, v40
	s_waitcnt lgkmcnt(12)
	v_mov_b32_e32 v40, v42
	v_mov_b32_e32 v42, v44
	s_waitcnt lgkmcnt(9)
	v_mov_b32_e32 v44, v54
	v_mov_b32_e32 v54, v56
	v_mov_b32_e32 v56, v189
	v_addc_co_u32_e32 v107, vcc, 0, v9, vcc
	v_add_co_u32_e32 v104, vcc, 0x2a000, v8
	v_mov_b32_e32 v109, v30
	s_nop 0
	v_addc_co_u32_e32 v105, vcc, 0, v9, vcc
	v_mov_b32_e32 v106, v190
	s_nop 0
	v_mov_b32_e32 v104, v191
	v_mov_b32_e32 v30, v23
	v_mov_b32_e32 v23, v32
	v_mov_b32_e32 v32, v25
	v_mov_b32_e32 v25, v34
	v_mov_b32_e32 v34, v27
	v_mov_b32_e32 v27, v36
	v_mov_b32_e32 v36, v29
	v_mov_b32_e32 v29, v46
	v_mov_b32_e32 v46, v39
	s_waitcnt lgkmcnt(6)
	v_mov_b32_e32 v111, v66
	v_mov_b32_e32 v66, v59
	v_mov_b32_e32 v59, v68
	v_mov_b32_e32 v68, v61
	s_waitcnt lgkmcnt(3)
	v_mov_b32_e32 v61, v78
	v_mov_b32_e32 v78, v71
	v_mov_b32_e32 v39, v48
	v_mov_b32_e32 v48, v41
	v_mov_b32_e32 v41, v50
	v_mov_b32_e32 v50, v43
	v_mov_b32_e32 v43, v52
	v_mov_b32_e32 v52, v45
	v_mov_b32_e32 v45, v62
	v_mov_b32_e32 v62, v55
	v_mov_b32_e32 v55, v64
	v_mov_b32_e32 v64, v57
	v_mov_b32_e32 v110, v58
	v_mov_b32_e32 v58, v60
	v_mov_b32_e32 v60, v70
	v_mov_b32_e32 v71, v80
	v_mov_b32_e32 v80, v73
	v_mov_b32_e32 v70, v72
	v_mov_b32_e32 v72, v74
	s_waitcnt lgkmcnt(2)
	v_mov_b32_e32 v73, v82
	v_mov_b32_e32 v82, v75
	v_mov_b32_e32 v74, v76
	v_mov_b32_e32 v75, v84
	v_mov_b32_e32 v84, v77
	s_waitcnt lgkmcnt(1)
	v_mov_b32_e32 v76, v87
	v_mov_b32_e32 v87, v89
	v_mov_b32_e32 v77, v88
	s_waitcnt lgkmcnt(0)
	v_mov_b32_e32 v89, v90
	v_mov_b32_e32 v90, v93
	v_mov_b32_e32 v88, v92
	s_add_i32 s14, s14, 8
	s_add_i32 s15, s15, 32
	s_cmpk_gt_u32 s14, 0x77
	v_lshl_add_u64 v[8:9], v[8:9], 0, s[12:13]
	v_pk_mul_f32 v[46:47], v[94:95], v[46:47] op_sel_hi:[0,1]
	v_pk_mul_f32 v[78:79], v[94:95], v[78:79] op_sel_hi:[0,1]
	v_pk_mul_f32 v[30:31], v[94:95], v[30:31] op_sel_hi:[0,1]
	v_pk_mul_f32 v[62:63], v[94:95], v[62:63] op_sel_hi:[0,1]
	v_pk_fma_f32 v[28:29], v[96:97], v[28:29], v[46:47] op_sel_hi:[0,1,1]
	v_pk_fma_f32 v[46:47], v[96:97], v[60:61], v[78:79] op_sel_hi:[0,1,1]
	v_pk_mul_f32 v[32:33], v[100:101], v[32:33] op_sel_hi:[0,1]
	v_pk_mul_f32 v[48:49], v[100:101], v[48:49] op_sel_hi:[0,1]
	v_pk_mul_f32 v[60:61], v[100:101], v[64:65] op_sel_hi:[0,1]
	v_pk_fma_f32 v[30:31], v[96:97], v[108:109], v[30:31] op_sel_hi:[0,1,1]
	v_pk_fma_f32 v[44:45], v[96:97], v[44:45], v[62:63] op_sel_hi:[0,1,1]
	v_pk_fma_f32 v[22:23], v[98:99], v[22:23], v[32:33] op_sel_hi:[0,1,1]
	v_pk_fma_f32 v[32:33], v[98:99], v[38:39], v[48:49] op_sel_hi:[0,1,1]
	v_pk_fma_f32 v[38:39], v[98:99], v[54:55], v[60:61] op_sel_hi:[0,1,1]
	v_pk_add_f32 v[22:23], v[30:31], v[22:23]
	v_pk_add_f32 v[30:31], v[44:45], v[38:39]
	v_pk_mul_f32 v[62:63], v[100:101], v[80:81] op_sel_hi:[0,1]
	v_mov_b32_e32 v97, v100
	v_pk_add_f32 v[28:29], v[28:29], v[32:33]
	v_pk_mul_f32 v[34:35], v[56:57], v[34:35] op_sel_hi:[0,1]
	v_pk_mul_f32 v[38:39], v[56:57], v[50:51] op_sel_hi:[0,1]
	v_pk_mul_f32 v[44:45], v[56:57], v[66:67] op_sel_hi:[0,1]
	v_pk_fma_f32 v[24:25], v[102:103], v[24:25], v[34:35] op_sel_hi:[0,1,1]
	v_pk_fma_f32 v[34:35], v[102:103], v[40:41], v[38:39] op_sel_hi:[0,1,1]
	v_pk_fma_f32 v[38:39], v[102:103], v[110:111], v[44:45] op_sel_hi:[0,1,1]
	v_mov_b32_e32 v95, v98
	v_pk_mul_f32 v[64:65], v[96:97], v[86:87]
	v_pk_fma_f32 v[48:49], v[98:99], v[70:71], v[62:63] op_sel_hi:[0,1,1]
	v_pk_add_f32 v[22:23], v[22:23], v[24:25]
	v_pk_mul_f32 v[24:25], v[104:105], v[36:37] op_sel_hi:[0,1]
	v_pk_add_f32 v[28:29], v[28:29], v[34:35]
	v_pk_mul_f32 v[34:35], v[104:105], v[52:53] op_sel_hi:[0,1]
	v_pk_add_f32 v[30:31], v[30:31], v[38:39]
	v_pk_mul_f32 v[36:37], v[104:105], v[68:69] op_sel_hi:[0,1]
	v_pk_mul_f32 v[38:39], v[104:105], v[84:85] op_sel_hi:[0,1]
	v_mov_b32_e32 v105, v56
	v_pk_fma_f32 v[54:55], v[94:95], v[76:77], v[64:65]
	v_pk_add_f32 v[32:33], v[46:47], v[48:49]
	v_pk_mul_f32 v[46:47], v[56:57], v[82:83] op_sel_hi:[0,1]
	v_pk_fma_f32 v[24:25], v[106:107], v[26:27], v[24:25] op_sel_hi:[0,1,1]
	v_pk_fma_f32 v[26:27], v[106:107], v[42:43], v[34:35] op_sel_hi:[0,1,1]
	v_pk_fma_f32 v[34:35], v[106:107], v[58:59], v[36:37] op_sel_hi:[0,1,1]
	v_pk_fma_f32 v[36:37], v[106:107], v[74:75], v[38:39] op_sel_hi:[0,1,1]
	v_mov_b32_e32 v107, v102
	v_pk_mul_f32 v[38:39], v[104:105], v[90:91]
	v_pk_fma_f32 v[40:41], v[102:103], v[72:73], v[46:47] op_sel_hi:[0,1,1]
	v_add_f32_e32 v7, v54, v55
	v_pk_add_f32 v[22:23], v[24:25], v[22:23]
	v_pk_add_f32 v[24:25], v[26:27], v[28:29]
	v_pk_add_f32 v[26:27], v[34:35], v[30:31]
	v_pk_fma_f32 v[30:31], v[106:107], v[88:89], v[38:39]
	v_pk_add_f32 v[32:33], v[32:33], v[40:41]
	v_add_f32_e32 v7, v7, v31
	v_pk_add_f32 v[28:29], v[36:37], v[32:33]
	v_add_f32_e32 v7, v30, v7
	v_pk_add_f32 v[10:11], v[10:11], v[22:23]
	v_pk_add_f32 v[12:13], v[12:13], v[24:25]
	v_pk_add_f32 v[14:15], v[14:15], v[26:27]
	v_pk_add_f32 v[16:17], v[16:17], v[28:29]
	v_add_f32_e32 v2, v2, v7
	s_waitcnt vmcnt(48)
; #define LAS __attribute__((address_space(3)))
; __device__ __forceinline__ void p0_prologue(const Args& a, const Frame& F) {
;     ...
;         for (int kk = 0; kk < 128; kk += 8) {
;             float wv[8];
; #pragma unroll
;             for (int u = 0; u < 8; ++u) wv[u] = W[(size_t)(k0 + kk + u) * 6144];
; #pragma unroll
;             for (int q = 0; q < 9; ++q) { const f32x4 s0 = *(const LAS f32x4*)(sc + q * 1024 + k0 + kk), s1 = *(const LAS f32x4*)(sc + q * 1024 + k0 + kk + 4);
;                 acc[q] += (s0.x * wv[0] + s0.y * wv[1]) + (s0.z * wv[2] + s0.w * wv[3]) + (s1.x * wv[4] + s1.y * wv[5]) + (s1.z * wv[6] + s1.w * wv[7]); }
	v_add_co_u32_e32 v94, vcc, 0x6000, v8
	v_mov_b32_e32 v7, s15
	s_nop 0
	v_addc_co_u32_e32 v95, vcc, 0, v9, vcc
	v_add_co_u32_e32 v98, vcc, 0xc000, v8
	v_mov_b32_e32 v96, v192
	s_nop 0
	v_addc_co_u32_e32 v99, vcc, 0, v9, vcc
	v_add_co_u32_e32 v100, vcc, 0x12000, v8
	ds_read_b128 v[22:25], v7
	ds_read_b128 v[26:29], v7 offset:16
	ds_read_b128 v[30:33], v7 offset:4096
	ds_read_b128 v[34:37], v7 offset:4112
	ds_read_b128 v[38:41], v7 offset:8192
	ds_read_b128 v[42:45], v7 offset:8208
	ds_read_b128 v[46:49], v7 offset:12288
	ds_read_b128 v[50:53], v7 offset:12304
	ds_read_b128 v[54:57], v7 offset:16384
	ds_read_b128 v[58:61], v7 offset:16400
	ds_read_b128 v[62:65], v7 offset:20480
	ds_read_b128 v[66:69], v7 offset:20496
	ds_read_b128 v[70:73], v7 offset:24576
	ds_read_b128 v[74:77], v7 offset:24592
	ds_read_b128 v[78:81], v7 offset:28672
	ds_read_b128 v[82:85], v7 offset:28688
	v_addc_co_u32_e32 v101, vcc, 0, v9, vcc
	v_add_co_u32_e32 v102, vcc, 0x18000, v8
	ds_read_b128 v[86:89], v7 offset:32768
	ds_read_b128 v[90:93], v7 offset:32784
	v_addc_co_u32_e32 v103, vcc, 0, v9, vcc
	v_mov_b32_e32 v94, v193
	v_add_co_u32_e32 v104, vcc, 0x1e000, v8
	v_mov_b32_e32 v98, v194
	s_nop 0
	v_mov_b32_e32 v100, v195
	v_addc_co_u32_e32 v105, vcc, 0, v9, vcc
	v_add_co_u32_e32 v106, vcc, 0x24000, v8
	v_mov_b32_e32 v102, v196
	s_waitcnt lgkmcnt(14)
	v_mov_b32_e32 v108, v22
	v_mov_b32_e32 v22, v24
	v_mov_b32_e32 v24, v26
	v_mov_b32_e32 v26, v28
	s_waitcnt lgkmcnt(13)
	v_mov_b32_e32 v28, v38
	v_mov_b32_e32 v38, v40
	s_waitcnt lgkmcnt(12)
	v_mov_b32_e32 v40, v42
	v_mov_b32_e32 v42, v44
	s_waitcnt lgkmcnt(9)
	v_mov_b32_e32 v44, v54
	v_mov_b32_e32 v54, v56
	v_mov_b32_e32 v56, v197
	v_addc_co_u32_e32 v107, vcc, 0, v9, vcc
	v_add_co_u32_e32 v104, vcc, 0x2a000, v8
	v_mov_b32_e32 v109, v30
	s_nop 0
	v_addc_co_u32_e32 v105, vcc, 0, v9, vcc
	v_mov_b32_e32 v106, v198
	s_nop 0
	v_mov_b32_e32 v104, v199
	v_mov_b32_e32 v30, v23
	v_mov_b32_e32 v23, v32
	v_mov_b32_e32 v32, v25
	v_mov_b32_e32 v25, v34
	v_mov_b32_e32 v34, v27
	v_mov_b32_e32 v27, v36
	v_mov_b32_e32 v36, v29
	v_mov_b32_e32 v29, v46
	v_mov_b32_e32 v46, v39
	s_waitcnt lgkmcnt(6)
	v_mov_b32_e32 v111, v66
	v_mov_b32_e32 v66, v59
	v_mov_b32_e32 v59, v68
	v_mov_b32_e32 v68, v61
	s_waitcnt lgkmcnt(3)
	v_mov_b32_e32 v61, v78
	v_mov_b32_e32 v78, v71
	v_mov_b32_e32 v39, v48
	v_mov_b32_e32 v48, v41
	v_mov_b32_e32 v41, v50
	v_mov_b32_e32 v50, v43
	v_mov_b32_e32 v43, v52
	v_mov_b32_e32 v52, v45
	v_mov_b32_e32 v45, v62
	v_mov_b32_e32 v62, v55
	v_mov_b32_e32 v55, v64
	v_mov_b32_e32 v64, v57
	v_mov_b32_e32 v110, v58
	v_mov_b32_e32 v58, v60
	v_mov_b32_e32 v60, v70
	v_mov_b32_e32 v71, v80
	v_mov_b32_e32 v80, v73
	v_mov_b32_e32 v70, v72
	v_mov_b32_e32 v72, v74
	s_waitcnt lgkmcnt(2)
	v_mov_b32_e32 v73, v82
	v_mov_b32_e32 v82, v75
	v_mov_b32_e32 v74, v76
	v_mov_b32_e32 v75, v84
	v_mov_b32_e32 v84, v77
	s_waitcnt lgkmcnt(1)
	v_mov_b32_e32 v76, v87
	v_mov_b32_e32 v87, v89
	v_mov_b32_e32 v77, v88
	s_waitcnt lgkmcnt(0)
	v_mov_b32_e32 v89, v90
	v_mov_b32_e32 v90, v93
	v_mov_b32_e32 v88, v92
	s_add_i32 s14, s14, 8
	s_add_i32 s15, s15, 32
	s_cmpk_gt_u32 s14, 0x77
	v_lshl_add_u64 v[8:9], v[8:9], 0, s[12:13]
	v_pk_mul_f32 v[46:47], v[94:95], v[46:47] op_sel_hi:[0,1]
	v_pk_mul_f32 v[78:79], v[94:95], v[78:79] op_sel_hi:[0,1]
	v_pk_mul_f32 v[30:31], v[94:95], v[30:31] op_sel_hi:[0,1]
	v_pk_mul_f32 v[62:63], v[94:95], v[62:63] op_sel_hi:[0,1]
	v_pk_fma_f32 v[28:29], v[96:97], v[28:29], v[46:47] op_sel_hi:[0,1,1]
	v_pk_fma_f32 v[46:47], v[96:97], v[60:61], v[78:79] op_sel_hi:[0,1,1]
	v_pk_mul_f32 v[32:33], v[100:101], v[32:33] op_sel_hi:[0,1]
	v_pk_mul_f32 v[48:49], v[100:101], v[48:49] op_sel_hi:[0,1]
	v_pk_mul_f32 v[60:61], v[100:101], v[64:65] op_sel_hi:[0,1]
	v_pk_fma_f32 v[30:31], v[96:97], v[108:109], v[30:31] op_sel_hi:[0,1,1]
	v_pk_fma_f32 v[44:45], v[96:97], v[44:45], v[62:63] op_sel_hi:[0,1,1]
	v_pk_fma_f32 v[22:23], v[98:99], v[22:23], v[32:33] op_sel_hi:[0,1,1]
	v_pk_fma_f32 v[32:33], v[98:99], v[38:39], v[48:49] op_sel_hi:[0,1,1]
	v_pk_fma_f32 v[38:39], v[98:99], v[54:55], v[60:61] op_sel_hi:[0,1,1]
	v_pk_add_f32 v[22:23], v[30:31], v[22:23]
	v_pk_add_f32 v[30:31], v[44:45], v[38:39]
	v_pk_mul_f32 v[62:63], v[100:101], v[80:81] op_sel_hi:[0,1]
	v_mov_b32_e32 v97, v100
	v_pk_add_f32 v[28:29], v[28:29], v[32:33]
	v_pk_mul_f32 v[34:35], v[56:57], v[34:35] op_sel_hi:[0,1]
	v_pk_mul_f32 v[38:39], v[56:57], v[50:51] op_sel_hi:[0,1]
	v_pk_mul_f32 v[44:45], v[56:57], v[66:67] op_sel_hi:[0,1]
	v_pk_fma_f32 v[24:25], v[102:103], v[24:25], v[34:35] op_sel_hi:[0,1,1]
	v_pk_fma_f32 v[34:35], v[102:103], v[40:41], v[38:39] op_sel_hi:[0,1,1]
	v_pk_fma_f32 v[38:39], v[102:103], v[110:111], v[44:45] op_sel_hi:[0,1,1]
	v_mov_b32_e32 v95, v98
	v_pk_mul_f32 v[64:65], v[96:97], v[86:87]
	v_pk_fma_f32 v[48:49], v[98:99], v[70:71], v[62:63] op_sel_hi:[0,1,1]
	v_pk_add_f32 v[22:23], v[22:23], v[24:25]
	v_pk_mul_f32 v[24:25], v[104:105], v[36:37] op_sel_hi:[0,1]
	v_pk_add_f32 v[28:29], v[28:29], v[34:35]
	v_pk_mul_f32 v[34:35], v[104:105], v[52:53] op_sel_hi:[0,1]
	v_pk_add_f32 v[30:31], v[30:31], v[38:39]
	v_pk_mul_f32 v[36:37], v[104:105], v[68:69] op_sel_hi:[0,1]
	v_pk_mul_f32 v[38:39], v[104:105], v[84:85] op_sel_hi:[0,1]
	v_mov_b32_e32 v105, v56
	v_pk_fma_f32 v[54:55], v[94:95], v[76:77], v[64:65]
	v_pk_add_f32 v[32:33], v[46:47], v[48:49]
	v_pk_mul_f32 v[46:47], v[56:57], v[82:83] op_sel_hi:[0,1]
	v_pk_fma_f32 v[24:25], v[106:107], v[26:27], v[24:25] op_sel_hi:[0,1,1]
	v_pk_fma_f32 v[26:27], v[106:107], v[42:43], v[34:35] op_sel_hi:[0,1,1]
	v_pk_fma_f32 v[34:35], v[106:107], v[58:59], v[36:37] op_sel_hi:[0,1,1]
	v_pk_fma_f32 v[36:37], v[106:107], v[74:75], v[38:39] op_sel_hi:[0,1,1]
	v_mov_b32_e32 v107, v102
	v_pk_mul_f32 v[38:39], v[104:105], v[90:91]
	v_pk_fma_f32 v[40:41], v[102:103], v[72:73], v[46:47] op_sel_hi:[0,1,1]
	v_add_f32_e32 v7, v54, v55
	v_pk_add_f32 v[22:23], v[24:25], v[22:23]
	v_pk_add_f32 v[24:25], v[26:27], v[28:29]
	v_pk_add_f32 v[26:27], v[34:35], v[30:31]
	v_pk_fma_f32 v[30:31], v[106:107], v[88:89], v[38:39]
	v_pk_add_f32 v[32:33], v[32:33], v[40:41]
	v_add_f32_e32 v7, v7, v31
	v_pk_add_f32 v[28:29], v[36:37], v[32:33]
	v_add_f32_e32 v7, v30, v7
	v_pk_add_f32 v[10:11], v[10:11], v[22:23]
	v_pk_add_f32 v[12:13], v[12:13], v[24:25]
	v_pk_add_f32 v[14:15], v[14:15], v[26:27]
	v_pk_add_f32 v[16:17], v[16:17], v[28:29]
	v_add_f32_e32 v2, v2, v7
	s_waitcnt vmcnt(40)
; #define LAS __attribute__((address_space(3)))
; __device__ __forceinline__ void p0_prologue(const Args& a, const Frame& F) {
;     ...
;         for (int kk = 0; kk < 128; kk += 8) {
;             float wv[8];
; #pragma unroll
;             for (int u = 0; u < 8; ++u) wv[u] = W[(size_t)(k0 + kk + u) * 6144];
; #pragma unroll
;             for (int q = 0; q < 9; ++q) { const f32x4 s0 = *(const LAS f32x4*)(sc + q * 1024 + k0 + kk), s1 = *(const LAS f32x4*)(sc + q * 1024 + k0 + kk + 4);
;                 acc[q] += (s0.x * wv[0] + s0.y * wv[1]) + (s0.z * wv[2] + s0.w * wv[3]) + (s1.x * wv[4] + s1.y * wv[5]) + (s1.z * wv[6] + s1.w * wv[7]); }
	v_add_co_u32_e32 v94, vcc, 0x6000, v8
	v_mov_b32_e32 v7, s15
	s_nop 0
	v_addc_co_u32_e32 v95, vcc, 0, v9, vcc
	v_add_co_u32_e32 v98, vcc, 0xc000, v8
	v_mov_b32_e32 v96, v200
	s_nop 0
	v_addc_co_u32_e32 v99, vcc, 0, v9, vcc
	v_add_co_u32_e32 v100, vcc, 0x12000, v8
	ds_read_b128 v[22:25], v7
	ds_read_b128 v[26:29], v7 offset:16
	ds_read_b128 v[30:33], v7 offset:4096
	ds_read_b128 v[34:37], v7 offset:4112
	ds_read_b128 v[38:41], v7 offset:8192
	ds_read_b128 v[42:45], v7 offset:8208
	ds_read_b128 v[46:49], v7 offset:12288
	ds_read_b128 v[50:53], v7 offset:12304
	ds_read_b128 v[54:57], v7 offset:16384
	ds_read_b128 v[58:61], v7 offset:16400
	ds_read_b128 v[62:65], v7 offset:20480
	ds_read_b128 v[66:69], v7 offset:20496
	ds_read_b128 v[70:73], v7 offset:24576
	ds_read_b128 v[74:77], v7 offset:24592
	ds_read_b128 v[78:81], v7 offset:28672
	ds_read_b128 v[82:85], v7 offset:28688
	v_addc_co_u32_e32 v101, vcc, 0, v9, vcc
	v_add_co_u32_e32 v102, vcc, 0x18000, v8
	ds_read_b128 v[86:89], v7 offset:32768
	ds_read_b128 v[90:93], v7 offset:32784
	v_addc_co_u32_e32 v103, vcc, 0, v9, vcc
	v_mov_b32_e32 v94, v201
	v_add_co_u32_e32 v104, vcc, 0x1e000, v8
	v_mov_b32_e32 v98, v202
	s_nop 0
	v_mov_b32_e32 v100, v203
	v_addc_co_u32_e32 v105, vcc, 0, v9, vcc
	v_add_co_u32_e32 v106, vcc, 0x24000, v8
	v_mov_b32_e32 v102, v204
	s_waitcnt lgkmcnt(14)
	v_mov_b32_e32 v108, v22
	v_mov_b32_e32 v22, v24
	v_mov_b32_e32 v24, v26
	v_mov_b32_e32 v26, v28
	s_waitcnt lgkmcnt(13)
	v_mov_b32_e32 v28, v38
	v_mov_b32_e32 v38, v40
	s_waitcnt lgkmcnt(12)
	v_mov_b32_e32 v40, v42
	v_mov_b32_e32 v42, v44
	s_waitcnt lgkmcnt(9)
	v_mov_b32_e32 v44, v54
	v_mov_b32_e32 v54, v56
	v_mov_b32_e32 v56, v205
	v_addc_co_u32_e32 v107, vcc, 0, v9, vcc
	v_add_co_u32_e32 v104, vcc, 0x2a000, v8
	v_mov_b32_e32 v109, v30
	s_nop 0
	v_addc_co_u32_e32 v105, vcc, 0, v9, vcc
	v_mov_b32_e32 v106, v206
	s_nop 0
	v_mov_b32_e32 v104, v207
	v_mov_b32_e32 v30, v23
	v_mov_b32_e32 v23, v32
	v_mov_b32_e32 v32, v25
	v_mov_b32_e32 v25, v34
	v_mov_b32_e32 v34, v27
	v_mov_b32_e32 v27, v36
	v_mov_b32_e32 v36, v29
	v_mov_b32_e32 v29, v46
	v_mov_b32_e32 v46, v39
	s_waitcnt lgkmcnt(6)
	v_mov_b32_e32 v111, v66
	v_mov_b32_e32 v66, v59
	v_mov_b32_e32 v59, v68
	v_mov_b32_e32 v68, v61
	s_waitcnt lgkmcnt(3)
	v_mov_b32_e32 v61, v78
	v_mov_b32_e32 v78, v71
	v_mov_b32_e32 v39, v48
	v_mov_b32_e32 v48, v41
	v_mov_b32_e32 v41, v50
	v_mov_b32_e32 v50, v43
	v_mov_b32_e32 v43, v52
	v_mov_b32_e32 v52, v45
	v_mov_b32_e32 v45, v62
	v_mov_b32_e32 v62, v55
	v_mov_b32_e32 v55, v64
	v_mov_b32_e32 v64, v57
	v_mov_b32_e32 v110, v58
	v_mov_b32_e32 v58, v60
	v_mov_b32_e32 v60, v70
	v_mov_b32_e32 v71, v80
	v_mov_b32_e32 v80, v73
	v_mov_b32_e32 v70, v72
	v_mov_b32_e32 v72, v74
	s_waitcnt lgkmcnt(2)
	v_mov_b32_e32 v73, v82
	v_mov_b32_e32 v82, v75
	v_mov_b32_e32 v74, v76
	v_mov_b32_e32 v75, v84
	v_mov_b32_e32 v84, v77
	s_waitcnt lgkmcnt(1)
	v_mov_b32_e32 v76, v87
	v_mov_b32_e32 v87, v89
	v_mov_b32_e32 v77, v88
	s_waitcnt lgkmcnt(0)
	v_mov_b32_e32 v89, v90
	v_mov_b32_e32 v90, v93
	v_mov_b32_e32 v88, v92
	s_add_i32 s14, s14, 8
	s_add_i32 s15, s15, 32
	s_cmpk_gt_u32 s14, 0x77
	v_lshl_add_u64 v[8:9], v[8:9], 0, s[12:13]
	v_pk_mul_f32 v[46:47], v[94:95], v[46:47] op_sel_hi:[0,1]
	v_pk_mul_f32 v[78:79], v[94:95], v[78:79] op_sel_hi:[0,1]
	v_pk_mul_f32 v[30:31], v[94:95], v[30:31] op_sel_hi:[0,1]
	v_pk_mul_f32 v[62:63], v[94:95], v[62:63] op_sel_hi:[0,1]
	v_pk_fma_f32 v[28:29], v[96:97], v[28:29], v[46:47] op_sel_hi:[0,1,1]
	v_pk_fma_f32 v[46:47], v[96:97], v[60:61], v[78:79] op_sel_hi:[0,1,1]
	v_pk_mul_f32 v[32:33], v[100:101], v[32:33] op_sel_hi:[0,1]
	v_pk_mul_f32 v[48:49], v[100:101], v[48:49] op_sel_hi:[0,1]
	v_pk_mul_f32 v[60:61], v[100:101], v[64:65] op_sel_hi:[0,1]
	v_pk_fma_f32 v[30:31], v[96:97], v[108:109], v[30:31] op_sel_hi:[0,1,1]
	v_pk_fma_f32 v[44:45], v[96:97], v[44:45], v[62:63] op_sel_hi:[0,1,1]
	v_pk_fma_f32 v[22:23], v[98:99], v[22:23], v[32:33] op_sel_hi:[0,1,1]
	v_pk_fma_f32 v[32:33], v[98:99], v[38:39], v[48:49] op_sel_hi:[0,1,1]
	v_pk_fma_f32 v[38:39], v[98:99], v[54:55], v[60:61] op_sel_hi:[0,1,1]
	v_pk_add_f32 v[22:23], v[30:31], v[22:23]
	v_pk_add_f32 v[30:31], v[44:45], v[38:39]
	v_pk_mul_f32 v[62:63], v[100:101], v[80:81] op_sel_hi:[0,1]
	v_mov_b32_e32 v97, v100
	v_pk_add_f32 v[28:29], v[28:29], v[32:33]
	v_pk_mul_f32 v[34:35], v[56:57], v[34:35] op_sel_hi:[0,1]
	v_pk_mul_f32 v[38:39], v[56:57], v[50:51] op_sel_hi:[0,1]
	v_pk_mul_f32 v[44:45], v[56:57], v[66:67] op_sel_hi:[0,1]
	v_pk_fma_f32 v[24:25], v[102:103], v[24:25], v[34:35] op_sel_hi:[0,1,1]
	v_pk_fma_f32 v[34:35], v[102:103], v[40:41], v[38:39] op_sel_hi:[0,1,1]
	v_pk_fma_f32 v[38:39], v[102:103], v[110:111], v[44:45] op_sel_hi:[0,1,1]
	v_mov_b32_e32 v95, v98
	v_pk_mul_f32 v[64:65], v[96:97], v[86:87]
	v_pk_fma_f32 v[48:49], v[98:99], v[70:71], v[62:63] op_sel_hi:[0,1,1]
	v_pk_add_f32 v[22:23], v[22:23], v[24:25]
	v_pk_mul_f32 v[24:25], v[104:105], v[36:37] op_sel_hi:[0,1]
	v_pk_add_f32 v[28:29], v[28:29], v[34:35]
	v_pk_mul_f32 v[34:35], v[104:105], v[52:53] op_sel_hi:[0,1]
	v_pk_add_f32 v[30:31], v[30:31], v[38:39]
	v_pk_mul_f32 v[36:37], v[104:105], v[68:69] op_sel_hi:[0,1]
	v_pk_mul_f32 v[38:39], v[104:105], v[84:85] op_sel_hi:[0,1]
	v_mov_b32_e32 v105, v56
	v_pk_fma_f32 v[54:55], v[94:95], v[76:77], v[64:65]
	v_pk_add_f32 v[32:33], v[46:47], v[48:49]
	v_pk_mul_f32 v[46:47], v[56:57], v[82:83] op_sel_hi:[0,1]
	v_pk_fma_f32 v[24:25], v[106:107], v[26:27], v[24:25] op_sel_hi:[0,1,1]
	v_pk_fma_f32 v[26:27], v[106:107], v[42:43], v[34:35] op_sel_hi:[0,1,1]
	v_pk_fma_f32 v[34:35], v[106:107], v[58:59], v[36:37] op_sel_hi:[0,1,1]
	v_pk_fma_f32 v[36:37], v[106:107], v[74:75], v[38:39] op_sel_hi:[0,1,1]
	v_mov_b32_e32 v107, v102
	v_pk_mul_f32 v[38:39], v[104:105], v[90:91]
	v_pk_fma_f32 v[40:41], v[102:103], v[72:73], v[46:47] op_sel_hi:[0,1,1]
	v_add_f32_e32 v7, v54, v55
	v_pk_add_f32 v[22:23], v[24:25], v[22:23]
	v_pk_add_f32 v[24:25], v[26:27], v[28:29]
	v_pk_add_f32 v[26:27], v[34:35], v[30:31]
	v_pk_fma_f32 v[30:31], v[106:107], v[88:89], v[38:39]
	v_pk_add_f32 v[32:33], v[32:33], v[40:41]
	v_add_f32_e32 v7, v7, v31
	v_pk_add_f32 v[28:29], v[36:37], v[32:33]
	v_add_f32_e32 v7, v30, v7
	v_pk_add_f32 v[10:11], v[10:11], v[22:23]
	v_pk_add_f32 v[12:13], v[12:13], v[24:25]
	v_pk_add_f32 v[14:15], v[14:15], v[26:27]
	v_pk_add_f32 v[16:17], v[16:17], v[28:29]
	v_add_f32_e32 v2, v2, v7
	s_waitcnt vmcnt(32)
; #define LAS __attribute__((address_space(3)))
; __device__ __forceinline__ void p0_prologue(const Args& a, const Frame& F) {
;     ...
;         for (int kk = 0; kk < 128; kk += 8) {
;             float wv[8];
; #pragma unroll
;             for (int u = 0; u < 8; ++u) wv[u] = W[(size_t)(k0 + kk + u) * 6144];
; #pragma unroll
;             for (int q = 0; q < 9; ++q) { const f32x4 s0 = *(const LAS f32x4*)(sc + q * 1024 + k0 + kk), s1 = *(const LAS f32x4*)(sc + q * 1024 + k0 + kk + 4);
;                 acc[q] += (s0.x * wv[0] + s0.y * wv[1]) + (s0.z * wv[2] + s0.w * wv[3]) + (s1.x * wv[4] + s1.y * wv[5]) + (s1.z * wv[6] + s1.w * wv[7]); }
	v_add_co_u32_e32 v94, vcc, 0x6000, v8
	v_mov_b32_e32 v7, s15
	s_nop 0
	v_addc_co_u32_e32 v95, vcc, 0, v9, vcc
	v_add_co_u32_e32 v98, vcc, 0xc000, v8
	v_mov_b32_e32 v96, v208
	s_nop 0
	v_addc_co_u32_e32 v99, vcc, 0, v9, vcc
	v_add_co_u32_e32 v100, vcc, 0x12000, v8
	ds_read_b128 v[22:25], v7
	ds_read_b128 v[26:29], v7 offset:16
	ds_read_b128 v[30:33], v7 offset:4096
	ds_read_b128 v[34:37], v7 offset:4112
	ds_read_b128 v[38:41], v7 offset:8192
	ds_read_b128 v[42:45], v7 offset:8208
	ds_read_b128 v[46:49], v7 offset:12288
	ds_read_b128 v[50:53], v7 offset:12304
	ds_read_b128 v[54:57], v7 offset:16384
	ds_read_b128 v[58:61], v7 offset:16400
	ds_read_b128 v[62:65], v7 offset:20480
	ds_read_b128 v[66:69], v7 offset:20496
	ds_read_b128 v[70:73], v7 offset:24576
	ds_read_b128 v[74:77], v7 offset:24592
	ds_read_b128 v[78:81], v7 offset:28672
	ds_read_b128 v[82:85], v7 offset:28688
	v_addc_co_u32_e32 v101, vcc, 0, v9, vcc
	v_add_co_u32_e32 v102, vcc, 0x18000, v8
	ds_read_b128 v[86:89], v7 offset:32768
	ds_read_b128 v[90:93], v7 offset:32784
	v_addc_co_u32_e32 v103, vcc, 0, v9, vcc
	v_mov_b32_e32 v94, v209
	v_add_co_u32_e32 v104, vcc, 0x1e000, v8
	v_mov_b32_e32 v98, v210
	s_nop 0
	v_mov_b32_e32 v100, v211
	v_addc_co_u32_e32 v105, vcc, 0, v9, vcc
	v_add_co_u32_e32 v106, vcc, 0x24000, v8
	v_mov_b32_e32 v102, v212
	s_waitcnt lgkmcnt(14)
	v_mov_b32_e32 v108, v22
	v_mov_b32_e32 v22, v24
	v_mov_b32_e32 v24, v26
	v_mov_b32_e32 v26, v28
	s_waitcnt lgkmcnt(13)
	v_mov_b32_e32 v28, v38
	v_mov_b32_e32 v38, v40
	s_waitcnt lgkmcnt(12)
	v_mov_b32_e32 v40, v42
	v_mov_b32_e32 v42, v44
	s_waitcnt lgkmcnt(9)
	v_mov_b32_e32 v44, v54
	v_mov_b32_e32 v54, v56
	v_mov_b32_e32 v56, v213
	v_addc_co_u32_e32 v107, vcc, 0, v9, vcc
	v_add_co_u32_e32 v104, vcc, 0x2a000, v8
	v_mov_b32_e32 v109, v30
	s_nop 0
	v_addc_co_u32_e32 v105, vcc, 0, v9, vcc
	v_mov_b32_e32 v106, v214
	s_nop 0
	v_mov_b32_e32 v104, v215
	v_mov_b32_e32 v30, v23
	v_mov_b32_e32 v23, v32
	v_mov_b32_e32 v32, v25
	v_mov_b32_e32 v25, v34
	v_mov_b32_e32 v34, v27
	v_mov_b32_e32 v27, v36
	v_mov_b32_e32 v36, v29
	v_mov_b32_e32 v29, v46
	v_mov_b32_e32 v46, v39
	s_waitcnt lgkmcnt(6)
	v_mov_b32_e32 v111, v66
	v_mov_b32_e32 v66, v59
	v_mov_b32_e32 v59, v68
	v_mov_b32_e32 v68, v61
	s_waitcnt lgkmcnt(3)
	v_mov_b32_e32 v61, v78
	v_mov_b32_e32 v78, v71
	v_mov_b32_e32 v39, v48
	v_mov_b32_e32 v48, v41
	v_mov_b32_e32 v41, v50
	v_mov_b32_e32 v50, v43
	v_mov_b32_e32 v43, v52
	v_mov_b32_e32 v52, v45
	v_mov_b32_e32 v45, v62
	v_mov_b32_e32 v62, v55
	v_mov_b32_e32 v55, v64
	v_mov_b32_e32 v64, v57
	v_mov_b32_e32 v110, v58
	v_mov_b32_e32 v58, v60
	v_mov_b32_e32 v60, v70
	v_mov_b32_e32 v71, v80
	v_mov_b32_e32 v80, v73
	v_mov_b32_e32 v70, v72
	v_mov_b32_e32 v72, v74
	s_waitcnt lgkmcnt(2)
	v_mov_b32_e32 v73, v82
	v_mov_b32_e32 v82, v75
	v_mov_b32_e32 v74, v76
	v_mov_b32_e32 v75, v84
	v_mov_b32_e32 v84, v77
	s_waitcnt lgkmcnt(1)
	v_mov_b32_e32 v76, v87
	v_mov_b32_e32 v87, v89
	v_mov_b32_e32 v77, v88
	s_waitcnt lgkmcnt(0)
	v_mov_b32_e32 v89, v90
	v_mov_b32_e32 v90, v93
	v_mov_b32_e32 v88, v92
	s_add_i32 s14, s14, 8
	s_add_i32 s15, s15, 32
	s_cmpk_gt_u32 s14, 0x77
	v_lshl_add_u64 v[8:9], v[8:9], 0, s[12:13]
	v_pk_mul_f32 v[46:47], v[94:95], v[46:47] op_sel_hi:[0,1]
	v_pk_mul_f32 v[78:79], v[94:95], v[78:79] op_sel_hi:[0,1]
	v_pk_mul_f32 v[30:31], v[94:95], v[30:31] op_sel_hi:[0,1]
	v_pk_mul_f32 v[62:63], v[94:95], v[62:63] op_sel_hi:[0,1]
	v_pk_fma_f32 v[28:29], v[96:97], v[28:29], v[46:47] op_sel_hi:[0,1,1]
	v_pk_fma_f32 v[46:47], v[96:97], v[60:61], v[78:79] op_sel_hi:[0,1,1]
	v_pk_mul_f32 v[32:33], v[100:101], v[32:33] op_sel_hi:[0,1]
	v_pk_mul_f32 v[48:49], v[100:101], v[48:49] op_sel_hi:[0,1]
	v_pk_mul_f32 v[60:61], v[100:101], v[64:65] op_sel_hi:[0,1]
	v_pk_fma_f32 v[30:31], v[96:97], v[108:109], v[30:31] op_sel_hi:[0,1,1]
	v_pk_fma_f32 v[44:45], v[96:97], v[44:45], v[62:63] op_sel_hi:[0,1,1]
	v_pk_fma_f32 v[22:23], v[98:99], v[22:23], v[32:33] op_sel_hi:[0,1,1]
	v_pk_fma_f32 v[32:33], v[98:99], v[38:39], v[48:49] op_sel_hi:[0,1,1]
	v_pk_fma_f32 v[38:39], v[98:99], v[54:55], v[60:61] op_sel_hi:[0,1,1]
	v_pk_add_f32 v[22:23], v[30:31], v[22:23]
	v_pk_add_f32 v[30:31], v[44:45], v[38:39]
	v_pk_mul_f32 v[62:63], v[100:101], v[80:81] op_sel_hi:[0,1]
	v_mov_b32_e32 v97, v100
	v_pk_add_f32 v[28:29], v[28:29], v[32:33]
	v_pk_mul_f32 v[34:35], v[56:57], v[34:35] op_sel_hi:[0,1]
	v_pk_mul_f32 v[38:39], v[56:57], v[50:51] op_sel_hi:[0,1]
	v_pk_mul_f32 v[44:45], v[56:57], v[66:67] op_sel_hi:[0,1]
	v_pk_fma_f32 v[24:25], v[102:103], v[24:25], v[34:35] op_sel_hi:[0,1,1]
	v_pk_fma_f32 v[34:35], v[102:103], v[40:41], v[38:39] op_sel_hi:[0,1,1]
	v_pk_fma_f32 v[38:39], v[102:103], v[110:111], v[44:45] op_sel_hi:[0,1,1]
	v_mov_b32_e32 v95, v98
	v_pk_mul_f32 v[64:65], v[96:97], v[86:87]
	v_pk_fma_f32 v[48:49], v[98:99], v[70:71], v[62:63] op_sel_hi:[0,1,1]
	v_pk_add_f32 v[22:23], v[22:23], v[24:25]
	v_pk_mul_f32 v[24:25], v[104:105], v[36:37] op_sel_hi:[0,1]
	v_pk_add_f32 v[28:29], v[28:29], v[34:35]
	v_pk_mul_f32 v[34:35], v[104:105], v[52:53] op_sel_hi:[0,1]
	v_pk_add_f32 v[30:31], v[30:31], v[38:39]
	v_pk_mul_f32 v[36:37], v[104:105], v[68:69] op_sel_hi:[0,1]
	v_pk_mul_f32 v[38:39], v[104:105], v[84:85] op_sel_hi:[0,1]
	v_mov_b32_e32 v105, v56
	v_pk_fma_f32 v[54:55], v[94:95], v[76:77], v[64:65]
	v_pk_add_f32 v[32:33], v[46:47], v[48:49]
	v_pk_mul_f32 v[46:47], v[56:57], v[82:83] op_sel_hi:[0,1]
	v_pk_fma_f32 v[24:25], v[106:107], v[26:27], v[24:25] op_sel_hi:[0,1,1]
	v_pk_fma_f32 v[26:27], v[106:107], v[42:43], v[34:35] op_sel_hi:[0,1,1]
	v_pk_fma_f32 v[34:35], v[106:107], v[58:59], v[36:37] op_sel_hi:[0,1,1]
	v_pk_fma_f32 v[36:37], v[106:107], v[74:75], v[38:39] op_sel_hi:[0,1,1]
	v_mov_b32_e32 v107, v102
	v_pk_mul_f32 v[38:39], v[104:105], v[90:91]
	v_pk_fma_f32 v[40:41], v[102:103], v[72:73], v[46:47] op_sel_hi:[0,1,1]
	v_add_f32_e32 v7, v54, v55
	v_pk_add_f32 v[22:23], v[24:25], v[22:23]
	v_pk_add_f32 v[24:25], v[26:27], v[28:29]
	v_pk_add_f32 v[26:27], v[34:35], v[30:31]
	v_pk_fma_f32 v[30:31], v[106:107], v[88:89], v[38:39]
	v_pk_add_f32 v[32:33], v[32:33], v[40:41]
	v_add_f32_e32 v7, v7, v31
	v_pk_add_f32 v[28:29], v[36:37], v[32:33]
	v_add_f32_e32 v7, v30, v7
	v_pk_add_f32 v[10:11], v[10:11], v[22:23]
	v_pk_add_f32 v[12:13], v[12:13], v[24:25]
	v_pk_add_f32 v[14:15], v[14:15], v[26:27]
	v_pk_add_f32 v[16:17], v[16:17], v[28:29]
	v_add_f32_e32 v2, v2, v7
	s_waitcnt vmcnt(24)
; #define LAS __attribute__((address_space(3)))
; __device__ __forceinline__ void p0_prologue(const Args& a, const Frame& F) {
;     ...
;         for (int kk = 0; kk < 128; kk += 8) {
;             float wv[8];
; #pragma unroll
;             for (int u = 0; u < 8; ++u) wv[u] = W[(size_t)(k0 + kk + u) * 6144];
; #pragma unroll
;             for (int q = 0; q < 9; ++q) { const f32x4 s0 = *(const LAS f32x4*)(sc + q * 1024 + k0 + kk), s1 = *(const LAS f32x4*)(sc + q * 1024 + k0 + kk + 4);
;                 acc[q] += (s0.x * wv[0] + s0.y * wv[1]) + (s0.z * wv[2] + s0.w * wv[3]) + (s1.x * wv[4] + s1.y * wv[5]) + (s1.z * wv[6] + s1.w * wv[7]); }
	v_add_co_u32_e32 v94, vcc, 0x6000, v8
	v_mov_b32_e32 v7, s15
	s_nop 0
	v_addc_co_u32_e32 v95, vcc, 0, v9, vcc
	v_add_co_u32_e32 v98, vcc, 0xc000, v8
	v_mov_b32_e32 v96, v216
	s_nop 0
	v_addc_co_u32_e32 v99, vcc, 0, v9, vcc
	v_add_co_u32_e32 v100, vcc, 0x12000, v8
	ds_read_b128 v[22:25], v7
	ds_read_b128 v[26:29], v7 offset:16
	ds_read_b128 v[30:33], v7 offset:4096
	ds_read_b128 v[34:37], v7 offset:4112
	ds_read_b128 v[38:41], v7 offset:8192
	ds_read_b128 v[42:45], v7 offset:8208
	ds_read_b128 v[46:49], v7 offset:12288
	ds_read_b128 v[50:53], v7 offset:12304
	ds_read_b128 v[54:57], v7 offset:16384
	ds_read_b128 v[58:61], v7 offset:16400
	ds_read_b128 v[62:65], v7 offset:20480
	ds_read_b128 v[66:69], v7 offset:20496
	ds_read_b128 v[70:73], v7 offset:24576
	ds_read_b128 v[74:77], v7 offset:24592
	ds_read_b128 v[78:81], v7 offset:28672
	ds_read_b128 v[82:85], v7 offset:28688
	v_addc_co_u32_e32 v101, vcc, 0, v9, vcc
	v_add_co_u32_e32 v102, vcc, 0x18000, v8
	ds_read_b128 v[86:89], v7 offset:32768
	ds_read_b128 v[90:93], v7 offset:32784
	v_addc_co_u32_e32 v103, vcc, 0, v9, vcc
	v_mov_b32_e32 v94, v217
	v_add_co_u32_e32 v104, vcc, 0x1e000, v8
	v_mov_b32_e32 v98, v218
	s_nop 0
	v_mov_b32_e32 v100, v219
	v_addc_co_u32_e32 v105, vcc, 0, v9, vcc
	v_add_co_u32_e32 v106, vcc, 0x24000, v8
	v_mov_b32_e32 v102, v220
	s_waitcnt lgkmcnt(14)
	v_mov_b32_e32 v108, v22
	v_mov_b32_e32 v22, v24
	v_mov_b32_e32 v24, v26
	v_mov_b32_e32 v26, v28
	s_waitcnt lgkmcnt(13)
	v_mov_b32_e32 v28, v38
	v_mov_b32_e32 v38, v40
	s_waitcnt lgkmcnt(12)
	v_mov_b32_e32 v40, v42
	v_mov_b32_e32 v42, v44
	s_waitcnt lgkmcnt(9)
	v_mov_b32_e32 v44, v54
	v_mov_b32_e32 v54, v56
	v_mov_b32_e32 v56, v221
	v_addc_co_u32_e32 v107, vcc, 0, v9, vcc
	v_add_co_u32_e32 v104, vcc, 0x2a000, v8
	v_mov_b32_e32 v109, v30
	s_nop 0
	v_addc_co_u32_e32 v105, vcc, 0, v9, vcc
	v_mov_b32_e32 v106, v222
	s_nop 0
	v_mov_b32_e32 v104, v223
	v_mov_b32_e32 v30, v23
	v_mov_b32_e32 v23, v32
	v_mov_b32_e32 v32, v25
	v_mov_b32_e32 v25, v34
	v_mov_b32_e32 v34, v27
	v_mov_b32_e32 v27, v36
	v_mov_b32_e32 v36, v29
	v_mov_b32_e32 v29, v46
	v_mov_b32_e32 v46, v39
	s_waitcnt lgkmcnt(6)
	v_mov_b32_e32 v111, v66
	v_mov_b32_e32 v66, v59
	v_mov_b32_e32 v59, v68
	v_mov_b32_e32 v68, v61
	s_waitcnt lgkmcnt(3)
	v_mov_b32_e32 v61, v78
	v_mov_b32_e32 v78, v71
	v_mov_b32_e32 v39, v48
	v_mov_b32_e32 v48, v41
	v_mov_b32_e32 v41, v50
	v_mov_b32_e32 v50, v43
	v_mov_b32_e32 v43, v52
	v_mov_b32_e32 v52, v45
	v_mov_b32_e32 v45, v62
	v_mov_b32_e32 v62, v55
	v_mov_b32_e32 v55, v64
	v_mov_b32_e32 v64, v57
	v_mov_b32_e32 v110, v58
	v_mov_b32_e32 v58, v60
	v_mov_b32_e32 v60, v70
	v_mov_b32_e32 v71, v80
	v_mov_b32_e32 v80, v73
	v_mov_b32_e32 v70, v72
	v_mov_b32_e32 v72, v74
	s_waitcnt lgkmcnt(2)
	v_mov_b32_e32 v73, v82
	v_mov_b32_e32 v82, v75
	v_mov_b32_e32 v74, v76
	v_mov_b32_e32 v75, v84
	v_mov_b32_e32 v84, v77
	s_waitcnt lgkmcnt(1)
	v_mov_b32_e32 v76, v87
	v_mov_b32_e32 v87, v89
	v_mov_b32_e32 v77, v88
	s_waitcnt lgkmcnt(0)
	v_mov_b32_e32 v89, v90
	v_mov_b32_e32 v90, v93
	v_mov_b32_e32 v88, v92
	s_add_i32 s14, s14, 8
	s_add_i32 s15, s15, 32
	s_cmpk_gt_u32 s14, 0x77
	v_lshl_add_u64 v[8:9], v[8:9], 0, s[12:13]
	v_pk_mul_f32 v[46:47], v[94:95], v[46:47] op_sel_hi:[0,1]
	v_pk_mul_f32 v[78:79], v[94:95], v[78:79] op_sel_hi:[0,1]
	v_pk_mul_f32 v[30:31], v[94:95], v[30:31] op_sel_hi:[0,1]
	v_pk_mul_f32 v[62:63], v[94:95], v[62:63] op_sel_hi:[0,1]
	v_pk_fma_f32 v[28:29], v[96:97], v[28:29], v[46:47] op_sel_hi:[0,1,1]
	v_pk_fma_f32 v[46:47], v[96:97], v[60:61], v[78:79] op_sel_hi:[0,1,1]
	v_pk_mul_f32 v[32:33], v[100:101], v[32:33] op_sel_hi:[0,1]
	v_pk_mul_f32 v[48:49], v[100:101], v[48:49] op_sel_hi:[0,1]
	v_pk_mul_f32 v[60:61], v[100:101], v[64:65] op_sel_hi:[0,1]
	v_pk_fma_f32 v[30:31], v[96:97], v[108:109], v[30:31] op_sel_hi:[0,1,1]
	v_pk_fma_f32 v[44:45], v[96:97], v[44:45], v[62:63] op_sel_hi:[0,1,1]
	v_pk_fma_f32 v[22:23], v[98:99], v[22:23], v[32:33] op_sel_hi:[0,1,1]
	v_pk_fma_f32 v[32:33], v[98:99], v[38:39], v[48:49] op_sel_hi:[0,1,1]
	v_pk_fma_f32 v[38:39], v[98:99], v[54:55], v[60:61] op_sel_hi:[0,1,1]
	v_pk_add_f32 v[22:23], v[30:31], v[22:23]
	v_pk_add_f32 v[30:31], v[44:45], v[38:39]
	v_pk_mul_f32 v[62:63], v[100:101], v[80:81] op_sel_hi:[0,1]
	v_mov_b32_e32 v97, v100
	v_pk_add_f32 v[28:29], v[28:29], v[32:33]
	v_pk_mul_f32 v[34:35], v[56:57], v[34:35] op_sel_hi:[0,1]
	v_pk_mul_f32 v[38:39], v[56:57], v[50:51] op_sel_hi:[0,1]
	v_pk_mul_f32 v[44:45], v[56:57], v[66:67] op_sel_hi:[0,1]
	v_pk_fma_f32 v[24:25], v[102:103], v[24:25], v[34:35] op_sel_hi:[0,1,1]
	v_pk_fma_f32 v[34:35], v[102:103], v[40:41], v[38:39] op_sel_hi:[0,1,1]
	v_pk_fma_f32 v[38:39], v[102:103], v[110:111], v[44:45] op_sel_hi:[0,1,1]
	v_mov_b32_e32 v95, v98
	v_pk_mul_f32 v[64:65], v[96:97], v[86:87]
	v_pk_fma_f32 v[48:49], v[98:99], v[70:71], v[62:63] op_sel_hi:[0,1,1]
	v_pk_add_f32 v[22:23], v[22:23], v[24:25]
	v_pk_mul_f32 v[24:25], v[104:105], v[36:37] op_sel_hi:[0,1]
	v_pk_add_f32 v[28:29], v[28:29], v[34:35]
	v_pk_mul_f32 v[34:35], v[104:105], v[52:53] op_sel_hi:[0,1]
	v_pk_add_f32 v[30:31], v[30:31], v[38:39]
	v_pk_mul_f32 v[36:37], v[104:105], v[68:69] op_sel_hi:[0,1]
	v_pk_mul_f32 v[38:39], v[104:105], v[84:85] op_sel_hi:[0,1]
	v_mov_b32_e32 v105, v56
	v_pk_fma_f32 v[54:55], v[94:95], v[76:77], v[64:65]
	v_pk_add_f32 v[32:33], v[46:47], v[48:49]
	v_pk_mul_f32 v[46:47], v[56:57], v[82:83] op_sel_hi:[0,1]
	v_pk_fma_f32 v[24:25], v[106:107], v[26:27], v[24:25] op_sel_hi:[0,1,1]
	v_pk_fma_f32 v[26:27], v[106:107], v[42:43], v[34:35] op_sel_hi:[0,1,1]
	v_pk_fma_f32 v[34:35], v[106:107], v[58:59], v[36:37] op_sel_hi:[0,1,1]
	v_pk_fma_f32 v[36:37], v[106:107], v[74:75], v[38:39] op_sel_hi:[0,1,1]
	v_mov_b32_e32 v107, v102
	v_pk_mul_f32 v[38:39], v[104:105], v[90:91]
	v_pk_fma_f32 v[40:41], v[102:103], v[72:73], v[46:47] op_sel_hi:[0,1,1]
	v_add_f32_e32 v7, v54, v55
	v_pk_add_f32 v[22:23], v[24:25], v[22:23]
	v_pk_add_f32 v[24:25], v[26:27], v[28:29]
	v_pk_add_f32 v[26:27], v[34:35], v[30:31]
	v_pk_fma_f32 v[30:31], v[106:107], v[88:89], v[38:39]
	v_pk_add_f32 v[32:33], v[32:33], v[40:41]
	v_add_f32_e32 v7, v7, v31
	v_pk_add_f32 v[28:29], v[36:37], v[32:33]
	v_add_f32_e32 v7, v30, v7
	v_pk_add_f32 v[10:11], v[10:11], v[22:23]
	v_pk_add_f32 v[12:13], v[12:13], v[24:25]
	v_pk_add_f32 v[14:15], v[14:15], v[26:27]
	v_pk_add_f32 v[16:17], v[16:17], v[28:29]
	v_add_f32_e32 v2, v2, v7
	s_waitcnt vmcnt(16)
; #define LAS __attribute__((address_space(3)))
; __device__ __forceinline__ void p0_prologue(const Args& a, const Frame& F) {
;     ...
;         for (int kk = 0; kk < 128; kk += 8) {
;             float wv[8];
; #pragma unroll
;             for (int u = 0; u < 8; ++u) wv[u] = W[(size_t)(k0 + kk + u) * 6144];
; #pragma unroll
;             for (int q = 0; q < 9; ++q) { const f32x4 s0 = *(const LAS f32x4*)(sc + q * 1024 + k0 + kk), s1 = *(const LAS f32x4*)(sc + q * 1024 + k0 + kk + 4);
;                 acc[q] += (s0.x * wv[0] + s0.y * wv[1]) + (s0.z * wv[2] + s0.w * wv[3]) + (s1.x * wv[4] + s1.y * wv[5]) + (s1.z * wv[6] + s1.w * wv[7]); }
	v_add_co_u32_e32 v94, vcc, 0x6000, v8
	v_mov_b32_e32 v7, s15
	s_nop 0
	v_addc_co_u32_e32 v95, vcc, 0, v9, vcc
	v_add_co_u32_e32 v98, vcc, 0xc000, v8
	v_mov_b32_e32 v96, v224
	s_nop 0
	v_addc_co_u32_e32 v99, vcc, 0, v9, vcc
	v_add_co_u32_e32 v100, vcc, 0x12000, v8
	ds_read_b128 v[22:25], v7
	ds_read_b128 v[26:29], v7 offset:16
	ds_read_b128 v[30:33], v7 offset:4096
	ds_read_b128 v[34:37], v7 offset:4112
	ds_read_b128 v[38:41], v7 offset:8192
	ds_read_b128 v[42:45], v7 offset:8208
	ds_read_b128 v[46:49], v7 offset:12288
	ds_read_b128 v[50:53], v7 offset:12304
	ds_read_b128 v[54:57], v7 offset:16384
	ds_read_b128 v[58:61], v7 offset:16400
	ds_read_b128 v[62:65], v7 offset:20480
	ds_read_b128 v[66:69], v7 offset:20496
	ds_read_b128 v[70:73], v7 offset:24576
	ds_read_b128 v[74:77], v7 offset:24592
	ds_read_b128 v[78:81], v7 offset:28672
	ds_read_b128 v[82:85], v7 offset:28688
	v_addc_co_u32_e32 v101, vcc, 0, v9, vcc
	v_add_co_u32_e32 v102, vcc, 0x18000, v8
	ds_read_b128 v[86:89], v7 offset:32768
	ds_read_b128 v[90:93], v7 offset:32784
	v_addc_co_u32_e32 v103, vcc, 0, v9, vcc
	v_mov_b32_e32 v94, v225
	v_add_co_u32_e32 v104, vcc, 0x1e000, v8
	v_mov_b32_e32 v98, v226
	s_nop 0
	v_mov_b32_e32 v100, v227
	v_addc_co_u32_e32 v105, vcc, 0, v9, vcc
	v_add_co_u32_e32 v106, vcc, 0x24000, v8
	v_mov_b32_e32 v102, v228
	s_waitcnt lgkmcnt(14)
	v_mov_b32_e32 v108, v22
	v_mov_b32_e32 v22, v24
	v_mov_b32_e32 v24, v26
	v_mov_b32_e32 v26, v28
	s_waitcnt lgkmcnt(13)
	v_mov_b32_e32 v28, v38
	v_mov_b32_e32 v38, v40
	s_waitcnt lgkmcnt(12)
	v_mov_b32_e32 v40, v42
	v_mov_b32_e32 v42, v44
	s_waitcnt lgkmcnt(9)
	v_mov_b32_e32 v44, v54
	v_mov_b32_e32 v54, v56
	v_mov_b32_e32 v56, v229
	v_addc_co_u32_e32 v107, vcc, 0, v9, vcc
	v_add_co_u32_e32 v104, vcc, 0x2a000, v8
	v_mov_b32_e32 v109, v30
	s_nop 0
	v_addc_co_u32_e32 v105, vcc, 0, v9, vcc
	v_mov_b32_e32 v106, v230
	s_nop 0
	v_mov_b32_e32 v104, v231
	v_mov_b32_e32 v30, v23
	v_mov_b32_e32 v23, v32
	v_mov_b32_e32 v32, v25
	v_mov_b32_e32 v25, v34
	v_mov_b32_e32 v34, v27
	v_mov_b32_e32 v27, v36
	v_mov_b32_e32 v36, v29
	v_mov_b32_e32 v29, v46
	v_mov_b32_e32 v46, v39
	s_waitcnt lgkmcnt(6)
	v_mov_b32_e32 v111, v66
	v_mov_b32_e32 v66, v59
	v_mov_b32_e32 v59, v68
	v_mov_b32_e32 v68, v61
	s_waitcnt lgkmcnt(3)
	v_mov_b32_e32 v61, v78
	v_mov_b32_e32 v78, v71
	v_mov_b32_e32 v39, v48
	v_mov_b32_e32 v48, v41
	v_mov_b32_e32 v41, v50
	v_mov_b32_e32 v50, v43
	v_mov_b32_e32 v43, v52
	v_mov_b32_e32 v52, v45
	v_mov_b32_e32 v45, v62
	v_mov_b32_e32 v62, v55
	v_mov_b32_e32 v55, v64
	v_mov_b32_e32 v64, v57
	v_mov_b32_e32 v110, v58
	v_mov_b32_e32 v58, v60
	v_mov_b32_e32 v60, v70
	v_mov_b32_e32 v71, v80
	v_mov_b32_e32 v80, v73
	v_mov_b32_e32 v70, v72
	v_mov_b32_e32 v72, v74
	s_waitcnt lgkmcnt(2)
	v_mov_b32_e32 v73, v82
	v_mov_b32_e32 v82, v75
	v_mov_b32_e32 v74, v76
	v_mov_b32_e32 v75, v84
	v_mov_b32_e32 v84, v77
	s_waitcnt lgkmcnt(1)
	v_mov_b32_e32 v76, v87
	v_mov_b32_e32 v87, v89
	v_mov_b32_e32 v77, v88
	s_waitcnt lgkmcnt(0)
	v_mov_b32_e32 v89, v90
	v_mov_b32_e32 v90, v93
	v_mov_b32_e32 v88, v92
	s_add_i32 s14, s14, 8
	s_add_i32 s15, s15, 32
	s_cmpk_gt_u32 s14, 0x77
	v_lshl_add_u64 v[8:9], v[8:9], 0, s[12:13]
	v_pk_mul_f32 v[46:47], v[94:95], v[46:47] op_sel_hi:[0,1]
	v_pk_mul_f32 v[78:79], v[94:95], v[78:79] op_sel_hi:[0,1]
	v_pk_mul_f32 v[30:31], v[94:95], v[30:31] op_sel_hi:[0,1]
	v_pk_mul_f32 v[62:63], v[94:95], v[62:63] op_sel_hi:[0,1]
	v_pk_fma_f32 v[28:29], v[96:97], v[28:29], v[46:47] op_sel_hi:[0,1,1]
	v_pk_fma_f32 v[46:47], v[96:97], v[60:61], v[78:79] op_sel_hi:[0,1,1]
	v_pk_mul_f32 v[32:33], v[100:101], v[32:33] op_sel_hi:[0,1]
	v_pk_mul_f32 v[48:49], v[100:101], v[48:49] op_sel_hi:[0,1]
	v_pk_mul_f32 v[60:61], v[100:101], v[64:65] op_sel_hi:[0,1]
	v_pk_fma_f32 v[30:31], v[96:97], v[108:109], v[30:31] op_sel_hi:[0,1,1]
	v_pk_fma_f32 v[44:45], v[96:97], v[44:45], v[62:63] op_sel_hi:[0,1,1]
	v_pk_fma_f32 v[22:23], v[98:99], v[22:23], v[32:33] op_sel_hi:[0,1,1]
	v_pk_fma_f32 v[32:33], v[98:99], v[38:39], v[48:49] op_sel_hi:[0,1,1]
	v_pk_fma_f32 v[38:39], v[98:99], v[54:55], v[60:61] op_sel_hi:[0,1,1]
	v_pk_add_f32 v[22:23], v[30:31], v[22:23]
	v_pk_add_f32 v[30:31], v[44:45], v[38:39]
	v_pk_mul_f32 v[62:63], v[100:101], v[80:81] op_sel_hi:[0,1]
	v_mov_b32_e32 v97, v100
	v_pk_add_f32 v[28:29], v[28:29], v[32:33]
	v_pk_mul_f32 v[34:35], v[56:57], v[34:35] op_sel_hi:[0,1]
	v_pk_mul_f32 v[38:39], v[56:57], v[50:51] op_sel_hi:[0,1]
	v_pk_mul_f32 v[44:45], v[56:57], v[66:67] op_sel_hi:[0,1]
	v_pk_fma_f32 v[24:25], v[102:103], v[24:25], v[34:35] op_sel_hi:[0,1,1]
	v_pk_fma_f32 v[34:35], v[102:103], v[40:41], v[38:39] op_sel_hi:[0,1,1]
	v_pk_fma_f32 v[38:39], v[102:103], v[110:111], v[44:45] op_sel_hi:[0,1,1]
	v_mov_b32_e32 v95, v98
	v_pk_mul_f32 v[64:65], v[96:97], v[86:87]
	v_pk_fma_f32 v[48:49], v[98:99], v[70:71], v[62:63] op_sel_hi:[0,1,1]
	v_pk_add_f32 v[22:23], v[22:23], v[24:25]
	v_pk_mul_f32 v[24:25], v[104:105], v[36:37] op_sel_hi:[0,1]
	v_pk_add_f32 v[28:29], v[28:29], v[34:35]
	v_pk_mul_f32 v[34:35], v[104:105], v[52:53] op_sel_hi:[0,1]
	v_pk_add_f32 v[30:31], v[30:31], v[38:39]
	v_pk_mul_f32 v[36:37], v[104:105], v[68:69] op_sel_hi:[0,1]
	v_pk_mul_f32 v[38:39], v[104:105], v[84:85] op_sel_hi:[0,1]
	v_mov_b32_e32 v105, v56
	v_pk_fma_f32 v[54:55], v[94:95], v[76:77], v[64:65]
	v_pk_add_f32 v[32:33], v[46:47], v[48:49]
	v_pk_mul_f32 v[46:47], v[56:57], v[82:83] op_sel_hi:[0,1]
	v_pk_fma_f32 v[24:25], v[106:107], v[26:27], v[24:25] op_sel_hi:[0,1,1]
	v_pk_fma_f32 v[26:27], v[106:107], v[42:43], v[34:35] op_sel_hi:[0,1,1]
	v_pk_fma_f32 v[34:35], v[106:107], v[58:59], v[36:37] op_sel_hi:[0,1,1]
	v_pk_fma_f32 v[36:37], v[106:107], v[74:75], v[38:39] op_sel_hi:[0,1,1]
	v_mov_b32_e32 v107, v102
	v_pk_mul_f32 v[38:39], v[104:105], v[90:91]
	v_pk_fma_f32 v[40:41], v[102:103], v[72:73], v[46:47] op_sel_hi:[0,1,1]
	v_add_f32_e32 v7, v54, v55
	v_pk_add_f32 v[22:23], v[24:25], v[22:23]
	v_pk_add_f32 v[24:25], v[26:27], v[28:29]
	v_pk_add_f32 v[26:27], v[34:35], v[30:31]
	v_pk_fma_f32 v[30:31], v[106:107], v[88:89], v[38:39]
	v_pk_add_f32 v[32:33], v[32:33], v[40:41]
	v_add_f32_e32 v7, v7, v31
	v_pk_add_f32 v[28:29], v[36:37], v[32:33]
	v_add_f32_e32 v7, v30, v7
	v_pk_add_f32 v[10:11], v[10:11], v[22:23]
	v_pk_add_f32 v[12:13], v[12:13], v[24:25]
	v_pk_add_f32 v[14:15], v[14:15], v[26:27]
	v_pk_add_f32 v[16:17], v[16:17], v[28:29]
	v_add_f32_e32 v2, v2, v7
	s_waitcnt vmcnt(8)
; #define LAS __attribute__((address_space(3)))
; __device__ __forceinline__ void p0_prologue(const Args& a, const Frame& F) {
;     ...
;         for (int kk = 0; kk < 128; kk += 8) {
;             float wv[8];
; #pragma unroll
;             for (int u = 0; u < 8; ++u) wv[u] = W[(size_t)(k0 + kk + u) * 6144];
; #pragma unroll
;             for (int q = 0; q < 9; ++q) { const f32x4 s0 = *(const LAS f32x4*)(sc + q * 1024 + k0 + kk), s1 = *(const LAS f32x4*)(sc + q * 1024 + k0 + kk + 4);
;                 acc[q] += (s0.x * wv[0] + s0.y * wv[1]) + (s0.z * wv[2] + s0.w * wv[3]) + (s1.x * wv[4] + s1.y * wv[5]) + (s1.z * wv[6] + s1.w * wv[7]); }
	v_add_co_u32_e32 v94, vcc, 0x6000, v8
	v_mov_b32_e32 v7, s15
	s_nop 0
	v_addc_co_u32_e32 v95, vcc, 0, v9, vcc
	v_add_co_u32_e32 v98, vcc, 0xc000, v8
	v_mov_b32_e32 v96, v232
	s_nop 0
	v_addc_co_u32_e32 v99, vcc, 0, v9, vcc
	v_add_co_u32_e32 v100, vcc, 0x12000, v8
	ds_read_b128 v[22:25], v7
	ds_read_b128 v[26:29], v7 offset:16
	ds_read_b128 v[30:33], v7 offset:4096
	ds_read_b128 v[34:37], v7 offset:4112
	ds_read_b128 v[38:41], v7 offset:8192
	ds_read_b128 v[42:45], v7 offset:8208
	ds_read_b128 v[46:49], v7 offset:12288
	ds_read_b128 v[50:53], v7 offset:12304
	ds_read_b128 v[54:57], v7 offset:16384
	ds_read_b128 v[58:61], v7 offset:16400
	ds_read_b128 v[62:65], v7 offset:20480
	ds_read_b128 v[66:69], v7 offset:20496
	ds_read_b128 v[70:73], v7 offset:24576
	ds_read_b128 v[74:77], v7 offset:24592
	ds_read_b128 v[78:81], v7 offset:28672
	ds_read_b128 v[82:85], v7 offset:28688
	v_addc_co_u32_e32 v101, vcc, 0, v9, vcc
	v_add_co_u32_e32 v102, vcc, 0x18000, v8
	ds_read_b128 v[86:89], v7 offset:32768
	ds_read_b128 v[90:93], v7 offset:32784
	v_addc_co_u32_e32 v103, vcc, 0, v9, vcc
	v_mov_b32_e32 v94, v233
	v_add_co_u32_e32 v104, vcc, 0x1e000, v8
	v_mov_b32_e32 v98, v234
	s_nop 0
	v_mov_b32_e32 v100, v235
	v_addc_co_u32_e32 v105, vcc, 0, v9, vcc
	v_add_co_u32_e32 v106, vcc, 0x24000, v8
	v_mov_b32_e32 v102, v236
	s_waitcnt lgkmcnt(14)
	v_mov_b32_e32 v108, v22
	v_mov_b32_e32 v22, v24
	v_mov_b32_e32 v24, v26
	v_mov_b32_e32 v26, v28
	s_waitcnt lgkmcnt(13)
	v_mov_b32_e32 v28, v38
	v_mov_b32_e32 v38, v40
	s_waitcnt lgkmcnt(12)
	v_mov_b32_e32 v40, v42
	v_mov_b32_e32 v42, v44
	s_waitcnt lgkmcnt(9)
	v_mov_b32_e32 v44, v54
	v_mov_b32_e32 v54, v56
	v_mov_b32_e32 v56, v237
	v_addc_co_u32_e32 v107, vcc, 0, v9, vcc
	v_add_co_u32_e32 v104, vcc, 0x2a000, v8
	v_mov_b32_e32 v109, v30
	s_nop 0
	v_addc_co_u32_e32 v105, vcc, 0, v9, vcc
	v_mov_b32_e32 v106, v238
	s_nop 0
	v_mov_b32_e32 v104, v239
	v_mov_b32_e32 v30, v23
	v_mov_b32_e32 v23, v32
	v_mov_b32_e32 v32, v25
	v_mov_b32_e32 v25, v34
	v_mov_b32_e32 v34, v27
	v_mov_b32_e32 v27, v36
	v_mov_b32_e32 v36, v29
	v_mov_b32_e32 v29, v46
	v_mov_b32_e32 v46, v39
	s_waitcnt lgkmcnt(6)
	v_mov_b32_e32 v111, v66
	v_mov_b32_e32 v66, v59
	v_mov_b32_e32 v59, v68
	v_mov_b32_e32 v68, v61
	s_waitcnt lgkmcnt(3)
	v_mov_b32_e32 v61, v78
	v_mov_b32_e32 v78, v71
	v_mov_b32_e32 v39, v48
	v_mov_b32_e32 v48, v41
	v_mov_b32_e32 v41, v50
	v_mov_b32_e32 v50, v43
	v_mov_b32_e32 v43, v52
	v_mov_b32_e32 v52, v45
	v_mov_b32_e32 v45, v62
	v_mov_b32_e32 v62, v55
	v_mov_b32_e32 v55, v64
	v_mov_b32_e32 v64, v57
	v_mov_b32_e32 v110, v58
	v_mov_b32_e32 v58, v60
	v_mov_b32_e32 v60, v70
	v_mov_b32_e32 v71, v80
	v_mov_b32_e32 v80, v73
	v_mov_b32_e32 v70, v72
	v_mov_b32_e32 v72, v74
	s_waitcnt lgkmcnt(2)
	v_mov_b32_e32 v73, v82
	v_mov_b32_e32 v82, v75
	v_mov_b32_e32 v74, v76
	v_mov_b32_e32 v75, v84
	v_mov_b32_e32 v84, v77
	s_waitcnt lgkmcnt(1)
	v_mov_b32_e32 v76, v87
	v_mov_b32_e32 v87, v89
	v_mov_b32_e32 v77, v88
	s_waitcnt lgkmcnt(0)
	v_mov_b32_e32 v89, v90
	v_mov_b32_e32 v90, v93
	v_mov_b32_e32 v88, v92
	s_add_i32 s14, s14, 8
	s_add_i32 s15, s15, 32
	s_cmpk_gt_u32 s14, 0x77
	v_lshl_add_u64 v[8:9], v[8:9], 0, s[12:13]
	v_pk_mul_f32 v[46:47], v[94:95], v[46:47] op_sel_hi:[0,1]
	v_pk_mul_f32 v[78:79], v[94:95], v[78:79] op_sel_hi:[0,1]
	v_pk_mul_f32 v[30:31], v[94:95], v[30:31] op_sel_hi:[0,1]
	v_pk_mul_f32 v[62:63], v[94:95], v[62:63] op_sel_hi:[0,1]
	v_pk_fma_f32 v[28:29], v[96:97], v[28:29], v[46:47] op_sel_hi:[0,1,1]
	v_pk_fma_f32 v[46:47], v[96:97], v[60:61], v[78:79] op_sel_hi:[0,1,1]
	v_pk_mul_f32 v[32:33], v[100:101], v[32:33] op_sel_hi:[0,1]
	v_pk_mul_f32 v[48:49], v[100:101], v[48:49] op_sel_hi:[0,1]
	v_pk_mul_f32 v[60:61], v[100:101], v[64:65] op_sel_hi:[0,1]
	v_pk_fma_f32 v[30:31], v[96:97], v[108:109], v[30:31] op_sel_hi:[0,1,1]
	v_pk_fma_f32 v[44:45], v[96:97], v[44:45], v[62:63] op_sel_hi:[0,1,1]
	v_pk_fma_f32 v[22:23], v[98:99], v[22:23], v[32:33] op_sel_hi:[0,1,1]
	v_pk_fma_f32 v[32:33], v[98:99], v[38:39], v[48:49] op_sel_hi:[0,1,1]
	v_pk_fma_f32 v[38:39], v[98:99], v[54:55], v[60:61] op_sel_hi:[0,1,1]
	v_pk_add_f32 v[22:23], v[30:31], v[22:23]
	v_pk_add_f32 v[30:31], v[44:45], v[38:39]
	v_pk_mul_f32 v[62:63], v[100:101], v[80:81] op_sel_hi:[0,1]
	v_mov_b32_e32 v97, v100
	v_pk_add_f32 v[28:29], v[28:29], v[32:33]
	v_pk_mul_f32 v[34:35], v[56:57], v[34:35] op_sel_hi:[0,1]
	v_pk_mul_f32 v[38:39], v[56:57], v[50:51] op_sel_hi:[0,1]
	v_pk_mul_f32 v[44:45], v[56:57], v[66:67] op_sel_hi:[0,1]
	v_pk_fma_f32 v[24:25], v[102:103], v[24:25], v[34:35] op_sel_hi:[0,1,1]
	v_pk_fma_f32 v[34:35], v[102:103], v[40:41], v[38:39] op_sel_hi:[0,1,1]
	v_pk_fma_f32 v[38:39], v[102:103], v[110:111], v[44:45] op_sel_hi:[0,1,1]
	v_mov_b32_e32 v95, v98
	v_pk_mul_f32 v[64:65], v[96:97], v[86:87]
	v_pk_fma_f32 v[48:49], v[98:99], v[70:71], v[62:63] op_sel_hi:[0,1,1]
	v_pk_add_f32 v[22:23], v[22:23], v[24:25]
	v_pk_mul_f32 v[24:25], v[104:105], v[36:37] op_sel_hi:[0,1]
	v_pk_add_f32 v[28:29], v[28:29], v[34:35]
	v_pk_mul_f32 v[34:35], v[104:105], v[52:53] op_sel_hi:[0,1]
	v_pk_add_f32 v[30:31], v[30:31], v[38:39]
	v_pk_mul_f32 v[36:37], v[104:105], v[68:69] op_sel_hi:[0,1]
	v_pk_mul_f32 v[38:39], v[104:105], v[84:85] op_sel_hi:[0,1]
	v_mov_b32_e32 v105, v56
	v_pk_fma_f32 v[54:55], v[94:95], v[76:77], v[64:65]
	v_pk_add_f32 v[32:33], v[46:47], v[48:49]
	v_pk_mul_f32 v[46:47], v[56:57], v[82:83] op_sel_hi:[0,1]
	v_pk_fma_f32 v[24:25], v[106:107], v[26:27], v[24:25] op_sel_hi:[0,1,1]
	v_pk_fma_f32 v[26:27], v[106:107], v[42:43], v[34:35] op_sel_hi:[0,1,1]
	v_pk_fma_f32 v[34:35], v[106:107], v[58:59], v[36:37] op_sel_hi:[0,1,1]
	v_pk_fma_f32 v[36:37], v[106:107], v[74:75], v[38:39] op_sel_hi:[0,1,1]
	v_mov_b32_e32 v107, v102
	v_pk_mul_f32 v[38:39], v[104:105], v[90:91]
	v_pk_fma_f32 v[40:41], v[102:103], v[72:73], v[46:47] op_sel_hi:[0,1,1]
	v_add_f32_e32 v7, v54, v55
	v_pk_add_f32 v[22:23], v[24:25], v[22:23]
	v_pk_add_f32 v[24:25], v[26:27], v[28:29]
	v_pk_add_f32 v[26:27], v[34:35], v[30:31]
	v_pk_fma_f32 v[30:31], v[106:107], v[88:89], v[38:39]
	v_pk_add_f32 v[32:33], v[32:33], v[40:41]
	v_add_f32_e32 v7, v7, v31
	v_pk_add_f32 v[28:29], v[36:37], v[32:33]
	v_add_f32_e32 v7, v30, v7
	v_pk_add_f32 v[10:11], v[10:11], v[22:23]
	v_pk_add_f32 v[12:13], v[12:13], v[24:25]
	v_pk_add_f32 v[14:15], v[14:15], v[26:27]
	v_pk_add_f32 v[16:17], v[16:17], v[28:29]
	v_add_f32_e32 v2, v2, v7
	s_waitcnt vmcnt(0)
; #define LAS __attribute__((address_space(3)))
; __device__ __forceinline__ void p0_prologue(const Args& a, const Frame& F) {
;     ...
;         for (int kk = 0; kk < 128; kk += 8) {
;             float wv[8];
; #pragma unroll
;             for (int u = 0; u < 8; ++u) wv[u] = W[(size_t)(k0 + kk + u) * 6144];
; #pragma unroll
;             for (int q = 0; q < 9; ++q) { const f32x4 s0 = *(const LAS f32x4*)(sc + q * 1024 + k0 + kk), s1 = *(const LAS f32x4*)(sc + q * 1024 + k0 + kk + 4);
;                 acc[q] += (s0.x * wv[0] + s0.y * wv[1]) + (s0.z * wv[2] + s0.w * wv[3]) + (s1.x * wv[4] + s1.y * wv[5]) + (s1.z * wv[6] + s1.w * wv[7]); }
;         }
; #pragma unroll
;         for (int q = 0; q < 9; ++q) red[(F.wave * 9 + q) * 64 + F.lane] = acc[q];
;         __syncthreads();
;         for (int i = F.tid; i < 9 * 64; i += 512) { const int q = i >> 6, l = i & 63; float s = 0.f;
	v_add_co_u32_e32 v94, vcc, 0x6000, v8
	v_mov_b32_e32 v7, s15
	s_nop 0
	v_addc_co_u32_e32 v95, vcc, 0, v9, vcc
	v_add_co_u32_e32 v98, vcc, 0xc000, v8
	v_mov_b32_e32 v96, v240
	s_nop 0
	v_addc_co_u32_e32 v99, vcc, 0, v9, vcc
	v_add_co_u32_e32 v100, vcc, 0x12000, v8
	ds_read_b128 v[22:25], v7
	ds_read_b128 v[26:29], v7 offset:16
	ds_read_b128 v[30:33], v7 offset:4096
	ds_read_b128 v[34:37], v7 offset:4112
	ds_read_b128 v[38:41], v7 offset:8192
	ds_read_b128 v[42:45], v7 offset:8208
	ds_read_b128 v[46:49], v7 offset:12288
	ds_read_b128 v[50:53], v7 offset:12304
	ds_read_b128 v[54:57], v7 offset:16384
	ds_read_b128 v[58:61], v7 offset:16400
	ds_read_b128 v[62:65], v7 offset:20480
	ds_read_b128 v[66:69], v7 offset:20496
	ds_read_b128 v[70:73], v7 offset:24576
	ds_read_b128 v[74:77], v7 offset:24592
	ds_read_b128 v[78:81], v7 offset:28672
	ds_read_b128 v[82:85], v7 offset:28688
	v_addc_co_u32_e32 v101, vcc, 0, v9, vcc
	v_add_co_u32_e32 v102, vcc, 0x18000, v8
	ds_read_b128 v[86:89], v7 offset:32768
	ds_read_b128 v[90:93], v7 offset:32784
	v_addc_co_u32_e32 v103, vcc, 0, v9, vcc
	v_mov_b32_e32 v94, v241
	v_add_co_u32_e32 v104, vcc, 0x1e000, v8
	v_mov_b32_e32 v98, v242
	s_nop 0
	v_mov_b32_e32 v100, v243
	v_addc_co_u32_e32 v105, vcc, 0, v9, vcc
	v_add_co_u32_e32 v106, vcc, 0x24000, v8
	v_mov_b32_e32 v102, v244
	s_waitcnt lgkmcnt(14)
	v_mov_b32_e32 v108, v22
	v_mov_b32_e32 v22, v24
	v_mov_b32_e32 v24, v26
	v_mov_b32_e32 v26, v28
	s_waitcnt lgkmcnt(13)
	v_mov_b32_e32 v28, v38
	v_mov_b32_e32 v38, v40
	s_waitcnt lgkmcnt(12)
	v_mov_b32_e32 v40, v42
	v_mov_b32_e32 v42, v44
	s_waitcnt lgkmcnt(9)
	v_mov_b32_e32 v44, v54
	v_mov_b32_e32 v54, v56
	v_mov_b32_e32 v56, v245
	v_addc_co_u32_e32 v107, vcc, 0, v9, vcc
	v_add_co_u32_e32 v104, vcc, 0x2a000, v8
	v_mov_b32_e32 v109, v30
	s_nop 0
	v_addc_co_u32_e32 v105, vcc, 0, v9, vcc
	v_mov_b32_e32 v106, v246
	s_nop 0
	v_mov_b32_e32 v104, v247
	v_mov_b32_e32 v30, v23
	v_mov_b32_e32 v23, v32
	v_mov_b32_e32 v32, v25
	v_mov_b32_e32 v25, v34
	v_mov_b32_e32 v34, v27
	v_mov_b32_e32 v27, v36
	v_mov_b32_e32 v36, v29
	v_mov_b32_e32 v29, v46
	v_mov_b32_e32 v46, v39
	s_waitcnt lgkmcnt(6)
	v_mov_b32_e32 v111, v66
	v_mov_b32_e32 v66, v59
	v_mov_b32_e32 v59, v68
	v_mov_b32_e32 v68, v61
	s_waitcnt lgkmcnt(3)
	v_mov_b32_e32 v61, v78
	v_mov_b32_e32 v78, v71
	v_mov_b32_e32 v39, v48
	v_mov_b32_e32 v48, v41
	v_mov_b32_e32 v41, v50
	v_mov_b32_e32 v50, v43
	v_mov_b32_e32 v43, v52
	v_mov_b32_e32 v52, v45
	v_mov_b32_e32 v45, v62
	v_mov_b32_e32 v62, v55
	v_mov_b32_e32 v55, v64
	v_mov_b32_e32 v64, v57
	v_mov_b32_e32 v110, v58
	v_mov_b32_e32 v58, v60
	v_mov_b32_e32 v60, v70
	v_mov_b32_e32 v71, v80
	v_mov_b32_e32 v80, v73
	v_mov_b32_e32 v70, v72
	v_mov_b32_e32 v72, v74
	s_waitcnt lgkmcnt(2)
	v_mov_b32_e32 v73, v82
	v_mov_b32_e32 v82, v75
	v_mov_b32_e32 v74, v76
	v_mov_b32_e32 v75, v84
	v_mov_b32_e32 v84, v77
	s_waitcnt lgkmcnt(1)
	v_mov_b32_e32 v76, v87
	v_mov_b32_e32 v87, v89
	v_mov_b32_e32 v77, v88
	s_waitcnt lgkmcnt(0)
	v_mov_b32_e32 v89, v90
	v_mov_b32_e32 v90, v93
	v_mov_b32_e32 v88, v92
	s_add_i32 s14, s14, 8
	s_add_i32 s15, s15, 32
	s_cmpk_gt_u32 s14, 0x77
	v_lshl_add_u64 v[8:9], v[8:9], 0, s[12:13]
	v_pk_mul_f32 v[46:47], v[94:95], v[46:47] op_sel_hi:[0,1]
	v_pk_mul_f32 v[78:79], v[94:95], v[78:79] op_sel_hi:[0,1]
	v_pk_mul_f32 v[30:31], v[94:95], v[30:31] op_sel_hi:[0,1]
	v_pk_mul_f32 v[62:63], v[94:95], v[62:63] op_sel_hi:[0,1]
	v_pk_fma_f32 v[28:29], v[96:97], v[28:29], v[46:47] op_sel_hi:[0,1,1]
	v_pk_fma_f32 v[46:47], v[96:97], v[60:61], v[78:79] op_sel_hi:[0,1,1]
	v_pk_mul_f32 v[32:33], v[100:101], v[32:33] op_sel_hi:[0,1]
	v_pk_mul_f32 v[48:49], v[100:101], v[48:49] op_sel_hi:[0,1]
	v_pk_mul_f32 v[60:61], v[100:101], v[64:65] op_sel_hi:[0,1]
	v_pk_fma_f32 v[30:31], v[96:97], v[108:109], v[30:31] op_sel_hi:[0,1,1]
	v_pk_fma_f32 v[44:45], v[96:97], v[44:45], v[62:63] op_sel_hi:[0,1,1]
	v_pk_fma_f32 v[22:23], v[98:99], v[22:23], v[32:33] op_sel_hi:[0,1,1]
	v_pk_fma_f32 v[32:33], v[98:99], v[38:39], v[48:49] op_sel_hi:[0,1,1]
	v_pk_fma_f32 v[38:39], v[98:99], v[54:55], v[60:61] op_sel_hi:[0,1,1]
	v_pk_add_f32 v[22:23], v[30:31], v[22:23]
	v_pk_add_f32 v[30:31], v[44:45], v[38:39]
	v_pk_mul_f32 v[62:63], v[100:101], v[80:81] op_sel_hi:[0,1]
	v_mov_b32_e32 v97, v100
	v_pk_add_f32 v[28:29], v[28:29], v[32:33]
	v_pk_mul_f32 v[34:35], v[56:57], v[34:35] op_sel_hi:[0,1]
	v_pk_mul_f32 v[38:39], v[56:57], v[50:51] op_sel_hi:[0,1]
	v_pk_mul_f32 v[44:45], v[56:57], v[66:67] op_sel_hi:[0,1]
	v_pk_fma_f32 v[24:25], v[102:103], v[24:25], v[34:35] op_sel_hi:[0,1,1]
	v_pk_fma_f32 v[34:35], v[102:103], v[40:41], v[38:39] op_sel_hi:[0,1,1]
	v_pk_fma_f32 v[38:39], v[102:103], v[110:111], v[44:45] op_sel_hi:[0,1,1]
	v_mov_b32_e32 v95, v98
	v_pk_mul_f32 v[64:65], v[96:97], v[86:87]
	v_pk_fma_f32 v[48:49], v[98:99], v[70:71], v[62:63] op_sel_hi:[0,1,1]
	v_pk_add_f32 v[22:23], v[22:23], v[24:25]
	v_pk_mul_f32 v[24:25], v[104:105], v[36:37] op_sel_hi:[0,1]
	v_pk_add_f32 v[28:29], v[28:29], v[34:35]
	v_pk_mul_f32 v[34:35], v[104:105], v[52:53] op_sel_hi:[0,1]
	v_pk_add_f32 v[30:31], v[30:31], v[38:39]
	v_pk_mul_f32 v[36:37], v[104:105], v[68:69] op_sel_hi:[0,1]
	v_pk_mul_f32 v[38:39], v[104:105], v[84:85] op_sel_hi:[0,1]
	v_mov_b32_e32 v105, v56
	v_pk_fma_f32 v[54:55], v[94:95], v[76:77], v[64:65]
	v_pk_add_f32 v[32:33], v[46:47], v[48:49]
	v_pk_mul_f32 v[46:47], v[56:57], v[82:83] op_sel_hi:[0,1]
	v_pk_fma_f32 v[24:25], v[106:107], v[26:27], v[24:25] op_sel_hi:[0,1,1]
	v_pk_fma_f32 v[26:27], v[106:107], v[42:43], v[34:35] op_sel_hi:[0,1,1]
	v_pk_fma_f32 v[34:35], v[106:107], v[58:59], v[36:37] op_sel_hi:[0,1,1]
	v_pk_fma_f32 v[36:37], v[106:107], v[74:75], v[38:39] op_sel_hi:[0,1,1]
	v_mov_b32_e32 v107, v102
	v_pk_mul_f32 v[38:39], v[104:105], v[90:91]
	v_pk_fma_f32 v[40:41], v[102:103], v[72:73], v[46:47] op_sel_hi:[0,1,1]
	v_add_f32_e32 v7, v54, v55
	v_pk_add_f32 v[22:23], v[24:25], v[22:23]
	v_pk_add_f32 v[24:25], v[26:27], v[28:29]
	v_pk_add_f32 v[26:27], v[34:35], v[30:31]
	v_pk_fma_f32 v[30:31], v[106:107], v[88:89], v[38:39]
	v_pk_add_f32 v[32:33], v[32:33], v[40:41]
	v_add_f32_e32 v7, v7, v31
	v_pk_add_f32 v[28:29], v[36:37], v[32:33]
	v_add_f32_e32 v7, v30, v7
	v_pk_add_f32 v[10:11], v[10:11], v[22:23]
	v_pk_add_f32 v[12:13], v[12:13], v[24:25]
	v_pk_add_f32 v[14:15], v[14:15], v[26:27]
	v_pk_add_f32 v[16:17], v[16:17], v[28:29]
	v_add_f32_e32 v2, v2, v7
	ds_write2st64_b32 v21, v10, v11 offset1:1
	ds_write2st64_b32 v21, v12, v13 offset0:2 offset1:3
	ds_write2st64_b32 v21, v14, v15 offset0:4 offset1:5
	ds_write2st64_b32 v21, v16, v17 offset0:6 offset1:7
	ds_write_b32 v21, v2 offset:2048
	s_waitcnt lgkmcnt(0)
	s_barrier
	s_and_saveexec_b64 s[14:15], s[0:1]
	s_cbranch_execz .LBB0_10
	v_lshl_or_b32 v8, s45, 6, v252
	v_ashrrev_i32_e32 v9, 31, v8
	v_lshl_add_u64 v[8:9], v[8:9], 2, s[46:47]
	s_mov_b64 s[38:39], 0
	v_mov_b32_e32 v2, v20
	v_mov_b32_e32 v10, v19
	v_mov_b32_e32 v7, v18
